# m8 + 40 converter workgroups in the gate/up GEMM phase (11 GEMM rounds on 216 workgroups), XP5 32, N_DEFER 64
# speedup vs baseline: 1.0156x; 1.0156x over previous
; #define LAS __attribute__((address_space(3)))
; __device__ __forceinline__ void cvt_item_lds(const float* src, int ld_src, fp8_t* dst, int ld_dst, LAS unsigned char* lds, int tid, int wv) {
;     const int lane = tid & 63;
;     const float* s = src + (size_t)(16 * wv) * ld_src + 4 * lane;
;     f32x4 va[16], vb[16];
;     cvt8_load(va, s, ld_src);
; #pragma unroll
;     for (int t = 0; t < 8; t += 2) {
;         cvt8_load(vb, s + (t + 1) * 256, ld_src); __builtin_amdgcn_sched_barrier(0);
; __device__ __forceinline__ void conv_queue(const Params& p, LAS unsigned char* lds, const int wave, const int cw, const int first, const int last, const int slot_off = LDS_MISC) {
;     ...
;     for (;;) {
;         __syncthreads();
;         if (tid == 0) *slot = first + (int)atomicAdd(&p.ctl[cw], 1u);
;         __syncthreads();
;         const int it = *slot;
;         if (it >= last) break;
;         if (it < N_GU) { const int e = it >> 5, rem = it & 31, kb = rem >> 1, nh = rem & 1;
;             const float* src = p.w_gu + (size_t)e * ND * (2 * DFF) + (size_t)(kb * 128) * (2 * DFF) + nh * 2048;
;             fp8_t* dst = p.wt_gu + (size_t)e * (2 * DFF) * ND + (size_t)(nh * 2048) * ND + kb * 128;
;             cvt_item_lds(src, 2 * DFF, dst, ND, lds, tid, wave); }
;         else { const int j = it - N_GU, e = j >> 4, kb = j & 15;
;             const float* src = p.w_down + (size_t)e * DFF * ND + (size_t)(kb * 128) * ND;
;             fp8_t* dst = p.wt_down + (size_t)e * ND * DFF + kb * 128;
;             cvt_item_lds(src, ND, dst, DFF, lds, tid, wave); }
.LBB0_822:
	s_or_b64 exec, exec, s[48:49]
	s_waitcnt lgkmcnt(0)
	s_barrier
	ds_read_b32 v0, v209
	s_movk_i32 s2, 0x41f
	s_mov_b64 s[48:49], -1
	s_waitcnt lgkmcnt(0)
	v_cmp_lt_i32_e32 vcc, s2, v0
	v_readfirstlane_b32 s33, v0
	s_cbranch_vccnz .LBB0_817
	s_cmpk_gt_i32 s33, 0x3ff
	s_cbranch_scc0 .LBB0_825
	s_add_i32 s2, s33, 0xfffffc00
	s_lshr_b32 s4, s2, 4
	v_readlane_b32 s16, v254, 22
	s_lshl_b64 s[34:35], s[4:5], 22
	s_lshl_b64 s[48:49], s[4:5], 24
	v_readlane_b32 s20, v254, 26
	v_readlane_b32 s21, v254, 27
	s_add_u32 s2, s20, s48
	s_addc_u32 s4, s21, s49
	s_lshl_b32 s48, s33, 7
	s_and_b32 s48, s48, 0x780
	s_lshl_b32 s49, s48, 13
	s_add_u32 s2, s2, s49
	s_addc_u32 s4, s4, 0
	s_add_u32 s34, s56, s34
	s_addc_u32 s35, s57, s35
	s_add_u32 s50, s34, s48
	s_addc_u32 s51, s35, 0
	s_add_u32 s48, s2, s14
	s_addc_u32 s49, s4, s15
	v_lshl_add_u64 v[172:173], s[48:49], 0, v[128:129]
	s_movk_i32 s2, 0x2000
	v_add_co_u32_e32 v174, vcc, s2, v172
	s_movk_i32 s2, 0x3000
	s_nop 0
	v_addc_co_u32_e32 v175, vcc, 0, v173, vcc
	v_add_co_u32_e32 v142, vcc, s2, v172
	s_movk_i32 s2, 0x6000
	s_nop 0
	v_addc_co_u32_e32 v143, vcc, 0, v173, vcc
	v_add_co_u32_e32 v176, vcc, s13, v172
	v_readlane_b32 s17, v254, 23
	s_nop 0
	v_addc_co_u32_e32 v177, vcc, 0, v173, vcc
	v_add_co_u32_e32 v144, vcc, s67, v172
	v_readlane_b32 s18, v254, 24
	s_nop 0
	v_addc_co_u32_e32 v145, vcc, 0, v173, vcc
	v_add_co_u32_e32 v178, vcc, s2, v172
	s_movk_i32 s2, 0x7000
	s_nop 0
	v_addc_co_u32_e32 v179, vcc, 0, v173, vcc
	v_add_co_u32_e32 v146, vcc, s2, v172
	s_mov_b32 s2, 0xa000
	s_nop 0
	v_addc_co_u32_e32 v147, vcc, 0, v173, vcc
	v_add_co_u32_e32 v180, vcc, s60, v172
	global_load_dwordx4 v[16:19], v[144:145], off offset:-4096 nt
	global_load_dwordx4 v[20:23], v[146:147], off offset:-4096 nt
	v_addc_co_u32_e32 v181, vcc, 0, v173, vcc
	v_add_co_u32_e32 v148, vcc, s68, v172
	v_readlane_b32 s19, v254, 25
	s_nop 0
	v_addc_co_u32_e32 v149, vcc, 0, v173, vcc
	v_add_co_u32_e32 v182, vcc, s2, v172
	s_mov_b32 s2, 0xb000
	s_nop 0
	v_addc_co_u32_e32 v183, vcc, 0, v173, vcc
	v_add_co_u32_e32 v150, vcc, s2, v172
	s_mov_b32 s2, 0xe000
	s_nop 0
	v_addc_co_u32_e32 v151, vcc, 0, v173, vcc
	v_add_co_u32_e32 v184, vcc, s61, v172
	global_load_dwordx4 v[24:27], v[148:149], off offset:-4096 nt
	global_load_dwordx4 v[28:31], v[150:151], off offset:-4096 nt
	v_addc_co_u32_e32 v185, vcc, 0, v173, vcc
	v_add_co_u32_e32 v152, vcc, s69, v172
	v_readlane_b32 s22, v254, 28
	s_nop 0
	v_addc_co_u32_e32 v153, vcc, 0, v173, vcc
	v_add_co_u32_e32 v186, vcc, s2, v172
	s_mov_b32 s2, 0xf000
	s_nop 0
	v_addc_co_u32_e32 v187, vcc, 0, v173, vcc
	v_add_co_u32_e32 v154, vcc, s2, v172
	s_mov_b32 s2, 0x12000
	s_nop 0
	v_addc_co_u32_e32 v155, vcc, 0, v173, vcc
	v_add_co_u32_e32 v188, vcc, s62, v172
	global_load_dwordx4 v[56:59], v[152:153], off offset:-4096 nt
	global_load_dwordx4 v[60:63], v[154:155], off offset:-4096 nt
	v_addc_co_u32_e32 v189, vcc, 0, v173, vcc
	v_add_co_u32_e32 v156, vcc, s88, v172
	v_readlane_b32 s23, v254, 29
	s_nop 0
	v_addc_co_u32_e32 v157, vcc, 0, v173, vcc
	v_add_co_u32_e32 v190, vcc, s2, v172
	s_mov_b32 s2, 0x13000
	s_nop 0
	v_addc_co_u32_e32 v191, vcc, 0, v173, vcc
	v_add_co_u32_e32 v158, vcc, s2, v172
	s_mov_b32 s2, 0x16000
	s_nop 0
	v_addc_co_u32_e32 v159, vcc, 0, v173, vcc
	v_add_co_u32_e32 v192, vcc, s63, v172
	global_load_dwordx4 v[48:51], v[156:157], off offset:-4096 nt
	global_load_dwordx4 v[52:55], v[158:159], off offset:-4096 nt
	v_addc_co_u32_e32 v193, vcc, 0, v173, vcc
	v_add_co_u32_e32 v160, vcc, s89, v172
	v_readlane_b32 s24, v254, 30
	s_nop 0
	v_addc_co_u32_e32 v161, vcc, 0, v173, vcc
	v_add_co_u32_e32 v194, vcc, s2, v172
	s_mov_b32 s2, 0x17000
	s_nop 0
	v_addc_co_u32_e32 v195, vcc, 0, v173, vcc
	v_add_co_u32_e32 v162, vcc, s2, v172
	s_mov_b32 s2, 0x1a000
	s_nop 0
	v_addc_co_u32_e32 v163, vcc, 0, v173, vcc
	v_add_co_u32_e32 v196, vcc, s64, v172
	global_load_dwordx4 v[80:83], v[160:161], off offset:-4096 nt
	global_load_dwordx4 v[84:87], v[162:163], off offset:-4096 nt
	v_addc_co_u32_e32 v197, vcc, 0, v173, vcc
	v_add_co_u32_e32 v164, vcc, s90, v172
	v_readlane_b32 s25, v254, 31
	s_nop 0
	v_addc_co_u32_e32 v165, vcc, 0, v173, vcc
	v_add_co_u32_e32 v198, vcc, s2, v172
	s_mov_b32 s2, 0x1b000
	s_nop 0
	v_addc_co_u32_e32 v199, vcc, 0, v173, vcc
	v_add_co_u32_e32 v166, vcc, s2, v172
	s_mov_b32 s2, 0x1e000
	s_nop 0
	v_addc_co_u32_e32 v167, vcc, 0, v173, vcc
	v_add_co_u32_e32 v200, vcc, s65, v172
	global_load_dwordx4 v[88:91], v[164:165], off offset:-4096 nt
	global_load_dwordx4 v[92:95], v[166:167], off offset:-4096 nt
	v_addc_co_u32_e32 v201, vcc, 0, v173, vcc
	v_add_co_u32_e32 v168, vcc, s91, v172
	v_readlane_b32 s26, v254, 32
	s_nop 0
	v_addc_co_u32_e32 v169, vcc, 0, v173, vcc
	v_add_co_u32_e32 v202, vcc, s2, v172
	s_mov_b32 s2, 0x1f000
	s_nop 0
	v_addc_co_u32_e32 v203, vcc, 0, v173, vcc
	v_add_co_u32_e32 v170, vcc, s2, v172
	v_readlane_b32 s27, v254, 33
	s_nop 0
	v_addc_co_u32_e32 v171, vcc, 0, v173, vcc
	global_load_dwordx4 v[108:111], v[168:169], off offset:-4096 nt
	global_load_dwordx4 v[112:115], v[170:171], off offset:-4096 nt
	global_load_dwordx4 v[116:119], v[142:143], off offset:-4096 nt
	global_load_dwordx4 v[96:99], v128, s[48:49] offset:1024 nt
	global_load_dwordx4 v[100:103], v[174:175], off offset:1024 nt
	global_load_dwordx4 v[104:107], v[176:177], off offset:1024 nt
	global_load_dwordx4 v[124:127], v[178:179], off offset:1024 nt
	global_load_dwordx4 v[64:67], v[180:181], off offset:1024 nt
	global_load_dwordx4 v[68:71], v[182:183], off offset:1024 nt
	global_load_dwordx4 v[72:75], v[184:185], off offset:1024 nt
	global_load_dwordx4 v[76:79], v[186:187], off offset:1024 nt
	global_load_dwordx4 v[32:35], v[188:189], off offset:1024 nt
	global_load_dwordx4 v[36:39], v[190:191], off offset:1024 nt
	global_load_dwordx4 v[40:43], v[192:193], off offset:1024 nt
	global_load_dwordx4 v[44:47], v[194:195], off offset:1024 nt
	global_load_dwordx4 v[0:3], v[196:197], off offset:1024 nt
	global_load_dwordx4 v[4:7], v[198:199], off offset:1024 nt
	global_load_dwordx4 v[8:11], v[200:201], off offset:1024 nt
	global_load_dwordx4 v[120:123], v128, s[48:49] nt
	global_load_dwordx4 v[12:15], v[202:203], off offset:1024 nt
	v_readlane_b32 s28, v254, 34
	v_readlane_b32 s29, v254, 35
	v_readlane_b32 s30, v254, 36
	v_readlane_b32 s31, v254, 37
	v_lshl_add_u64 v[140:141], s[50:51], 0, v[130:131]
	s_waitcnt vmcnt(1)
; #define LAS __attribute__((address_space(3)))
; __device__ __forceinline__ unsigned pack4_fp8(float a, float b, float c, float d) { int r = 0; r = __builtin_amdgcn_cvt_pk_fp8_f32(a, b, r, false); r = __builtin_amdgcn_cvt_pk_fp8_f32(c, d, r, true); return (unsigned)r; }
; __device__ __forceinline__ void cvt8_to_lds(const f32x4 (&v)[16], LAS unsigned char* tile, int lane, int wv) {
; #pragma unroll
;     for (int i = 0; i < 4; ++i) { u32x4 w; w.x = pack4_fp8(v[0][i] * W8_SCALE, v[1][i] * W8_SCALE, v[2][i] * W8_SCALE, v[3][i] * W8_SCALE); w.y = pack4_fp8(v[4][i] * W8_SCALE, v[5][i] * W8_SCALE, v[6][i] * W8_SCALE, v[7][i] * W8_SCALE);
;         w.z = pack4_fp8(v[8][i] * W8_SCALE, v[9][i] * W8_SCALE, v[10][i] * W8_SCALE, v[11][i] * W8_SCALE); w.w = pack4_fp8(v[12][i] * W8_SCALE, v[13][i] * W8_SCALE, v[14][i] * W8_SCALE, v[15][i] * W8_SCALE);
;         *(LAS u32x4*)(tile + (4 * lane + i) * 128 + ((wv ^ (lane & 7)) << 4)) = w; }
; }
; __device__ __forceinline__ void cvt8_from_lds(const LAS unsigned char* tile, fp8_t* d, int ld_dst, int tid) {
;     const int c = tid & 7;
; #pragma unroll
;     for (int q = 0; q < 4; ++q) { const int r = (tid >> 3) + 64 * q; const u32x4 w = *(const LAS u32x4*)(tile + r * 128 + ((c ^ ((r >> 2) & 7)) << 4));
;         __builtin_nontemporal_store(w, (u32x4*)(d + (size_t)r * ld_dst + 16 * c)); }
	v_mul_f32_e32 v120, 0x42800000, v120
	v_mul_f32_e32 v116, 0x42800000, v116
	v_mov_b32_e32 v210, v129
	v_cvt_pk_fp8_f32 v210, v120, v116
	v_mul_f32_e32 v16, 0x42800000, v16
	v_mul_f32_e32 v20, 0x42800000, v20
	v_mov_b32_e32 v211, v129
	v_cvt_pk_fp8_f32 v210, v16, v20 op_sel:[0,0,1]
	v_mul_f32_e32 v16, 0x42800000, v24
	v_mul_f32_e32 v20, 0x42800000, v28
	v_cvt_pk_fp8_f32 v211, v16, v20
	v_mul_f32_e32 v16, 0x42800000, v48
	v_mul_f32_e32 v20, 0x42800000, v52
	v_mov_b32_e32 v212, v129
	v_cvt_pk_fp8_f32 v212, v16, v20
	v_mul_f32_e32 v16, 0x42800000, v88
	v_mul_f32_e32 v20, 0x42800000, v92
	v_mov_b32_e32 v213, v129
	v_cvt_pk_fp8_f32 v213, v16, v20
	v_mul_f32_e32 v24, 0x42800000, v56
	v_mul_f32_e32 v28, 0x42800000, v60
	v_cvt_pk_fp8_f32 v211, v24, v28 op_sel:[0,0,1]
	v_mul_f32_e32 v24, 0x42800000, v80
	v_mul_f32_e32 v28, 0x42800000, v84
	v_cvt_pk_fp8_f32 v212, v24, v28 op_sel:[0,0,1]
	v_mul_f32_e32 v24, 0x42800000, v108
	v_mul_f32_e32 v28, 0x42800000, v112
	v_cvt_pk_fp8_f32 v213, v24, v28 op_sel:[0,0,1]
	v_mul_f32_e32 v16, 0x42800000, v121
	v_mul_f32_e32 v20, 0x42800000, v117
	v_mul_f32_e32 v17, 0x42800000, v17
	ds_write_b128 v204, v[210:213]
	v_mov_b32_e32 v210, v129
	v_cvt_pk_fp8_f32 v210, v16, v20
	v_mul_f32_e32 v21, 0x42800000, v21
	v_mul_f32_e32 v16, 0x42800000, v25
	v_mov_b32_e32 v211, v129
	v_cvt_pk_fp8_f32 v210, v17, v21 op_sel:[0,0,1]
	v_mul_f32_e32 v17, 0x42800000, v29
	v_cvt_pk_fp8_f32 v211, v16, v17
	v_mul_f32_e32 v16, 0x42800000, v49
	v_mul_f32_e32 v17, 0x42800000, v53
	v_mov_b32_e32 v212, v129
	v_cvt_pk_fp8_f32 v212, v16, v17
	v_mul_f32_e32 v16, 0x42800000, v89
	v_mul_f32_e32 v17, 0x42800000, v93
	v_mov_b32_e32 v213, v129
	v_cvt_pk_fp8_f32 v213, v16, v17
	v_mul_f32_e32 v20, 0x42800000, v57
	v_mul_f32_e32 v21, 0x42800000, v61
	v_cvt_pk_fp8_f32 v211, v20, v21 op_sel:[0,0,1]
	v_mul_f32_e32 v20, 0x42800000, v81
	v_mul_f32_e32 v21, 0x42800000, v85
	v_cvt_pk_fp8_f32 v212, v20, v21 op_sel:[0,0,1]
	v_mul_f32_e32 v20, 0x42800000, v109
	v_mul_f32_e32 v21, 0x42800000, v113
	v_cvt_pk_fp8_f32 v213, v20, v21 op_sel:[0,0,1]
	v_mul_f32_e32 v16, 0x42800000, v122
	v_mul_f32_e32 v17, 0x42800000, v118
	v_mul_f32_e32 v18, 0x42800000, v18
	ds_write_b128 v204, v[210:213] offset:128
	v_mov_b32_e32 v210, v129
	v_cvt_pk_fp8_f32 v210, v16, v17
	v_mul_f32_e32 v16, 0x42800000, v26
	v_mul_f32_e32 v17, 0x42800000, v30
	v_mov_b32_e32 v211, v129
	v_cvt_pk_fp8_f32 v211, v16, v17
	v_mul_f32_e32 v16, 0x42800000, v50
	v_mul_f32_e32 v17, 0x42800000, v54
	v_mov_b32_e32 v212, v129
	v_cvt_pk_fp8_f32 v212, v16, v17
	v_mul_f32_e32 v16, 0x42800000, v90
	v_mul_f32_e32 v17, 0x42800000, v94
	v_mov_b32_e32 v213, v129
	v_mul_f32_e32 v20, 0x42800000, v22
	v_cvt_pk_fp8_f32 v213, v16, v17
	v_cvt_pk_fp8_f32 v210, v18, v20 op_sel:[0,0,1]
	v_mul_f32_e32 v18, 0x42800000, v58
	v_mul_f32_e32 v20, 0x42800000, v62
	v_cvt_pk_fp8_f32 v211, v18, v20 op_sel:[0,0,1]
	v_mul_f32_e32 v18, 0x42800000, v82
	v_mul_f32_e32 v20, 0x42800000, v86
	v_cvt_pk_fp8_f32 v212, v18, v20 op_sel:[0,0,1]
	v_mul_f32_e32 v18, 0x42800000, v110
	v_mul_f32_e32 v20, 0x42800000, v114
	v_cvt_pk_fp8_f32 v213, v18, v20 op_sel:[0,0,1]
	v_mul_f32_e32 v17, 0x42800000, v123
	v_mul_f32_e32 v18, 0x42800000, v119
	v_mov_b32_e32 v16, v129
	v_cvt_pk_fp8_f32 v16, v17, v18
	v_mul_f32_e32 v19, 0x42800000, v19
	v_mul_f32_e32 v20, 0x42800000, v23
	v_mul_f32_e32 v18, 0x42800000, v27
	v_cvt_pk_fp8_f32 v16, v19, v20 op_sel:[0,0,1]
	v_mul_f32_e32 v19, 0x42800000, v31
	v_mov_b32_e32 v17, v129
	v_cvt_pk_fp8_f32 v17, v18, v19
	v_mul_f32_e32 v20, 0x42800000, v59
	v_mul_f32_e32 v21, 0x42800000, v63
	v_mul_f32_e32 v19, 0x42800000, v51
	v_cvt_pk_fp8_f32 v17, v20, v21 op_sel:[0,0,1]
	v_mul_f32_e32 v20, 0x42800000, v55
	v_mov_b32_e32 v18, v129
	v_cvt_pk_fp8_f32 v18, v19, v20
	v_mul_f32_e32 v21, 0x42800000, v83
	v_mul_f32_e32 v22, 0x42800000, v87
	v_mul_f32_e32 v20, 0x42800000, v91
	v_cvt_pk_fp8_f32 v18, v21, v22 op_sel:[0,0,1]
	v_mul_f32_e32 v21, 0x42800000, v95
	v_mov_b32_e32 v19, v129
	v_cvt_pk_fp8_f32 v19, v20, v21
	v_mul_f32_e32 v22, 0x42800000, v111
	v_mul_f32_e32 v23, 0x42800000, v115
	ds_write_b128 v204, v[210:213] offset:256
	v_cvt_pk_fp8_f32 v19, v22, v23 op_sel:[0,0,1]
	ds_write_b128 v204, v[16:19] offset:384
	s_waitcnt lgkmcnt(0)
	s_barrier
	ds_read_b128 v[16:19], v205
	v_lshl_add_u64 v[20:21], v[140:141], 0, v[132:133]
	s_waitcnt lgkmcnt(0)
	global_store_dwordx4 v[20:21], v[16:19], off nt
	ds_read_b128 v[16:19], v206
	v_lshl_add_u64 v[20:21], v[140:141], 0, v[134:135]
	s_waitcnt lgkmcnt(0)
	global_store_dwordx4 v[20:21], v[16:19], off nt
	ds_read_b128 v[16:19], v207
	v_lshl_add_u64 v[20:21], v[140:141], 0, v[136:137]
	s_waitcnt lgkmcnt(0)
	global_store_dwordx4 v[20:21], v[16:19], off nt
	ds_read_b128 v[16:19], v208
	v_lshl_add_u64 v[20:21], v[140:141], 0, v[138:139]
	s_waitcnt lgkmcnt(0)
; #define LAS __attribute__((address_space(3)))
; __device__ __forceinline__ unsigned pack4_fp8(float a, float b, float c, float d) { int r = 0; r = __builtin_amdgcn_cvt_pk_fp8_f32(a, b, r, false); r = __builtin_amdgcn_cvt_pk_fp8_f32(c, d, r, true); return (unsigned)r; }
; #define CVT_LDS_BAR() do { asm volatile("s_waitcnt lgkmcnt(0)" ::: "memory"); __builtin_amdgcn_s_barrier(); asm volatile("" ::: "memory"); } while (0)
; __device__ __forceinline__ void cvt8_to_lds(const f32x4 (&v)[16], LAS unsigned char* tile, int lane, int wv) {
; #pragma unroll
;     for (int i = 0; i < 4; ++i) { u32x4 w; w.x = pack4_fp8(v[0][i] * W8_SCALE, v[1][i] * W8_SCALE, v[2][i] * W8_SCALE, v[3][i] * W8_SCALE); w.y = pack4_fp8(v[4][i] * W8_SCALE, v[5][i] * W8_SCALE, v[6][i] * W8_SCALE, v[7][i] * W8_SCALE);
;         w.z = pack4_fp8(v[8][i] * W8_SCALE, v[9][i] * W8_SCALE, v[10][i] * W8_SCALE, v[11][i] * W8_SCALE); w.w = pack4_fp8(v[12][i] * W8_SCALE, v[13][i] * W8_SCALE, v[14][i] * W8_SCALE, v[15][i] * W8_SCALE);
;         *(LAS u32x4*)(tile + (4 * lane + i) * 128 + ((wv ^ (lane & 7)) << 4)) = w; }
; __device__ __forceinline__ void cvt_item_lds(const float* src, int ld_src, fp8_t* dst, int ld_dst, LAS unsigned char* lds, int tid, int wv) {
;     ...
;         cvt8_load(vb, s + (t + 1) * 256, ld_src); __builtin_amdgcn_sched_barrier(0);
;         cvt8_to_lds(va, lds, lane, wv); CVT_LDS_BAR(); __builtin_amdgcn_sched_barrier(0);
;         cvt8_from_lds(lds, dst + (size_t)(t * 256) * ld_dst, ld_dst, tid); __builtin_amdgcn_sched_barrier(0);
;         if (t + 2 < 8) { cvt8_load(va, s + (t + 2) * 256, ld_src); __builtin_amdgcn_sched_barrier(0); }
;         cvt8_to_lds(vb, lds + 32768, lane, wv); CVT_LDS_BAR(); __builtin_amdgcn_sched_barrier(0);
	global_store_dwordx4 v[20:21], v[16:19], off nt
	global_load_dwordx4 v[108:111], v[174:175], off offset:2048 nt
	global_load_dwordx4 v[112:115], v[176:177], off offset:2048 nt
	global_load_dwordx4 v[116:119], v[178:179], off offset:2048 nt
	global_load_dwordx4 v[80:83], v[180:181], off offset:2048 nt
	global_load_dwordx4 v[84:87], v[182:183], off offset:2048 nt
	global_load_dwordx4 v[88:91], v[184:185], off offset:2048 nt
	global_load_dwordx4 v[92:95], v[186:187], off offset:2048 nt
	global_load_dwordx4 v[48:51], v[188:189], off offset:2048 nt
	global_load_dwordx4 v[52:55], v[190:191], off offset:2048 nt
	global_load_dwordx4 v[56:59], v[192:193], off offset:2048 nt
	global_load_dwordx4 v[60:63], v[194:195], off offset:2048 nt
	global_load_dwordx4 v[16:19], v[196:197], off offset:2048 nt
	global_load_dwordx4 v[20:23], v[198:199], off offset:2048 nt
	global_load_dwordx4 v[24:27], v[200:201], off offset:2048 nt
	global_load_dwordx4 v[120:123], v128, s[48:49] offset:2048 nt
	global_load_dwordx4 v[28:31], v[202:203], off offset:2048 nt
	v_mul_f32_e32 v96, 0x42800000, v96
	v_mul_f32_e32 v100, 0x42800000, v100
	v_mov_b32_e32 v210, v129
	v_mul_f32_e32 v64, 0x42800000, v64
	v_mul_f32_e32 v68, 0x42800000, v68
	v_mov_b32_e32 v211, v129
	v_mul_f32_e32 v32, 0x42800000, v32
	v_mul_f32_e32 v36, 0x42800000, v36
	v_mov_b32_e32 v212, v129
	v_mul_f32_e32 v0, 0x42800000, v0
	v_mul_f32_e32 v4, 0x42800000, v4
	v_mov_b32_e32 v213, v129
	v_cvt_pk_fp8_f32 v210, v96, v100
	v_cvt_pk_fp8_f32 v211, v64, v68
	v_cvt_pk_fp8_f32 v212, v32, v36
	v_cvt_pk_fp8_f32 v213, v0, v4
	v_mul_f32_e32 v104, 0x42800000, v104
	v_mul_f32_e32 v124, 0x42800000, v124
	v_mul_f32_e32 v72, 0x42800000, v72
	v_mul_f32_e32 v76, 0x42800000, v76
	v_mul_f32_e32 v40, 0x42800000, v40
	v_mul_f32_e32 v44, 0x42800000, v44
	v_mul_f32_e32 v8, 0x42800000, v8
	s_waitcnt vmcnt(20)
	v_mul_f32_e32 v12, 0x42800000, v12
	v_cvt_pk_fp8_f32 v210, v104, v124 op_sel:[0,0,1]
	v_cvt_pk_fp8_f32 v211, v72, v76 op_sel:[0,0,1]
	v_cvt_pk_fp8_f32 v212, v40, v44 op_sel:[0,0,1]
	v_cvt_pk_fp8_f32 v213, v8, v12 op_sel:[0,0,1]
	v_mul_f32_e32 v0, 0x42800000, v97
	v_mul_f32_e32 v4, 0x42800000, v101
	v_mul_f32_e32 v8, 0x42800000, v105
	ds_write_b128 v204, v[210:213] offset:32768
	v_mov_b32_e32 v210, v129
	v_cvt_pk_fp8_f32 v210, v0, v4
	v_mul_f32_e32 v0, 0x42800000, v65
	v_mul_f32_e32 v4, 0x42800000, v69
	v_mov_b32_e32 v211, v129
	v_cvt_pk_fp8_f32 v211, v0, v4
	v_mul_f32_e32 v0, 0x42800000, v33
	v_mul_f32_e32 v4, 0x42800000, v37
	v_mov_b32_e32 v212, v129
	v_cvt_pk_fp8_f32 v212, v0, v4
	v_mul_f32_e32 v0, 0x42800000, v1
	v_mul_f32_e32 v1, 0x42800000, v5
	v_mov_b32_e32 v213, v129
	v_cvt_pk_fp8_f32 v213, v0, v1
	v_mul_f32_e32 v12, 0x42800000, v125
	v_cvt_pk_fp8_f32 v210, v8, v12 op_sel:[0,0,1]
	v_mul_f32_e32 v8, 0x42800000, v73
	v_mul_f32_e32 v12, 0x42800000, v77
	v_cvt_pk_fp8_f32 v211, v8, v12 op_sel:[0,0,1]
	v_mul_f32_e32 v8, 0x42800000, v41
	v_mul_f32_e32 v12, 0x42800000, v45
	v_mul_f32_e32 v4, 0x42800000, v9
	v_mul_f32_e32 v5, 0x42800000, v13
	v_cvt_pk_fp8_f32 v212, v8, v12 op_sel:[0,0,1]
	v_cvt_pk_fp8_f32 v213, v4, v5 op_sel:[0,0,1]
	v_mul_f32_e32 v0, 0x42800000, v98
	v_mul_f32_e32 v1, 0x42800000, v102
	v_mul_f32_e32 v4, 0x42800000, v106
	ds_write_b128 v204, v[210:213] offset:32896
	v_mov_b32_e32 v210, v129
	v_cvt_pk_fp8_f32 v210, v0, v1
	v_mul_f32_e32 v0, 0x42800000, v66
	v_mul_f32_e32 v1, 0x42800000, v70
	v_mov_b32_e32 v211, v129
	v_cvt_pk_fp8_f32 v211, v0, v1
	v_mul_f32_e32 v0, 0x42800000, v34
	v_mul_f32_e32 v1, 0x42800000, v38
	v_mov_b32_e32 v212, v129
	v_cvt_pk_fp8_f32 v212, v0, v1
	v_mul_f32_e32 v0, 0x42800000, v2
	v_mul_f32_e32 v1, 0x42800000, v6
	v_mov_b32_e32 v213, v129
	v_mul_f32_e32 v5, 0x42800000, v126
	v_cvt_pk_fp8_f32 v213, v0, v1
	v_cvt_pk_fp8_f32 v210, v4, v5 op_sel:[0,0,1]
	v_mul_f32_e32 v4, 0x42800000, v74
	v_mul_f32_e32 v5, 0x42800000, v78
	v_cvt_pk_fp8_f32 v211, v4, v5 op_sel:[0,0,1]
	v_mul_f32_e32 v4, 0x42800000, v42
	v_mul_f32_e32 v5, 0x42800000, v46
	v_cvt_pk_fp8_f32 v212, v4, v5 op_sel:[0,0,1]
	v_mul_f32_e32 v2, 0x42800000, v10
	v_mul_f32_e32 v4, 0x42800000, v14
	v_cvt_pk_fp8_f32 v213, v2, v4 op_sel:[0,0,1]
	v_mul_f32_e32 v1, 0x42800000, v99
	v_mul_f32_e32 v2, 0x42800000, v103
	v_mov_b32_e32 v0, v129
	v_cvt_pk_fp8_f32 v0, v1, v2
	v_mul_f32_e32 v4, 0x42800000, v107
	v_mul_f32_e32 v5, 0x42800000, v127
	v_mul_f32_e32 v2, 0x42800000, v67
	v_cvt_pk_fp8_f32 v0, v4, v5 op_sel:[0,0,1]
	v_mul_f32_e32 v4, 0x42800000, v71
	v_mov_b32_e32 v1, v129
	v_cvt_pk_fp8_f32 v1, v2, v4
	v_mul_f32_e32 v5, 0x42800000, v75
	v_mul_f32_e32 v6, 0x42800000, v79
	v_mul_f32_e32 v4, 0x42800000, v35
	v_cvt_pk_fp8_f32 v1, v5, v6 op_sel:[0,0,1]
	v_mul_f32_e32 v5, 0x42800000, v39
	v_mov_b32_e32 v2, v129
	v_cvt_pk_fp8_f32 v2, v4, v5
	v_mul_f32_e32 v4, 0x42800000, v3
	v_mul_f32_e32 v5, 0x42800000, v7
	v_mov_b32_e32 v3, v129
	v_cvt_pk_fp8_f32 v3, v4, v5
	v_mul_f32_e32 v6, 0x42800000, v43
	v_mul_f32_e32 v8, 0x42800000, v47
	v_cvt_pk_fp8_f32 v2, v6, v8 op_sel:[0,0,1]
	v_mul_f32_e32 v6, 0x42800000, v11
	v_mul_f32_e32 v7, 0x42800000, v15
	v_cvt_pk_fp8_f32 v3, v6, v7 op_sel:[0,0,1]
	ds_write_b128 v204, v[210:213] offset:33024
	ds_write_b128 v204, v[0:3] offset:33152
	s_waitcnt lgkmcnt(0)
	s_barrier
; #define LAS __attribute__((address_space(3)))
; #define CVT_LDS_BAR() do { asm volatile("s_waitcnt lgkmcnt(0)" ::: "memory"); __builtin_amdgcn_s_barrier(); asm volatile("" ::: "memory"); } while (0)
; __device__ __forceinline__ void cvt8_from_lds(const LAS unsigned char* tile, fp8_t* d, int ld_dst, int tid) {
;     const int c = tid & 7;
; #pragma unroll
;     for (int q = 0; q < 4; ++q) { const int r = (tid >> 3) + 64 * q; const u32x4 w = *(const LAS u32x4*)(tile + r * 128 + ((c ^ ((r >> 2) & 7)) << 4));
;         __builtin_nontemporal_store(w, (u32x4*)(d + (size_t)r * ld_dst + 16 * c)); }
; __device__ __forceinline__ void cvt_item_lds(const float* src, int ld_src, fp8_t* dst, int ld_dst, LAS unsigned char* lds, int tid, int wv) {
;     ...
;     for (int t = 0; t < 8; t += 2) {
;         cvt8_load(vb, s + (t + 1) * 256, ld_src); __builtin_amdgcn_sched_barrier(0);
;         cvt8_to_lds(va, lds, lane, wv); CVT_LDS_BAR(); __builtin_amdgcn_sched_barrier(0);
;         cvt8_from_lds(lds, dst + (size_t)(t * 256) * ld_dst, ld_dst, tid); __builtin_amdgcn_sched_barrier(0);
;         if (t + 2 < 8) { cvt8_load(va, s + (t + 2) * 256, ld_src); __builtin_amdgcn_sched_barrier(0); }
	ds_read_b128 v[0:3], v205 offset:32768
	v_lshl_add_u64 v[4:5], v[140:141], 0, s[8:9]
	v_lshl_add_u64 v[6:7], v[4:5], 0, v[132:133]
	s_waitcnt lgkmcnt(0)
	global_store_dwordx4 v[6:7], v[0:3], off nt
	ds_read_b128 v[0:3], v206 offset:32768
	v_lshl_add_u64 v[6:7], v[4:5], 0, v[134:135]
	s_waitcnt lgkmcnt(0)
	global_store_dwordx4 v[6:7], v[0:3], off nt
	ds_read_b128 v[0:3], v207 offset:32768
	v_lshl_add_u64 v[6:7], v[4:5], 0, v[136:137]
	v_lshl_add_u64 v[4:5], v[4:5], 0, v[138:139]
	s_waitcnt lgkmcnt(0)
	global_store_dwordx4 v[6:7], v[0:3], off nt
	ds_read_b128 v[0:3], v208 offset:32768
	s_waitcnt lgkmcnt(0)
	global_store_dwordx4 v[4:5], v[0:3], off nt
	global_load_dwordx4 v[96:99], v[174:175], off offset:3072 nt
	global_load_dwordx4 v[100:103], v[176:177], off offset:3072 nt
	global_load_dwordx4 v[104:107], v[178:179], off offset:3072 nt
	global_load_dwordx4 v[64:67], v[180:181], off offset:3072 nt
	global_load_dwordx4 v[68:71], v[182:183], off offset:3072 nt
	global_load_dwordx4 v[72:75], v[184:185], off offset:3072 nt
	global_load_dwordx4 v[76:79], v[186:187], off offset:3072 nt
	global_load_dwordx4 v[32:35], v[188:189], off offset:3072 nt
	global_load_dwordx4 v[36:39], v[190:191], off offset:3072 nt
	global_load_dwordx4 v[40:43], v[192:193], off offset:3072 nt
	global_load_dwordx4 v[44:47], v[194:195], off offset:3072 nt
	global_load_dwordx4 v[0:3], v[196:197], off offset:3072 nt
	global_load_dwordx4 v[4:7], v[198:199], off offset:3072 nt
	global_load_dwordx4 v[8:11], v[200:201], off offset:3072 nt
	global_load_dwordx4 v[124:127], v128, s[48:49] offset:3072 nt
	global_load_dwordx4 v[12:15], v[202:203], off offset:3072 nt
	s_waitcnt vmcnt(21)
	v_mul_f32_e32 v120, 0x42800000, v120
	v_mul_f32_e32 v108, 0x42800000, v108
	v_mov_b32_e32 v174, v129
	v_mul_f32_e32 v80, 0x42800000, v80
	v_mul_f32_e32 v84, 0x42800000, v84
	v_mov_b32_e32 v175, v129
	v_mul_f32_e32 v48, 0x42800000, v48
	v_mul_f32_e32 v52, 0x42800000, v52
	v_mov_b32_e32 v176, v129
	v_mul_f32_e32 v16, 0x42800000, v16
	v_mul_f32_e32 v20, 0x42800000, v20
	v_mov_b32_e32 v177, v129
	v_cvt_pk_fp8_f32 v174, v120, v108
	v_cvt_pk_fp8_f32 v175, v80, v84
	v_cvt_pk_fp8_f32 v176, v48, v52
	v_cvt_pk_fp8_f32 v177, v16, v20
	v_mul_f32_e32 v112, 0x42800000, v112
	v_mul_f32_e32 v116, 0x42800000, v116
	v_mul_f32_e32 v88, 0x42800000, v88
	v_mul_f32_e32 v92, 0x42800000, v92
	v_mul_f32_e32 v56, 0x42800000, v56
	v_mul_f32_e32 v60, 0x42800000, v60
	v_mul_f32_e32 v24, 0x42800000, v24
	s_waitcnt vmcnt(20)
	v_mul_f32_e32 v28, 0x42800000, v28
	v_cvt_pk_fp8_f32 v174, v112, v116 op_sel:[0,0,1]
	v_cvt_pk_fp8_f32 v175, v88, v92 op_sel:[0,0,1]
	v_cvt_pk_fp8_f32 v176, v56, v60 op_sel:[0,0,1]
	v_cvt_pk_fp8_f32 v177, v24, v28 op_sel:[0,0,1]
	v_mul_f32_e32 v16, 0x42800000, v121
	v_mul_f32_e32 v20, 0x42800000, v109
	v_mul_f32_e32 v24, 0x42800000, v113
	ds_write_b128 v204, v[174:177]
	v_mov_b32_e32 v174, v129
	v_cvt_pk_fp8_f32 v174, v16, v20
	v_mul_f32_e32 v16, 0x42800000, v81
	v_mul_f32_e32 v20, 0x42800000, v85
	v_mov_b32_e32 v175, v129
	v_cvt_pk_fp8_f32 v175, v16, v20
	v_mul_f32_e32 v16, 0x42800000, v49
	v_mul_f32_e32 v20, 0x42800000, v53
	v_mov_b32_e32 v176, v129
	v_cvt_pk_fp8_f32 v176, v16, v20
	v_mul_f32_e32 v16, 0x42800000, v17
	v_mul_f32_e32 v17, 0x42800000, v21
	v_mov_b32_e32 v177, v129
	v_cvt_pk_fp8_f32 v177, v16, v17
	v_mul_f32_e32 v28, 0x42800000, v117
	v_cvt_pk_fp8_f32 v174, v24, v28 op_sel:[0,0,1]
	v_mul_f32_e32 v24, 0x42800000, v89
	v_mul_f32_e32 v28, 0x42800000, v93
	v_cvt_pk_fp8_f32 v175, v24, v28 op_sel:[0,0,1]
	v_mul_f32_e32 v24, 0x42800000, v57
	v_mul_f32_e32 v28, 0x42800000, v61
	v_mul_f32_e32 v20, 0x42800000, v25
	v_mul_f32_e32 v21, 0x42800000, v29
	v_cvt_pk_fp8_f32 v176, v24, v28 op_sel:[0,0,1]
	v_cvt_pk_fp8_f32 v177, v20, v21 op_sel:[0,0,1]
	v_mul_f32_e32 v16, 0x42800000, v122
	v_mul_f32_e32 v17, 0x42800000, v110
	v_mul_f32_e32 v20, 0x42800000, v114
	ds_write_b128 v204, v[174:177] offset:128
	v_mov_b32_e32 v174, v129
	v_cvt_pk_fp8_f32 v174, v16, v17
	v_mul_f32_e32 v16, 0x42800000, v82
	v_mul_f32_e32 v17, 0x42800000, v86
	v_mov_b32_e32 v175, v129
	v_cvt_pk_fp8_f32 v175, v16, v17
	v_mul_f32_e32 v16, 0x42800000, v50
	v_mul_f32_e32 v17, 0x42800000, v54
	v_mov_b32_e32 v176, v129
	v_cvt_pk_fp8_f32 v176, v16, v17
	v_mul_f32_e32 v16, 0x42800000, v18
	v_mul_f32_e32 v17, 0x42800000, v22
	v_mov_b32_e32 v177, v129
	v_mul_f32_e32 v21, 0x42800000, v118
	v_cvt_pk_fp8_f32 v177, v16, v17
	v_cvt_pk_fp8_f32 v174, v20, v21 op_sel:[0,0,1]
	v_mul_f32_e32 v20, 0x42800000, v90
	v_mul_f32_e32 v21, 0x42800000, v94
	v_cvt_pk_fp8_f32 v175, v20, v21 op_sel:[0,0,1]
	v_mul_f32_e32 v20, 0x42800000, v58
	v_mul_f32_e32 v21, 0x42800000, v62
	v_cvt_pk_fp8_f32 v176, v20, v21 op_sel:[0,0,1]
	v_mul_f32_e32 v18, 0x42800000, v26
	v_mul_f32_e32 v20, 0x42800000, v30
	v_cvt_pk_fp8_f32 v177, v18, v20 op_sel:[0,0,1]
	v_mul_f32_e32 v17, 0x42800000, v123
	v_mul_f32_e32 v18, 0x42800000, v111
	v_mov_b32_e32 v16, v129
	v_cvt_pk_fp8_f32 v16, v17, v18
	v_mul_f32_e32 v20, 0x42800000, v115
	v_mul_f32_e32 v21, 0x42800000, v119
	v_mul_f32_e32 v18, 0x42800000, v83
	v_cvt_pk_fp8_f32 v16, v20, v21 op_sel:[0,0,1]
	v_mul_f32_e32 v20, 0x42800000, v87
	v_mov_b32_e32 v17, v129
	v_cvt_pk_fp8_f32 v17, v18, v20
	v_mul_f32_e32 v21, 0x42800000, v91
	v_mul_f32_e32 v22, 0x42800000, v95
	v_mul_f32_e32 v20, 0x42800000, v51
	v_cvt_pk_fp8_f32 v17, v21, v22 op_sel:[0,0,1]
	v_mul_f32_e32 v21, 0x42800000, v55
	v_mov_b32_e32 v18, v129
	v_cvt_pk_fp8_f32 v18, v20, v21
	v_mul_f32_e32 v20, 0x42800000, v19
	v_mul_f32_e32 v21, 0x42800000, v23
	v_mov_b32_e32 v19, v129
	v_cvt_pk_fp8_f32 v19, v20, v21
	v_mul_f32_e32 v22, 0x42800000, v59
	v_mul_f32_e32 v24, 0x42800000, v63
	v_cvt_pk_fp8_f32 v18, v22, v24 op_sel:[0,0,1]
	v_mul_f32_e32 v22, 0x42800000, v27
	v_mul_f32_e32 v23, 0x42800000, v31
	v_cvt_pk_fp8_f32 v19, v22, v23 op_sel:[0,0,1]
	ds_write_b128 v204, v[174:177] offset:256
	ds_write_b128 v204, v[16:19] offset:384
	s_waitcnt lgkmcnt(0)
	s_barrier
; #define LAS __attribute__((address_space(3)))
; #define CVT_LDS_BAR() do { asm volatile("s_waitcnt lgkmcnt(0)" ::: "memory"); __builtin_amdgcn_s_barrier(); asm volatile("" ::: "memory"); } while (0)
; __device__ __forceinline__ void cvt8_from_lds(const LAS unsigned char* tile, fp8_t* d, int ld_dst, int tid) {
;     const int c = tid & 7;
; #pragma unroll
;     for (int q = 0; q < 4; ++q) { const int r = (tid >> 3) + 64 * q; const u32x4 w = *(const LAS u32x4*)(tile + r * 128 + ((c ^ ((r >> 2) & 7)) << 4));
;         __builtin_nontemporal_store(w, (u32x4*)(d + (size_t)r * ld_dst + 16 * c)); }
; __device__ __forceinline__ void cvt_item_lds(const float* src, int ld_src, fp8_t* dst, int ld_dst, LAS unsigned char* lds, int tid, int wv) {
;     ...
;     for (int t = 0; t < 8; t += 2) {
;         cvt8_load(vb, s + (t + 1) * 256, ld_src); __builtin_amdgcn_sched_barrier(0);
;         cvt8_to_lds(va, lds, lane, wv); CVT_LDS_BAR(); __builtin_amdgcn_sched_barrier(0);
;         cvt8_from_lds(lds, dst + (size_t)(t * 256) * ld_dst, ld_dst, tid); __builtin_amdgcn_sched_barrier(0);
;         if (t + 2 < 8) { cvt8_load(va, s + (t + 2) * 256, ld_src); __builtin_amdgcn_sched_barrier(0); }
;         cvt8_to_lds(vb, lds + 32768, lane, wv); CVT_LDS_BAR(); __builtin_amdgcn_sched_barrier(0);
	ds_read_b128 v[16:19], v205
	v_lshl_add_u64 v[20:21], v[140:141], 0, s[10:11]
	v_lshl_add_u64 v[22:23], v[20:21], 0, v[132:133]
	s_waitcnt lgkmcnt(0)
	global_store_dwordx4 v[22:23], v[16:19], off nt
	ds_read_b128 v[16:19], v206
	v_lshl_add_u64 v[22:23], v[20:21], 0, v[134:135]
	s_waitcnt lgkmcnt(0)
	global_store_dwordx4 v[22:23], v[16:19], off nt
	ds_read_b128 v[16:19], v207
	v_lshl_add_u64 v[22:23], v[20:21], 0, v[136:137]
	v_lshl_add_u64 v[20:21], v[20:21], 0, v[138:139]
	s_waitcnt lgkmcnt(0)
	global_store_dwordx4 v[22:23], v[16:19], off nt
	ds_read_b128 v[16:19], v208
	s_waitcnt lgkmcnt(0)
	global_store_dwordx4 v[20:21], v[16:19], off nt
	v_add_co_u32_e32 v172, vcc, s66, v172
	s_nop 1
	v_addc_co_u32_e32 v173, vcc, 0, v173, vcc
	global_load_dwordx4 v[108:111], v[172:173], off nt
	global_load_dwordx4 v[112:115], v[142:143], off nt
	global_load_dwordx4 v[116:119], v[144:145], off nt
	global_load_dwordx4 v[120:123], v[146:147], off nt
	global_load_dwordx4 v[80:83], v[148:149], off nt
	global_load_dwordx4 v[84:87], v[150:151], off nt
	global_load_dwordx4 v[88:91], v[152:153], off nt
	global_load_dwordx4 v[92:95], v[154:155], off nt
	global_load_dwordx4 v[48:51], v[156:157], off nt
	global_load_dwordx4 v[52:55], v[158:159], off nt
	global_load_dwordx4 v[56:59], v[160:161], off nt
	global_load_dwordx4 v[60:63], v[162:163], off nt
	global_load_dwordx4 v[16:19], v[164:165], off nt
	global_load_dwordx4 v[20:23], v[166:167], off nt
	global_load_dwordx4 v[24:27], v[168:169], off nt
	global_load_dwordx4 v[28:31], v[170:171], off nt
	s_waitcnt vmcnt(21)
	v_mul_f32_e32 v124, 0x42800000, v124
	v_mul_f32_e32 v96, 0x42800000, v96
	v_mov_b32_e32 v174, v129
	v_mul_f32_e32 v64, 0x42800000, v64
	v_mul_f32_e32 v68, 0x42800000, v68
	v_mov_b32_e32 v175, v129
	v_mul_f32_e32 v32, 0x42800000, v32
	v_mul_f32_e32 v36, 0x42800000, v36
	v_mov_b32_e32 v176, v129
	v_mul_f32_e32 v0, 0x42800000, v0
	v_mul_f32_e32 v4, 0x42800000, v4
	v_mov_b32_e32 v177, v129
	v_cvt_pk_fp8_f32 v174, v124, v96
	v_cvt_pk_fp8_f32 v175, v64, v68
	v_cvt_pk_fp8_f32 v176, v32, v36
	v_cvt_pk_fp8_f32 v177, v0, v4
	v_mul_f32_e32 v100, 0x42800000, v100
	v_mul_f32_e32 v104, 0x42800000, v104
	v_mul_f32_e32 v72, 0x42800000, v72
	v_mul_f32_e32 v76, 0x42800000, v76
	v_mul_f32_e32 v40, 0x42800000, v40
	v_mul_f32_e32 v44, 0x42800000, v44
	v_mul_f32_e32 v8, 0x42800000, v8
	s_waitcnt vmcnt(20)
	v_mul_f32_e32 v12, 0x42800000, v12
	v_cvt_pk_fp8_f32 v174, v100, v104 op_sel:[0,0,1]
	v_cvt_pk_fp8_f32 v175, v72, v76 op_sel:[0,0,1]
	v_cvt_pk_fp8_f32 v176, v40, v44 op_sel:[0,0,1]
	v_cvt_pk_fp8_f32 v177, v8, v12 op_sel:[0,0,1]
	v_mul_f32_e32 v0, 0x42800000, v125
	v_mul_f32_e32 v4, 0x42800000, v97
	v_mul_f32_e32 v8, 0x42800000, v101
	ds_write_b128 v204, v[174:177] offset:32768
	v_mov_b32_e32 v174, v129
	v_cvt_pk_fp8_f32 v174, v0, v4
	v_mul_f32_e32 v0, 0x42800000, v65
	v_mul_f32_e32 v4, 0x42800000, v69
	v_mov_b32_e32 v175, v129
	v_cvt_pk_fp8_f32 v175, v0, v4
	v_mul_f32_e32 v0, 0x42800000, v33
	v_mul_f32_e32 v4, 0x42800000, v37
	v_mov_b32_e32 v176, v129
	v_cvt_pk_fp8_f32 v176, v0, v4
	v_mul_f32_e32 v0, 0x42800000, v1
	v_mul_f32_e32 v1, 0x42800000, v5
	v_mov_b32_e32 v177, v129
	v_cvt_pk_fp8_f32 v177, v0, v1
	v_mul_f32_e32 v12, 0x42800000, v105
	v_cvt_pk_fp8_f32 v174, v8, v12 op_sel:[0,0,1]
	v_mul_f32_e32 v8, 0x42800000, v73
	v_mul_f32_e32 v12, 0x42800000, v77
	v_cvt_pk_fp8_f32 v175, v8, v12 op_sel:[0,0,1]
	v_mul_f32_e32 v8, 0x42800000, v41
	v_mul_f32_e32 v12, 0x42800000, v45
	v_mul_f32_e32 v4, 0x42800000, v9
	v_mul_f32_e32 v5, 0x42800000, v13
	v_cvt_pk_fp8_f32 v176, v8, v12 op_sel:[0,0,1]
	v_cvt_pk_fp8_f32 v177, v4, v5 op_sel:[0,0,1]
	v_mul_f32_e32 v0, 0x42800000, v126
	v_mul_f32_e32 v1, 0x42800000, v98
	v_mul_f32_e32 v4, 0x42800000, v102
	ds_write_b128 v204, v[174:177] offset:32896
	v_mov_b32_e32 v174, v129
	v_cvt_pk_fp8_f32 v174, v0, v1
	v_mul_f32_e32 v0, 0x42800000, v66
	v_mul_f32_e32 v1, 0x42800000, v70
	v_mov_b32_e32 v175, v129
	v_cvt_pk_fp8_f32 v175, v0, v1
	v_mul_f32_e32 v0, 0x42800000, v34
	v_mul_f32_e32 v1, 0x42800000, v38
	v_mov_b32_e32 v176, v129
	v_cvt_pk_fp8_f32 v176, v0, v1
	v_mul_f32_e32 v0, 0x42800000, v2
	v_mul_f32_e32 v1, 0x42800000, v6
	v_mov_b32_e32 v177, v129
	v_mul_f32_e32 v5, 0x42800000, v106
	v_cvt_pk_fp8_f32 v177, v0, v1
	v_cvt_pk_fp8_f32 v174, v4, v5 op_sel:[0,0,1]
	v_mul_f32_e32 v4, 0x42800000, v74
	v_mul_f32_e32 v5, 0x42800000, v78
	v_cvt_pk_fp8_f32 v175, v4, v5 op_sel:[0,0,1]
	v_mul_f32_e32 v4, 0x42800000, v42
	v_mul_f32_e32 v5, 0x42800000, v46
	v_cvt_pk_fp8_f32 v176, v4, v5 op_sel:[0,0,1]
	v_mul_f32_e32 v2, 0x42800000, v10
	v_mul_f32_e32 v4, 0x42800000, v14
	v_cvt_pk_fp8_f32 v177, v2, v4 op_sel:[0,0,1]
	v_mul_f32_e32 v1, 0x42800000, v127
	v_mul_f32_e32 v2, 0x42800000, v99
	v_mov_b32_e32 v0, v129
	v_cvt_pk_fp8_f32 v0, v1, v2
	v_mul_f32_e32 v4, 0x42800000, v103
	v_mul_f32_e32 v5, 0x42800000, v107
	v_mul_f32_e32 v2, 0x42800000, v67
	v_cvt_pk_fp8_f32 v0, v4, v5 op_sel:[0,0,1]
	v_mul_f32_e32 v4, 0x42800000, v71
	v_mov_b32_e32 v1, v129
	v_cvt_pk_fp8_f32 v1, v2, v4
	v_mul_f32_e32 v5, 0x42800000, v75
	v_mul_f32_e32 v6, 0x42800000, v79
	v_mul_f32_e32 v4, 0x42800000, v35
	v_cvt_pk_fp8_f32 v1, v5, v6 op_sel:[0,0,1]
	v_mul_f32_e32 v5, 0x42800000, v39
	v_mov_b32_e32 v2, v129
	v_cvt_pk_fp8_f32 v2, v4, v5
	v_mul_f32_e32 v4, 0x42800000, v3
	v_mul_f32_e32 v5, 0x42800000, v7
	v_mov_b32_e32 v3, v129
	v_cvt_pk_fp8_f32 v3, v4, v5
	v_mul_f32_e32 v6, 0x42800000, v43
	v_mul_f32_e32 v8, 0x42800000, v47
	v_cvt_pk_fp8_f32 v2, v6, v8 op_sel:[0,0,1]
	v_mul_f32_e32 v6, 0x42800000, v11
	v_mul_f32_e32 v7, 0x42800000, v15
	v_cvt_pk_fp8_f32 v3, v6, v7 op_sel:[0,0,1]
	ds_write_b128 v204, v[174:177] offset:33024
	ds_write_b128 v204, v[0:3] offset:33152
	s_waitcnt lgkmcnt(0)
	s_barrier
; #define LAS __attribute__((address_space(3)))
; #define CVT_LDS_BAR() do { asm volatile("s_waitcnt lgkmcnt(0)" ::: "memory"); __builtin_amdgcn_s_barrier(); asm volatile("" ::: "memory"); } while (0)
; __device__ __forceinline__ void cvt8_from_lds(const LAS unsigned char* tile, fp8_t* d, int ld_dst, int tid) {
;     const int c = tid & 7;
; #pragma unroll
;     for (int q = 0; q < 4; ++q) { const int r = (tid >> 3) + 64 * q; const u32x4 w = *(const LAS u32x4*)(tile + r * 128 + ((c ^ ((r >> 2) & 7)) << 4));
;         __builtin_nontemporal_store(w, (u32x4*)(d + (size_t)r * ld_dst + 16 * c)); }
; __device__ __forceinline__ void cvt_item_lds(const float* src, int ld_src, fp8_t* dst, int ld_dst, LAS unsigned char* lds, int tid, int wv) {
;     ...
;     for (int t = 0; t < 8; t += 2) {
;         cvt8_load(vb, s + (t + 1) * 256, ld_src); __builtin_amdgcn_sched_barrier(0);
;         cvt8_to_lds(va, lds, lane, wv); CVT_LDS_BAR(); __builtin_amdgcn_sched_barrier(0);
;         cvt8_from_lds(lds, dst + (size_t)(t * 256) * ld_dst, ld_dst, tid); __builtin_amdgcn_sched_barrier(0);
;         if (t + 2 < 8) { cvt8_load(va, s + (t + 2) * 256, ld_src); __builtin_amdgcn_sched_barrier(0); }
;         cvt8_to_lds(vb, lds + 32768, lane, wv); CVT_LDS_BAR(); __builtin_amdgcn_sched_barrier(0);
	ds_read_b128 v[0:3], v205 offset:32768
	v_lshl_add_u64 v[4:5], v[140:141], 0, s[38:39]
	v_lshl_add_u64 v[6:7], v[4:5], 0, v[132:133]
	s_waitcnt lgkmcnt(0)
	global_store_dwordx4 v[6:7], v[0:3], off nt
	ds_read_b128 v[0:3], v206 offset:32768
	v_lshl_add_u64 v[6:7], v[4:5], 0, v[134:135]
	s_waitcnt lgkmcnt(0)
	global_store_dwordx4 v[6:7], v[0:3], off nt
	ds_read_b128 v[0:3], v207 offset:32768
	v_lshl_add_u64 v[6:7], v[4:5], 0, v[136:137]
	v_lshl_add_u64 v[4:5], v[4:5], 0, v[138:139]
	s_waitcnt lgkmcnt(0)
	global_store_dwordx4 v[6:7], v[0:3], off nt
	ds_read_b128 v[0:3], v208 offset:32768
	s_waitcnt lgkmcnt(0)
	global_store_dwordx4 v[4:5], v[0:3], off nt
	global_load_dwordx4 v[96:99], v[172:173], off offset:1024 nt
	global_load_dwordx4 v[100:103], v[142:143], off offset:1024 nt
	global_load_dwordx4 v[104:107], v[144:145], off offset:1024 nt
	global_load_dwordx4 v[124:127], v[146:147], off offset:1024 nt
	global_load_dwordx4 v[64:67], v[148:149], off offset:1024 nt
	global_load_dwordx4 v[68:71], v[150:151], off offset:1024 nt
	global_load_dwordx4 v[72:75], v[152:153], off offset:1024 nt
	global_load_dwordx4 v[76:79], v[154:155], off offset:1024 nt
	global_load_dwordx4 v[32:35], v[156:157], off offset:1024 nt
	global_load_dwordx4 v[36:39], v[158:159], off offset:1024 nt
	global_load_dwordx4 v[40:43], v[160:161], off offset:1024 nt
	global_load_dwordx4 v[44:47], v[162:163], off offset:1024 nt
	global_load_dwordx4 v[0:3], v[164:165], off offset:1024 nt
	global_load_dwordx4 v[4:7], v[166:167], off offset:1024 nt
	global_load_dwordx4 v[8:11], v[168:169], off offset:1024 nt
	global_load_dwordx4 v[12:15], v[170:171], off offset:1024 nt
	s_waitcnt vmcnt(35)
	v_mul_f32_e32 v108, 0x42800000, v108
	s_waitcnt vmcnt(34)
	v_mul_f32_e32 v112, 0x42800000, v112
	v_mov_b32_e32 v174, v129
	s_waitcnt vmcnt(31)
	v_mul_f32_e32 v80, 0x42800000, v80
	s_waitcnt vmcnt(30)
	v_mul_f32_e32 v84, 0x42800000, v84
	v_mov_b32_e32 v175, v129
	s_waitcnt vmcnt(27)
	v_mul_f32_e32 v48, 0x42800000, v48
	s_waitcnt vmcnt(26)
	v_mul_f32_e32 v52, 0x42800000, v52
	v_mov_b32_e32 v176, v129
	s_waitcnt vmcnt(23)
	v_mul_f32_e32 v16, 0x42800000, v16
	s_waitcnt vmcnt(22)
	v_mul_f32_e32 v20, 0x42800000, v20
	v_mov_b32_e32 v177, v129
	v_cvt_pk_fp8_f32 v174, v108, v112
	v_cvt_pk_fp8_f32 v175, v80, v84
	v_cvt_pk_fp8_f32 v176, v48, v52
	v_cvt_pk_fp8_f32 v177, v16, v20
	v_mul_f32_e32 v116, 0x42800000, v116
	v_mul_f32_e32 v120, 0x42800000, v120
	v_mul_f32_e32 v88, 0x42800000, v88
	v_mul_f32_e32 v92, 0x42800000, v92
	v_mul_f32_e32 v56, 0x42800000, v56
	v_mul_f32_e32 v60, 0x42800000, v60
	s_waitcnt vmcnt(21)
	v_mul_f32_e32 v24, 0x42800000, v24
	s_waitcnt vmcnt(20)
	v_mul_f32_e32 v28, 0x42800000, v28
	v_cvt_pk_fp8_f32 v174, v116, v120 op_sel:[0,0,1]
	v_cvt_pk_fp8_f32 v175, v88, v92 op_sel:[0,0,1]
	v_cvt_pk_fp8_f32 v176, v56, v60 op_sel:[0,0,1]
	v_cvt_pk_fp8_f32 v177, v24, v28 op_sel:[0,0,1]
	v_mul_f32_e32 v16, 0x42800000, v109
	v_mul_f32_e32 v20, 0x42800000, v113
	v_mul_f32_e32 v24, 0x42800000, v117
	ds_write_b128 v204, v[174:177]
	v_mov_b32_e32 v174, v129
	v_cvt_pk_fp8_f32 v174, v16, v20
	v_mul_f32_e32 v16, 0x42800000, v81
	v_mul_f32_e32 v20, 0x42800000, v85
	v_mov_b32_e32 v175, v129
	v_cvt_pk_fp8_f32 v175, v16, v20
	v_mul_f32_e32 v16, 0x42800000, v49
	v_mul_f32_e32 v20, 0x42800000, v53
	v_mov_b32_e32 v176, v129
	v_cvt_pk_fp8_f32 v176, v16, v20
	v_mul_f32_e32 v16, 0x42800000, v17
	v_mul_f32_e32 v17, 0x42800000, v21
	v_mov_b32_e32 v177, v129
	v_cvt_pk_fp8_f32 v177, v16, v17
	v_mul_f32_e32 v28, 0x42800000, v121
	v_cvt_pk_fp8_f32 v174, v24, v28 op_sel:[0,0,1]
	v_mul_f32_e32 v24, 0x42800000, v89
	v_mul_f32_e32 v28, 0x42800000, v93
	v_cvt_pk_fp8_f32 v175, v24, v28 op_sel:[0,0,1]
	v_mul_f32_e32 v24, 0x42800000, v57
	v_mul_f32_e32 v28, 0x42800000, v61
	v_mul_f32_e32 v20, 0x42800000, v25
	v_mul_f32_e32 v21, 0x42800000, v29
	v_cvt_pk_fp8_f32 v176, v24, v28 op_sel:[0,0,1]
	v_cvt_pk_fp8_f32 v177, v20, v21 op_sel:[0,0,1]
	v_mul_f32_e32 v16, 0x42800000, v110
	v_mul_f32_e32 v17, 0x42800000, v114
	v_mul_f32_e32 v20, 0x42800000, v118
	ds_write_b128 v204, v[174:177] offset:128
	v_mov_b32_e32 v174, v129
	v_cvt_pk_fp8_f32 v174, v16, v17
	v_mul_f32_e32 v16, 0x42800000, v82
	v_mul_f32_e32 v17, 0x42800000, v86
	v_mov_b32_e32 v175, v129
	v_cvt_pk_fp8_f32 v175, v16, v17
	v_mul_f32_e32 v16, 0x42800000, v50
	v_mul_f32_e32 v17, 0x42800000, v54
	v_mov_b32_e32 v176, v129
	v_cvt_pk_fp8_f32 v176, v16, v17
	v_mul_f32_e32 v16, 0x42800000, v18
	v_mul_f32_e32 v17, 0x42800000, v22
	v_mov_b32_e32 v177, v129
	v_mul_f32_e32 v21, 0x42800000, v122
	v_cvt_pk_fp8_f32 v177, v16, v17
	v_cvt_pk_fp8_f32 v174, v20, v21 op_sel:[0,0,1]
	v_mul_f32_e32 v20, 0x42800000, v90
	v_mul_f32_e32 v21, 0x42800000, v94
	v_cvt_pk_fp8_f32 v175, v20, v21 op_sel:[0,0,1]
	v_mul_f32_e32 v20, 0x42800000, v58
	v_mul_f32_e32 v21, 0x42800000, v62
	v_cvt_pk_fp8_f32 v176, v20, v21 op_sel:[0,0,1]
	v_mul_f32_e32 v18, 0x42800000, v26
	v_mul_f32_e32 v20, 0x42800000, v30
	v_cvt_pk_fp8_f32 v177, v18, v20 op_sel:[0,0,1]
	v_mul_f32_e32 v17, 0x42800000, v111
	v_mul_f32_e32 v18, 0x42800000, v115
	v_mov_b32_e32 v16, v129
	v_cvt_pk_fp8_f32 v16, v17, v18
	v_mul_f32_e32 v20, 0x42800000, v119
	v_mul_f32_e32 v21, 0x42800000, v123
	v_mul_f32_e32 v18, 0x42800000, v83
	v_cvt_pk_fp8_f32 v16, v20, v21 op_sel:[0,0,1]
	v_mul_f32_e32 v20, 0x42800000, v87
	v_mov_b32_e32 v17, v129
	v_cvt_pk_fp8_f32 v17, v18, v20
	v_mul_f32_e32 v21, 0x42800000, v91
	v_mul_f32_e32 v22, 0x42800000, v95
	v_mul_f32_e32 v20, 0x42800000, v51
	v_cvt_pk_fp8_f32 v17, v21, v22 op_sel:[0,0,1]
	v_mul_f32_e32 v21, 0x42800000, v55
	v_mov_b32_e32 v18, v129
	v_cvt_pk_fp8_f32 v18, v20, v21
	v_mul_f32_e32 v20, 0x42800000, v19
	v_mul_f32_e32 v21, 0x42800000, v23
	v_mov_b32_e32 v19, v129
	v_cvt_pk_fp8_f32 v19, v20, v21
	v_mul_f32_e32 v22, 0x42800000, v59
	v_mul_f32_e32 v24, 0x42800000, v63
	v_cvt_pk_fp8_f32 v18, v22, v24 op_sel:[0,0,1]
	v_mul_f32_e32 v22, 0x42800000, v27
	v_mul_f32_e32 v23, 0x42800000, v31
	v_cvt_pk_fp8_f32 v19, v22, v23 op_sel:[0,0,1]
	ds_write_b128 v204, v[174:177] offset:256
	ds_write_b128 v204, v[16:19] offset:384
	s_waitcnt lgkmcnt(0)
	s_barrier
; #define LAS __attribute__((address_space(3)))
; #define CVT_LDS_BAR() do { asm volatile("s_waitcnt lgkmcnt(0)" ::: "memory"); __builtin_amdgcn_s_barrier(); asm volatile("" ::: "memory"); } while (0)
; __device__ __forceinline__ void cvt8_from_lds(const LAS unsigned char* tile, fp8_t* d, int ld_dst, int tid) {
;     const int c = tid & 7;
; #pragma unroll
;     for (int q = 0; q < 4; ++q) { const int r = (tid >> 3) + 64 * q; const u32x4 w = *(const LAS u32x4*)(tile + r * 128 + ((c ^ ((r >> 2) & 7)) << 4));
;         __builtin_nontemporal_store(w, (u32x4*)(d + (size_t)r * ld_dst + 16 * c)); }
; __device__ __forceinline__ void cvt_item_lds(const float* src, int ld_src, fp8_t* dst, int ld_dst, LAS unsigned char* lds, int tid, int wv) {
;     ...
;     for (int t = 0; t < 8; t += 2) {
;         cvt8_load(vb, s + (t + 1) * 256, ld_src); __builtin_amdgcn_sched_barrier(0);
;         cvt8_to_lds(va, lds, lane, wv); CVT_LDS_BAR(); __builtin_amdgcn_sched_barrier(0);
;         cvt8_from_lds(lds, dst + (size_t)(t * 256) * ld_dst, ld_dst, tid); __builtin_amdgcn_sched_barrier(0);
;         if (t + 2 < 8) { cvt8_load(va, s + (t + 2) * 256, ld_src); __builtin_amdgcn_sched_barrier(0); }
;         cvt8_to_lds(vb, lds + 32768, lane, wv); CVT_LDS_BAR(); __builtin_amdgcn_sched_barrier(0);
	ds_read_b128 v[16:19], v205
	v_lshl_add_u64 v[20:21], v[140:141], 0, s[40:41]
	v_lshl_add_u64 v[22:23], v[20:21], 0, v[132:133]
	s_waitcnt lgkmcnt(0)
	global_store_dwordx4 v[22:23], v[16:19], off nt
	ds_read_b128 v[16:19], v206
	v_lshl_add_u64 v[22:23], v[20:21], 0, v[134:135]
	s_waitcnt lgkmcnt(0)
	global_store_dwordx4 v[22:23], v[16:19], off nt
	ds_read_b128 v[16:19], v207
	v_lshl_add_u64 v[22:23], v[20:21], 0, v[136:137]
	v_lshl_add_u64 v[20:21], v[20:21], 0, v[138:139]
	s_waitcnt lgkmcnt(0)
	global_store_dwordx4 v[22:23], v[16:19], off nt
	ds_read_b128 v[16:19], v208
	s_waitcnt lgkmcnt(0)
	global_store_dwordx4 v[20:21], v[16:19], off nt
	global_load_dwordx4 v[108:111], v[172:173], off offset:2048 nt
	global_load_dwordx4 v[112:115], v[142:143], off offset:2048 nt
	global_load_dwordx4 v[116:119], v[144:145], off offset:2048 nt
	global_load_dwordx4 v[120:123], v[146:147], off offset:2048 nt
	global_load_dwordx4 v[80:83], v[148:149], off offset:2048 nt
	global_load_dwordx4 v[84:87], v[150:151], off offset:2048 nt
	global_load_dwordx4 v[88:91], v[152:153], off offset:2048 nt
	global_load_dwordx4 v[92:95], v[154:155], off offset:2048 nt
	global_load_dwordx4 v[48:51], v[156:157], off offset:2048 nt
	global_load_dwordx4 v[52:55], v[158:159], off offset:2048 nt
	global_load_dwordx4 v[56:59], v[160:161], off offset:2048 nt
	global_load_dwordx4 v[60:63], v[162:163], off offset:2048 nt
	global_load_dwordx4 v[16:19], v[164:165], off offset:2048 nt
	global_load_dwordx4 v[20:23], v[166:167], off offset:2048 nt
	global_load_dwordx4 v[24:27], v[168:169], off offset:2048 nt
	global_load_dwordx4 v[28:31], v[170:171], off offset:2048 nt
	s_waitcnt vmcnt(35)
	v_mul_f32_e32 v96, 0x42800000, v96
	s_waitcnt vmcnt(34)
	v_mul_f32_e32 v100, 0x42800000, v100
	v_mov_b32_e32 v174, v129
	s_waitcnt vmcnt(31)
	v_mul_f32_e32 v64, 0x42800000, v64
	s_waitcnt vmcnt(30)
	v_mul_f32_e32 v68, 0x42800000, v68
	v_mov_b32_e32 v175, v129
	s_waitcnt vmcnt(27)
	v_mul_f32_e32 v32, 0x42800000, v32
	s_waitcnt vmcnt(26)
	v_mul_f32_e32 v36, 0x42800000, v36
	v_mov_b32_e32 v176, v129
	s_waitcnt vmcnt(23)
	v_mul_f32_e32 v0, 0x42800000, v0
	s_waitcnt vmcnt(22)
	v_mul_f32_e32 v4, 0x42800000, v4
	v_mov_b32_e32 v177, v129
	v_cvt_pk_fp8_f32 v174, v96, v100
	v_cvt_pk_fp8_f32 v175, v64, v68
	v_cvt_pk_fp8_f32 v176, v32, v36
	v_cvt_pk_fp8_f32 v177, v0, v4
	v_mul_f32_e32 v104, 0x42800000, v104
	v_mul_f32_e32 v124, 0x42800000, v124
	v_mul_f32_e32 v72, 0x42800000, v72
	v_mul_f32_e32 v76, 0x42800000, v76
	v_mul_f32_e32 v40, 0x42800000, v40
	v_mul_f32_e32 v44, 0x42800000, v44
	s_waitcnt vmcnt(21)
	v_mul_f32_e32 v8, 0x42800000, v8
	s_waitcnt vmcnt(20)
	v_mul_f32_e32 v12, 0x42800000, v12
	v_cvt_pk_fp8_f32 v174, v104, v124 op_sel:[0,0,1]
	v_cvt_pk_fp8_f32 v175, v72, v76 op_sel:[0,0,1]
	v_cvt_pk_fp8_f32 v176, v40, v44 op_sel:[0,0,1]
	v_cvt_pk_fp8_f32 v177, v8, v12 op_sel:[0,0,1]
	v_mul_f32_e32 v0, 0x42800000, v97
	v_mul_f32_e32 v4, 0x42800000, v101
	v_mul_f32_e32 v8, 0x42800000, v105
	ds_write_b128 v204, v[174:177] offset:32768
	v_mov_b32_e32 v174, v129
	v_cvt_pk_fp8_f32 v174, v0, v4
	v_mul_f32_e32 v0, 0x42800000, v65
	v_mul_f32_e32 v4, 0x42800000, v69
	v_mov_b32_e32 v175, v129
	v_cvt_pk_fp8_f32 v175, v0, v4
	v_mul_f32_e32 v0, 0x42800000, v33
	v_mul_f32_e32 v4, 0x42800000, v37
	v_mov_b32_e32 v176, v129
	v_cvt_pk_fp8_f32 v176, v0, v4
	v_mul_f32_e32 v0, 0x42800000, v1
	v_mul_f32_e32 v1, 0x42800000, v5
	v_mov_b32_e32 v177, v129
	v_cvt_pk_fp8_f32 v177, v0, v1
	v_mul_f32_e32 v12, 0x42800000, v125
	v_cvt_pk_fp8_f32 v174, v8, v12 op_sel:[0,0,1]
	v_mul_f32_e32 v8, 0x42800000, v73
	v_mul_f32_e32 v12, 0x42800000, v77
	v_cvt_pk_fp8_f32 v175, v8, v12 op_sel:[0,0,1]
	v_mul_f32_e32 v8, 0x42800000, v41
	v_mul_f32_e32 v12, 0x42800000, v45
	v_mul_f32_e32 v4, 0x42800000, v9
	v_mul_f32_e32 v5, 0x42800000, v13
	v_cvt_pk_fp8_f32 v176, v8, v12 op_sel:[0,0,1]
	v_cvt_pk_fp8_f32 v177, v4, v5 op_sel:[0,0,1]
	v_mul_f32_e32 v0, 0x42800000, v98
	v_mul_f32_e32 v1, 0x42800000, v102
	v_mul_f32_e32 v4, 0x42800000, v106
	ds_write_b128 v204, v[174:177] offset:32896
	v_mov_b32_e32 v174, v129
	v_cvt_pk_fp8_f32 v174, v0, v1
	v_mul_f32_e32 v0, 0x42800000, v66
	v_mul_f32_e32 v1, 0x42800000, v70
	v_mov_b32_e32 v175, v129
	v_cvt_pk_fp8_f32 v175, v0, v1
	v_mul_f32_e32 v0, 0x42800000, v34
	v_mul_f32_e32 v1, 0x42800000, v38
	v_mov_b32_e32 v176, v129
	v_cvt_pk_fp8_f32 v176, v0, v1
	v_mul_f32_e32 v0, 0x42800000, v2
	v_mul_f32_e32 v1, 0x42800000, v6
	v_mov_b32_e32 v177, v129
	v_mul_f32_e32 v5, 0x42800000, v126
	v_cvt_pk_fp8_f32 v177, v0, v1
	v_cvt_pk_fp8_f32 v174, v4, v5 op_sel:[0,0,1]
	v_mul_f32_e32 v4, 0x42800000, v74
	v_mul_f32_e32 v5, 0x42800000, v78
	v_cvt_pk_fp8_f32 v175, v4, v5 op_sel:[0,0,1]
	v_mul_f32_e32 v4, 0x42800000, v42
	v_mul_f32_e32 v5, 0x42800000, v46
	v_cvt_pk_fp8_f32 v176, v4, v5 op_sel:[0,0,1]
	v_mul_f32_e32 v2, 0x42800000, v10
	v_mul_f32_e32 v4, 0x42800000, v14
	v_cvt_pk_fp8_f32 v177, v2, v4 op_sel:[0,0,1]
	v_mul_f32_e32 v1, 0x42800000, v99
	v_mul_f32_e32 v2, 0x42800000, v103
	v_mov_b32_e32 v0, v129
	v_cvt_pk_fp8_f32 v0, v1, v2
	v_mul_f32_e32 v4, 0x42800000, v107
	v_mul_f32_e32 v5, 0x42800000, v127
	v_mul_f32_e32 v2, 0x42800000, v67
	v_cvt_pk_fp8_f32 v0, v4, v5 op_sel:[0,0,1]
	v_mul_f32_e32 v4, 0x42800000, v71
	v_mov_b32_e32 v1, v129
	v_cvt_pk_fp8_f32 v1, v2, v4
	v_mul_f32_e32 v5, 0x42800000, v75
	v_mul_f32_e32 v6, 0x42800000, v79
	v_mul_f32_e32 v4, 0x42800000, v35
	v_cvt_pk_fp8_f32 v1, v5, v6 op_sel:[0,0,1]
	v_mul_f32_e32 v5, 0x42800000, v39
	v_mov_b32_e32 v2, v129
	v_cvt_pk_fp8_f32 v2, v4, v5
	v_mul_f32_e32 v4, 0x42800000, v3
	v_mul_f32_e32 v5, 0x42800000, v7
	v_mov_b32_e32 v3, v129
	v_cvt_pk_fp8_f32 v3, v4, v5
	v_mul_f32_e32 v6, 0x42800000, v43
	v_mul_f32_e32 v8, 0x42800000, v47
	v_cvt_pk_fp8_f32 v2, v6, v8 op_sel:[0,0,1]
	v_mul_f32_e32 v6, 0x42800000, v11
	v_mul_f32_e32 v7, 0x42800000, v15
	v_cvt_pk_fp8_f32 v3, v6, v7 op_sel:[0,0,1]
	ds_write_b128 v204, v[174:177] offset:33024
	ds_write_b128 v204, v[0:3] offset:33152
	s_waitcnt lgkmcnt(0)
	s_barrier
; #define LAS __attribute__((address_space(3)))
; #define CVT_LDS_BAR() do { asm volatile("s_waitcnt lgkmcnt(0)" ::: "memory"); __builtin_amdgcn_s_barrier(); asm volatile("" ::: "memory"); } while (0)
; __device__ __forceinline__ void cvt8_from_lds(const LAS unsigned char* tile, fp8_t* d, int ld_dst, int tid) {
;     const int c = tid & 7;
; #pragma unroll
;     for (int q = 0; q < 4; ++q) { const int r = (tid >> 3) + 64 * q; const u32x4 w = *(const LAS u32x4*)(tile + r * 128 + ((c ^ ((r >> 2) & 7)) << 4));
;         __builtin_nontemporal_store(w, (u32x4*)(d + (size_t)r * ld_dst + 16 * c)); }
; __device__ __forceinline__ void cvt_item_lds(const float* src, int ld_src, fp8_t* dst, int ld_dst, LAS unsigned char* lds, int tid, int wv) {
;     ...
;     for (int t = 0; t < 8; t += 2) {
;         cvt8_load(vb, s + (t + 1) * 256, ld_src); __builtin_amdgcn_sched_barrier(0);
;         cvt8_to_lds(va, lds, lane, wv); CVT_LDS_BAR(); __builtin_amdgcn_sched_barrier(0);
;         cvt8_from_lds(lds, dst + (size_t)(t * 256) * ld_dst, ld_dst, tid); __builtin_amdgcn_sched_barrier(0);
;         if (t + 2 < 8) { cvt8_load(va, s + (t + 2) * 256, ld_src); __builtin_amdgcn_sched_barrier(0); }
;         cvt8_to_lds(vb, lds + 32768, lane, wv); CVT_LDS_BAR(); __builtin_amdgcn_sched_barrier(0);
	ds_read_b128 v[0:3], v205 offset:32768
	v_lshl_add_u64 v[4:5], v[140:141], 0, s[42:43]
	v_lshl_add_u64 v[6:7], v[4:5], 0, v[132:133]
	s_waitcnt lgkmcnt(0)
	global_store_dwordx4 v[6:7], v[0:3], off nt
	ds_read_b128 v[0:3], v206 offset:32768
	v_lshl_add_u64 v[6:7], v[4:5], 0, v[134:135]
	s_waitcnt lgkmcnt(0)
	global_store_dwordx4 v[6:7], v[0:3], off nt
	ds_read_b128 v[0:3], v207 offset:32768
	v_lshl_add_u64 v[6:7], v[4:5], 0, v[136:137]
	v_lshl_add_u64 v[4:5], v[4:5], 0, v[138:139]
	s_waitcnt lgkmcnt(0)
	global_store_dwordx4 v[6:7], v[0:3], off nt
	ds_read_b128 v[0:3], v208 offset:32768
	s_waitcnt lgkmcnt(0)
	global_store_dwordx4 v[4:5], v[0:3], off nt
	global_load_dwordx4 v[96:99], v[172:173], off offset:3072 nt
	global_load_dwordx4 v[100:103], v[142:143], off offset:3072 nt
	global_load_dwordx4 v[104:107], v[144:145], off offset:3072 nt
	global_load_dwordx4 v[124:127], v[146:147], off offset:3072 nt
	global_load_dwordx4 v[64:67], v[148:149], off offset:3072 nt
	global_load_dwordx4 v[68:71], v[150:151], off offset:3072 nt
	global_load_dwordx4 v[72:75], v[152:153], off offset:3072 nt
	global_load_dwordx4 v[76:79], v[154:155], off offset:3072 nt
	global_load_dwordx4 v[32:35], v[156:157], off offset:3072 nt
	global_load_dwordx4 v[36:39], v[158:159], off offset:3072 nt
	global_load_dwordx4 v[40:43], v[160:161], off offset:3072 nt
	global_load_dwordx4 v[44:47], v[162:163], off offset:3072 nt
	global_load_dwordx4 v[0:3], v[164:165], off offset:3072 nt
	global_load_dwordx4 v[4:7], v[166:167], off offset:3072 nt
	global_load_dwordx4 v[8:11], v[168:169], off offset:3072 nt
	global_load_dwordx4 v[12:15], v[170:171], off offset:3072 nt
	s_waitcnt vmcnt(35)
	v_mul_f32_e32 v108, 0x42800000, v108
	s_waitcnt vmcnt(34)
	v_mul_f32_e32 v112, 0x42800000, v112
	v_mov_b32_e32 v142, v129
	s_waitcnt vmcnt(31)
	v_mul_f32_e32 v80, 0x42800000, v80
	s_waitcnt vmcnt(30)
	v_mul_f32_e32 v84, 0x42800000, v84
	v_mov_b32_e32 v143, v129
	s_waitcnt vmcnt(27)
	v_mul_f32_e32 v48, 0x42800000, v48
	s_waitcnt vmcnt(26)
	v_mul_f32_e32 v52, 0x42800000, v52
	v_mov_b32_e32 v144, v129
	s_waitcnt vmcnt(23)
	v_mul_f32_e32 v16, 0x42800000, v16
	s_waitcnt vmcnt(22)
	v_mul_f32_e32 v20, 0x42800000, v20
	v_mov_b32_e32 v145, v129
	v_cvt_pk_fp8_f32 v142, v108, v112
	v_cvt_pk_fp8_f32 v143, v80, v84
	v_cvt_pk_fp8_f32 v144, v48, v52
	v_cvt_pk_fp8_f32 v145, v16, v20
	v_mul_f32_e32 v116, 0x42800000, v116
	v_mul_f32_e32 v120, 0x42800000, v120
	v_mul_f32_e32 v88, 0x42800000, v88
	v_mul_f32_e32 v92, 0x42800000, v92
	v_mul_f32_e32 v56, 0x42800000, v56
	v_mul_f32_e32 v60, 0x42800000, v60
	s_waitcnt vmcnt(21)
	v_mul_f32_e32 v24, 0x42800000, v24
	s_waitcnt vmcnt(20)
	v_mul_f32_e32 v28, 0x42800000, v28
	v_cvt_pk_fp8_f32 v142, v116, v120 op_sel:[0,0,1]
	v_cvt_pk_fp8_f32 v143, v88, v92 op_sel:[0,0,1]
	v_cvt_pk_fp8_f32 v144, v56, v60 op_sel:[0,0,1]
	v_cvt_pk_fp8_f32 v145, v24, v28 op_sel:[0,0,1]
	v_mul_f32_e32 v16, 0x42800000, v109
	v_mul_f32_e32 v20, 0x42800000, v113
	v_mul_f32_e32 v24, 0x42800000, v117
	ds_write_b128 v204, v[142:145]
	v_mov_b32_e32 v142, v129
	v_cvt_pk_fp8_f32 v142, v16, v20
	v_mul_f32_e32 v16, 0x42800000, v81
	v_mul_f32_e32 v20, 0x42800000, v85
	v_mov_b32_e32 v143, v129
	v_cvt_pk_fp8_f32 v143, v16, v20
	v_mul_f32_e32 v16, 0x42800000, v49
	v_mul_f32_e32 v20, 0x42800000, v53
	v_mov_b32_e32 v144, v129
	v_cvt_pk_fp8_f32 v144, v16, v20
	v_mul_f32_e32 v16, 0x42800000, v17
	v_mul_f32_e32 v17, 0x42800000, v21
	v_mov_b32_e32 v145, v129
	v_cvt_pk_fp8_f32 v145, v16, v17
	v_mul_f32_e32 v28, 0x42800000, v121
	v_cvt_pk_fp8_f32 v142, v24, v28 op_sel:[0,0,1]
	v_mul_f32_e32 v24, 0x42800000, v89
	v_mul_f32_e32 v28, 0x42800000, v93
	v_cvt_pk_fp8_f32 v143, v24, v28 op_sel:[0,0,1]
	v_mul_f32_e32 v24, 0x42800000, v57
	v_mul_f32_e32 v28, 0x42800000, v61
	v_mul_f32_e32 v20, 0x42800000, v25
	v_mul_f32_e32 v21, 0x42800000, v29
	v_cvt_pk_fp8_f32 v144, v24, v28 op_sel:[0,0,1]
	v_cvt_pk_fp8_f32 v145, v20, v21 op_sel:[0,0,1]
	v_mul_f32_e32 v16, 0x42800000, v110
	v_mul_f32_e32 v17, 0x42800000, v114
	v_mul_f32_e32 v20, 0x42800000, v118
	ds_write_b128 v204, v[142:145] offset:128
	v_mov_b32_e32 v142, v129
	v_cvt_pk_fp8_f32 v142, v16, v17
	v_mul_f32_e32 v16, 0x42800000, v82
	v_mul_f32_e32 v17, 0x42800000, v86
	v_mov_b32_e32 v143, v129
	v_cvt_pk_fp8_f32 v143, v16, v17
	v_mul_f32_e32 v16, 0x42800000, v50
	v_mul_f32_e32 v17, 0x42800000, v54
	v_mov_b32_e32 v144, v129
	v_cvt_pk_fp8_f32 v144, v16, v17
	v_mul_f32_e32 v16, 0x42800000, v18
	v_mul_f32_e32 v17, 0x42800000, v22
	v_mov_b32_e32 v145, v129
	v_mul_f32_e32 v21, 0x42800000, v122
	v_cvt_pk_fp8_f32 v145, v16, v17
	v_cvt_pk_fp8_f32 v142, v20, v21 op_sel:[0,0,1]
	v_mul_f32_e32 v20, 0x42800000, v90
	v_mul_f32_e32 v21, 0x42800000, v94
	v_cvt_pk_fp8_f32 v143, v20, v21 op_sel:[0,0,1]
	v_mul_f32_e32 v20, 0x42800000, v58
	v_mul_f32_e32 v21, 0x42800000, v62
	v_cvt_pk_fp8_f32 v144, v20, v21 op_sel:[0,0,1]
	v_mul_f32_e32 v18, 0x42800000, v26
	v_mul_f32_e32 v20, 0x42800000, v30
	v_cvt_pk_fp8_f32 v145, v18, v20 op_sel:[0,0,1]
	v_mul_f32_e32 v17, 0x42800000, v111
	v_mul_f32_e32 v18, 0x42800000, v115
	v_mov_b32_e32 v16, v129
	v_cvt_pk_fp8_f32 v16, v17, v18
	v_mul_f32_e32 v20, 0x42800000, v119
	v_mul_f32_e32 v21, 0x42800000, v123
	v_mul_f32_e32 v18, 0x42800000, v83
	v_cvt_pk_fp8_f32 v16, v20, v21 op_sel:[0,0,1]
	v_mul_f32_e32 v20, 0x42800000, v87
	v_mov_b32_e32 v17, v129
	v_cvt_pk_fp8_f32 v17, v18, v20
	v_mul_f32_e32 v21, 0x42800000, v91
	v_mul_f32_e32 v22, 0x42800000, v95
	v_mul_f32_e32 v20, 0x42800000, v51
	v_cvt_pk_fp8_f32 v17, v21, v22 op_sel:[0,0,1]
	v_mul_f32_e32 v21, 0x42800000, v55
	v_mov_b32_e32 v18, v129
	v_cvt_pk_fp8_f32 v18, v20, v21
	v_mul_f32_e32 v20, 0x42800000, v19
	v_mul_f32_e32 v21, 0x42800000, v23
	v_mov_b32_e32 v19, v129
	v_cvt_pk_fp8_f32 v19, v20, v21
	v_mul_f32_e32 v22, 0x42800000, v59
	v_mul_f32_e32 v24, 0x42800000, v63
	v_cvt_pk_fp8_f32 v18, v22, v24 op_sel:[0,0,1]
	v_mul_f32_e32 v22, 0x42800000, v27
	v_mul_f32_e32 v23, 0x42800000, v31
	v_cvt_pk_fp8_f32 v19, v22, v23 op_sel:[0,0,1]
	ds_write_b128 v204, v[142:145] offset:256
	ds_write_b128 v204, v[16:19] offset:384
	s_waitcnt lgkmcnt(0)
	s_barrier
; #define LAS __attribute__((address_space(3)))
; __device__ __forceinline__ unsigned pack4_fp8(float a, float b, float c, float d) { int r = 0; r = __builtin_amdgcn_cvt_pk_fp8_f32(a, b, r, false); r = __builtin_amdgcn_cvt_pk_fp8_f32(c, d, r, true); return (unsigned)r; }
; #define CVT_LDS_BAR() do { asm volatile("s_waitcnt lgkmcnt(0)" ::: "memory"); __builtin_amdgcn_s_barrier(); asm volatile("" ::: "memory"); } while (0)
; __device__ __forceinline__ void cvt8_to_lds(const f32x4 (&v)[16], LAS unsigned char* tile, int lane, int wv) {
; #pragma unroll
;     for (int i = 0; i < 4; ++i) { u32x4 w; w.x = pack4_fp8(v[0][i] * W8_SCALE, v[1][i] * W8_SCALE, v[2][i] * W8_SCALE, v[3][i] * W8_SCALE); w.y = pack4_fp8(v[4][i] * W8_SCALE, v[5][i] * W8_SCALE, v[6][i] * W8_SCALE, v[7][i] * W8_SCALE);
;         w.z = pack4_fp8(v[8][i] * W8_SCALE, v[9][i] * W8_SCALE, v[10][i] * W8_SCALE, v[11][i] * W8_SCALE); w.w = pack4_fp8(v[12][i] * W8_SCALE, v[13][i] * W8_SCALE, v[14][i] * W8_SCALE, v[15][i] * W8_SCALE);
;         *(LAS u32x4*)(tile + (4 * lane + i) * 128 + ((wv ^ (lane & 7)) << 4)) = w; }
; }
; __device__ __forceinline__ void cvt8_from_lds(const LAS unsigned char* tile, fp8_t* d, int ld_dst, int tid) {
;     const int c = tid & 7;
; #pragma unroll
;     for (int q = 0; q < 4; ++q) { const int r = (tid >> 3) + 64 * q; const u32x4 w = *(const LAS u32x4*)(tile + r * 128 + ((c ^ ((r >> 2) & 7)) << 4));
;         __builtin_nontemporal_store(w, (u32x4*)(d + (size_t)r * ld_dst + 16 * c)); }
; __device__ __forceinline__ void cvt_item_lds(const float* src, int ld_src, fp8_t* dst, int ld_dst, LAS unsigned char* lds, int tid, int wv) {
;     ...
;         cvt8_to_lds(vb, lds + 32768, lane, wv); CVT_LDS_BAR(); __builtin_amdgcn_sched_barrier(0);
;         cvt8_from_lds(lds + 32768, dst + (size_t)((t + 1) * 256) * ld_dst, ld_dst, tid); __builtin_amdgcn_sched_barrier(0);
	ds_read_b128 v[16:19], v205
	v_lshl_add_u64 v[20:21], v[140:141], 0, s[44:45]
	v_lshl_add_u64 v[22:23], v[20:21], 0, v[132:133]
	s_waitcnt lgkmcnt(0)
	global_store_dwordx4 v[22:23], v[16:19], off nt
	ds_read_b128 v[16:19], v206
	v_lshl_add_u64 v[22:23], v[20:21], 0, v[134:135]
	s_waitcnt lgkmcnt(0)
	global_store_dwordx4 v[22:23], v[16:19], off nt
	ds_read_b128 v[16:19], v207
	v_lshl_add_u64 v[22:23], v[20:21], 0, v[136:137]
	v_lshl_add_u64 v[20:21], v[20:21], 0, v[138:139]
	s_waitcnt lgkmcnt(0)
	global_store_dwordx4 v[22:23], v[16:19], off nt
	ds_read_b128 v[16:19], v208
	s_waitcnt lgkmcnt(0)
	global_store_dwordx4 v[20:21], v[16:19], off nt
	s_waitcnt vmcnt(19)
	s_nop 0
	v_mul_f32_e32 v17, 0x42800000, v96
	s_waitcnt vmcnt(18)
	v_mul_f32_e32 v18, 0x42800000, v100
	v_mov_b32_e32 v16, v129
	v_cvt_pk_fp8_f32 v16, v17, v18
	s_waitcnt vmcnt(17)
	v_mul_f32_e32 v19, 0x42800000, v104
	s_waitcnt vmcnt(16)
	v_mul_f32_e32 v20, 0x42800000, v124
	s_waitcnt vmcnt(15)
	v_mul_f32_e32 v18, 0x42800000, v64
	v_cvt_pk_fp8_f32 v16, v19, v20 op_sel:[0,0,1]
	s_waitcnt vmcnt(14)
	v_mul_f32_e32 v19, 0x42800000, v68
	v_mov_b32_e32 v17, v129
	v_cvt_pk_fp8_f32 v17, v18, v19
	s_waitcnt vmcnt(13)
	v_mul_f32_e32 v20, 0x42800000, v72
	s_waitcnt vmcnt(12)
	v_mul_f32_e32 v21, 0x42800000, v76
	s_waitcnt vmcnt(11)
	v_mul_f32_e32 v19, 0x42800000, v32
	v_cvt_pk_fp8_f32 v17, v20, v21 op_sel:[0,0,1]
	s_waitcnt vmcnt(10)
	v_mul_f32_e32 v20, 0x42800000, v36
	v_mov_b32_e32 v18, v129
	v_cvt_pk_fp8_f32 v18, v19, v20
	s_waitcnt vmcnt(7)
	v_mul_f32_e32 v0, 0x42800000, v0
	s_waitcnt vmcnt(6)
	v_mul_f32_e32 v4, 0x42800000, v4
	v_mov_b32_e32 v19, v129
	v_cvt_pk_fp8_f32 v19, v0, v4
	v_mul_f32_e32 v21, 0x42800000, v40
	v_mul_f32_e32 v22, 0x42800000, v44
	s_waitcnt vmcnt(5)
	v_mul_f32_e32 v8, 0x42800000, v8
	s_waitcnt vmcnt(4)
	v_mul_f32_e32 v12, 0x42800000, v12
	v_cvt_pk_fp8_f32 v18, v21, v22 op_sel:[0,0,1]
	v_cvt_pk_fp8_f32 v19, v8, v12 op_sel:[0,0,1]
	v_mul_f32_e32 v0, 0x42800000, v97
	v_mul_f32_e32 v4, 0x42800000, v101
	v_mul_f32_e32 v8, 0x42800000, v105
	ds_write_b128 v204, v[16:19] offset:32768
	v_mov_b32_e32 v16, v129
	v_cvt_pk_fp8_f32 v16, v0, v4
	v_mul_f32_e32 v0, 0x42800000, v65
	v_mul_f32_e32 v4, 0x42800000, v69
	v_mov_b32_e32 v17, v129
	v_cvt_pk_fp8_f32 v17, v0, v4
	v_mul_f32_e32 v0, 0x42800000, v33
	v_mul_f32_e32 v4, 0x42800000, v37
	v_mov_b32_e32 v18, v129
	v_cvt_pk_fp8_f32 v18, v0, v4
	v_mul_f32_e32 v0, 0x42800000, v1
	v_mul_f32_e32 v1, 0x42800000, v5
	v_mov_b32_e32 v19, v129
	v_cvt_pk_fp8_f32 v19, v0, v1
	v_mul_f32_e32 v12, 0x42800000, v125
	v_cvt_pk_fp8_f32 v16, v8, v12 op_sel:[0,0,1]
	v_mul_f32_e32 v8, 0x42800000, v73
	v_mul_f32_e32 v12, 0x42800000, v77
	v_cvt_pk_fp8_f32 v17, v8, v12 op_sel:[0,0,1]
	v_mul_f32_e32 v8, 0x42800000, v41
	v_mul_f32_e32 v12, 0x42800000, v45
	v_mul_f32_e32 v4, 0x42800000, v9
	v_mul_f32_e32 v5, 0x42800000, v13
	v_cvt_pk_fp8_f32 v18, v8, v12 op_sel:[0,0,1]
	v_cvt_pk_fp8_f32 v19, v4, v5 op_sel:[0,0,1]
	v_mul_f32_e32 v0, 0x42800000, v98
	v_mul_f32_e32 v1, 0x42800000, v102
	v_mul_f32_e32 v4, 0x42800000, v106
	ds_write_b128 v204, v[16:19] offset:32896
	v_mov_b32_e32 v16, v129
	v_cvt_pk_fp8_f32 v16, v0, v1
	v_mul_f32_e32 v0, 0x42800000, v66
	v_mul_f32_e32 v1, 0x42800000, v70
	v_mov_b32_e32 v17, v129
	v_cvt_pk_fp8_f32 v17, v0, v1
	v_mul_f32_e32 v0, 0x42800000, v34
	v_mul_f32_e32 v1, 0x42800000, v38
	v_mov_b32_e32 v18, v129
	v_cvt_pk_fp8_f32 v18, v0, v1
	v_mul_f32_e32 v0, 0x42800000, v2
	v_mul_f32_e32 v1, 0x42800000, v6
	v_mov_b32_e32 v19, v129
	v_mul_f32_e32 v5, 0x42800000, v126
	v_cvt_pk_fp8_f32 v19, v0, v1
	v_cvt_pk_fp8_f32 v16, v4, v5 op_sel:[0,0,1]
	v_mul_f32_e32 v4, 0x42800000, v74
	v_mul_f32_e32 v5, 0x42800000, v78
	v_cvt_pk_fp8_f32 v17, v4, v5 op_sel:[0,0,1]
	v_mul_f32_e32 v4, 0x42800000, v42
	v_mul_f32_e32 v5, 0x42800000, v46
	v_cvt_pk_fp8_f32 v18, v4, v5 op_sel:[0,0,1]
	v_mul_f32_e32 v2, 0x42800000, v10
	v_mul_f32_e32 v4, 0x42800000, v14
	v_cvt_pk_fp8_f32 v19, v2, v4 op_sel:[0,0,1]
	v_mul_f32_e32 v1, 0x42800000, v99
	v_mul_f32_e32 v2, 0x42800000, v103
	v_mov_b32_e32 v0, v129
	v_cvt_pk_fp8_f32 v0, v1, v2
	v_mul_f32_e32 v4, 0x42800000, v107
	v_mul_f32_e32 v5, 0x42800000, v127
	v_mul_f32_e32 v2, 0x42800000, v67
	v_cvt_pk_fp8_f32 v0, v4, v5 op_sel:[0,0,1]
	v_mul_f32_e32 v4, 0x42800000, v71
	v_mov_b32_e32 v1, v129
	v_cvt_pk_fp8_f32 v1, v2, v4
	v_mul_f32_e32 v5, 0x42800000, v75
	v_mul_f32_e32 v6, 0x42800000, v79
	v_mul_f32_e32 v4, 0x42800000, v35
	v_cvt_pk_fp8_f32 v1, v5, v6 op_sel:[0,0,1]
	v_mul_f32_e32 v5, 0x42800000, v39
	v_mov_b32_e32 v2, v129
	v_cvt_pk_fp8_f32 v2, v4, v5
	v_mul_f32_e32 v4, 0x42800000, v3
	v_mul_f32_e32 v5, 0x42800000, v7
	v_mov_b32_e32 v3, v129
	v_cvt_pk_fp8_f32 v3, v4, v5
	v_mul_f32_e32 v6, 0x42800000, v43
	v_mul_f32_e32 v8, 0x42800000, v47
	v_cvt_pk_fp8_f32 v2, v6, v8 op_sel:[0,0,1]
	v_mul_f32_e32 v6, 0x42800000, v11
	v_mul_f32_e32 v7, 0x42800000, v15
	v_cvt_pk_fp8_f32 v3, v6, v7 op_sel:[0,0,1]
	ds_write_b128 v204, v[16:19] offset:33024
	ds_write_b128 v204, v[0:3] offset:33152
	s_waitcnt lgkmcnt(0)
	s_barrier
	ds_read_b128 v[0:3], v205 offset:32768
	v_lshl_add_u64 v[4:5], v[140:141], 0, s[46:47]
	v_lshl_add_u64 v[6:7], v[4:5], 0, v[132:133]
	s_waitcnt lgkmcnt(0)
	global_store_dwordx4 v[6:7], v[0:3], off nt
	ds_read_b128 v[0:3], v206 offset:32768
	v_lshl_add_u64 v[6:7], v[4:5], 0, v[134:135]
	s_waitcnt lgkmcnt(0)
	global_store_dwordx4 v[6:7], v[0:3], off nt
	ds_read_b128 v[0:3], v207 offset:32768
	v_lshl_add_u64 v[6:7], v[4:5], 0, v[136:137]
	v_lshl_add_u64 v[4:5], v[4:5], 0, v[138:139]
	s_waitcnt lgkmcnt(0)
	global_store_dwordx4 v[6:7], v[0:3], off nt
	ds_read_b128 v[0:3], v208 offset:32768
	s_waitcnt lgkmcnt(0)
	global_store_dwordx4 v[4:5], v[0:3], off nt
	s_mov_b64 s[48:49], 0

; #define LAS __attribute__((address_space(3)))
; __device__ __forceinline__ void conv_queue(const Params& p, LAS unsigned char* lds, const int wave, const int cw, const int first, const int last, const int slot_off = LDS_MISC) {
;     const int tid = phase_tid(wave);
;     const int lane = tid & 63, wv = tid >> 6;
;     LAS int* slot = (LAS int*)(lds + slot_off);
; __global__ void __launch_bounds__(NTHREADS, 2) fwd(Params p) {
;     ...
;         ntiles = __builtin_amdgcn_readfirstlane(cnt[NE]); }
;     {
;         pg8::Gemm g{(const bf16_t*)p.xb, (const bf16_t*)p.wt_gu, ND / 2, ND / 2, ND / 2};
;         MoeOrder S{G, bid, 2 * DFF / 256, ntiles, (const LAS unsigned*)(lds + LDS_MISC), (size_t)256 * ND, (size_t)(2 * DFF) * ND, (size_t)256 * ND}; S.ncv = NCV;
;         if (bid < NCV) conv_queue(p, lds, wave, CW_CONV4, N_GU + XP5, N_GU + N_DN - N_DEFER, LDS_MISC + 1024);
.LBB0_1244:
	s_or_b64 exec, exec, s[4:5]
	s_add_i32 s0, 0, 0x20580
	v_mov_b32_e32 v0, s0
	s_waitcnt lgkmcnt(0)
	s_barrier
	ds_read_b32 v0, v0
	v_readlane_b32 s0, v254, 3
	s_cmp_gt_i32 s0, 39
	s_cselect_b64 s[6:7], -1, 0
	s_mov_b32 s5, 0
	s_waitcnt lgkmcnt(0)
	v_readfirstlane_b32 s3, v0
	s_and_b64 vcc, exec, s[6:7]
	v_readlane_b32 s1, v254, 4
	s_cbranch_vccnz .LBB0_1257
	v_mbcnt_lo_u32_b32 v1, -1, 0
	v_mbcnt_hi_u32_b32 v1, -1, v1
	v_readlane_b32 s2, v255, 30
	v_and_b32_e32 v2, 63, v1
	v_add_u32_e32 v3, s91, v1
	v_lshlrev_b32_e32 v0, 2, v2
	v_lshl_add_u32 v6, v2, 9, 0
	v_bitop3_b32 v2, v1, s2, 7 bitop3:0x6c
	v_cmp_eq_u32_e64 s[0:1], 0, v3
	v_lshlrev_b32_e32 v7, 4, v2
	v_ashrrev_i32_e32 v2, 3, v3
	v_lshrrev_b32_e32 v3, 5, v3
	v_xor_b32_e32 v3, v3, v1
	v_lshlrev_b32_e32 v3, 4, v3
	v_add_u32_e32 v4, 64, v2
	v_and_b32_e32 v3, 0x70, v3
	v_ashrrev_i32_e32 v5, 31, v4
	v_add_u32_e32 v8, 0, v3
	v_lshlrev_b32_e32 v1, 4, v1
	v_ashrrev_i32_e32 v3, 31, v2
	v_lshlrev_b32_e32 v9, 7, v4
	v_lshlrev_b64 v[142:143], 11, v[4:5]
	v_add_u32_e32 v4, 0x80, v2
	v_readlane_b32 s16, v254, 5
	v_and_b32_e32 v138, 0x70, v1
	v_lshlrev_b32_e32 v1, 7, v2
	v_lshlrev_b64 v[140:141], 11, v[2:3]
	v_ashrrev_i32_e32 v5, 31, v4
	v_add_u32_e32 v2, 0xc0, v2
	v_readlane_b32 s17, v254, 6
	s_add_u32 s8, s16, 0x20e0
	v_mov_b32_e32 v137, 0
	v_lshlrev_b32_e32 v10, 7, v4
	v_lshlrev_b64 v[144:145], 11, v[4:5]
	v_lshlrev_b32_e32 v4, 7, v2
	v_ashrrev_i32_e32 v3, 31, v2
	s_addc_u32 s9, s17, 0
	s_add_i32 s13, 0, 0x20400
	v_mov_b32_e32 v139, v137
	v_lshlrev_b64 v[146:147], 11, v[2:3]
	v_mov_b32_e32 v204, s13
	s_movk_i32 s60, 0x4000
	s_mov_b32 s61, 0x8000
	s_mov_b32 s62, 0xc000
	s_mov_b32 s63, 0x10000
	s_mov_b32 s64, 0x14000
	s_mov_b32 s65, 0x18000
	s_mov_b32 s66, 0x1c000
	v_add_u32_e32 v205, v6, v7
	v_add_u32_e32 v206, v8, v1
	v_add_u32_e32 v207, v8, v9
	v_add_u32_e32 v208, v8, v10
	v_add_u32_e32 v209, v8, v4
	s_mov_b64 s[10:11], 0x80000
	s_mov_b64 s[38:39], 0x100000
	s_movk_i32 s67, 0x1000
	s_movk_i32 s68, 0x5000
	s_mov_b32 s69, 0x9000
	s_mov_b32 s70, 0xd000
	s_mov_b32 s71, 0x11000
	s_mov_b32 s72, 0x15000
	s_mov_b32 s73, 0x19000
	s_mov_b32 s74, 0x1d000
	s_mov_b64 s[40:41], 0x180000
	s_mov_b64 s[42:43], 0x200000
	s_mov_b64 s[44:45], 0x280000
	s_mov_b64 s[46:47], 0x300000
	s_mov_b64 s[48:49], 0x380000
	v_lshlrev_b32_e32 v136, 2, v0
	v_readlane_b32 s18, v254, 7
	v_readlane_b32 s19, v254, 8
	v_readlane_b32 s20, v254, 9
	v_readlane_b32 s21, v254, 10
	v_readlane_b32 s22, v254, 11
	v_readlane_b32 s23, v254, 12
	v_readlane_b32 s24, v254, 13
	v_readlane_b32 s25, v254, 14
	v_readlane_b32 s26, v254, 15
	v_readlane_b32 s27, v254, 16
	v_readlane_b32 s28, v254, 17
	v_readlane_b32 s29, v254, 18
	v_readlane_b32 s30, v254, 19
	v_readlane_b32 s31, v254, 20
	s_branch .LBB0_1248

; #define LAS __attribute__((address_space(3)))
; __device__ __forceinline__ void cvt_item_lds(const float* src, int ld_src, fp8_t* dst, int ld_dst, LAS unsigned char* lds, int tid, int wv) {
;     const int lane = tid & 63;
;     const float* s = src + (size_t)(16 * wv) * ld_src + 4 * lane;
;     f32x4 va[16], vb[16];
;     cvt8_load(va, s, ld_src);
; __device__ __forceinline__ void conv_queue(const Params& p, LAS unsigned char* lds, const int wave, const int cw, const int first, const int last, const int slot_off = LDS_MISC) {
;     ...
;     for (;;) {
;         __syncthreads();
;         if (tid == 0) *slot = first + (int)atomicAdd(&p.ctl[cw], 1u);
;         __syncthreads();
;         const int it = *slot;
;         if (it >= last) break;
;         if (it < N_GU) { const int e = it >> 5, rem = it & 31, kb = rem >> 1, nh = rem & 1;
;             const float* src = p.w_gu + (size_t)e * ND * (2 * DFF) + (size_t)(kb * 128) * (2 * DFF) + nh * 2048;
;             fp8_t* dst = p.wt_gu + (size_t)e * (2 * DFF) * ND + (size_t)(nh * 2048) * ND + kb * 128;
;             cvt_item_lds(src, 2 * DFF, dst, ND, lds, tid, wave); }
;         else { const int j = it - N_GU, e = j >> 4, kb = j & 15;
;             const float* src = p.w_down + (size_t)e * DFF * ND + (size_t)(kb * 128) * ND;
;             fp8_t* dst = p.wt_down + (size_t)e * ND * DFF + kb * 128;
;             cvt_item_lds(src, ND, dst, DFF, lds, tid, wave); }
.LBB0_1251:
	s_or_b64 exec, exec, s[52:53]
	s_waitcnt vmcnt(0)
	v_readfirstlane_b32 s2, v1
	v_mov_b32_e32 v1, s13
	s_nop 0
	v_add_u32_e32 v0, s2, v0
	v_add_u32_e32 v0, 0x420, v0
	ds_write_b32 v1, v0
.LBB0_1252:
	s_or_b64 exec, exec, s[50:51]
	s_waitcnt lgkmcnt(0)
	s_barrier
	ds_read_b32 v0, v204
	s_movk_i32 s2, 0x5bf
	s_mov_b64 s[50:51], -1
	s_waitcnt lgkmcnt(0)
	v_cmp_lt_i32_e32 vcc, s2, v0
	v_readfirstlane_b32 s33, v0
	s_cbranch_vccnz .LBB0_1247
	s_cmpk_gt_i32 s33, 0x3ff
	s_cbranch_scc0 .LBB0_1255
	s_add_i32 s2, s33, 0xfffffc00
	v_readlane_b32 s52, v254, 26
	v_readlane_b32 s53, v254, 27
	s_lshr_b32 s4, s2, 4
	s_lshl_b64 s[34:35], s[4:5], 22
	s_add_u32 s34, s56, s34
	s_addc_u32 s35, s57, s35
	s_lshl_b32 s50, s33, 7
	s_and_b32 s50, s50, 0x780
	s_add_u32 s64, s34, s50
	s_addc_u32 s65, s35, 0
	s_lshr_b32 s51, s2, 12
	s_lshl_b32 s50, s2, 20
	s_add_u32 s50, s50, s52
	s_addc_u32 s51, s51, s53
	s_add_u32 s16, s50, s14
	s_addc_u32 s17, s51, s15
	s_add_u32 s18, s16, 0x2000
	s_addc_u32 s19, s17, 0
	s_add_u32 s20, s18, 0x2000
	s_addc_u32 s21, s19, 0
	s_add_u32 s22, s20, 0x2000
	s_addc_u32 s23, s21, 0
	s_add_u32 s24, s22, 0x2000
	s_addc_u32 s25, s23, 0
	s_add_u32 s26, s24, 0x2000
	s_addc_u32 s27, s25, 0
	s_add_u32 s28, s26, 0x2000
	s_addc_u32 s29, s27, 0
	s_add_u32 s30, s28, 0x2000
	s_addc_u32 s31, s29, 0
	s_add_u32 s38, s30, 0x2000
	s_addc_u32 s39, s31, 0
	s_add_u32 s40, s38, 0x2000
	s_addc_u32 s41, s39, 0
	s_add_u32 s42, s40, 0x2000
	s_addc_u32 s43, s41, 0
	s_add_u32 s44, s42, 0x2000
	s_addc_u32 s45, s43, 0
	s_add_u32 s46, s44, 0x2000
	s_addc_u32 s47, s45, 0
	s_add_u32 s48, s46, 0x2000
	s_addc_u32 s49, s47, 0
	s_add_u32 s60, s48, 0x2000
	s_addc_u32 s61, s49, 0
	s_add_u32 s62, s60, 0x2000
	s_addc_u32 s63, s61, 0
	global_load_dwordx4 v[0:3], v136, s[16:17] nt
	global_load_dwordx4 v[4:7], v136, s[18:19] nt
	global_load_dwordx4 v[8:11], v136, s[20:21] nt
	global_load_dwordx4 v[12:15], v136, s[22:23] nt
	global_load_dwordx4 v[16:19], v136, s[24:25] nt
	global_load_dwordx4 v[20:23], v136, s[26:27] nt
	global_load_dwordx4 v[24:27], v136, s[28:29] nt
	global_load_dwordx4 v[28:31], v136, s[30:31] nt
	global_load_dwordx4 v[32:35], v136, s[38:39] nt
	global_load_dwordx4 v[36:39], v136, s[40:41] nt
	global_load_dwordx4 v[40:43], v136, s[42:43] nt
	global_load_dwordx4 v[44:47], v136, s[44:45] nt
	global_load_dwordx4 v[48:51], v136, s[46:47] nt
	global_load_dwordx4 v[52:55], v136, s[48:49] nt
	global_load_dwordx4 v[56:59], v136, s[60:61] nt
	global_load_dwordx4 v[60:63], v136, s[62:63] nt
	global_load_dwordx4 v[64:67], v136, s[16:17] offset:1024 nt
	global_load_dwordx4 v[68:71], v136, s[18:19] offset:1024 nt
	global_load_dwordx4 v[72:75], v136, s[20:21] offset:1024 nt
	global_load_dwordx4 v[76:79], v136, s[22:23] offset:1024 nt
	global_load_dwordx4 v[80:83], v136, s[24:25] offset:1024 nt
	global_load_dwordx4 v[84:87], v136, s[26:27] offset:1024 nt
	global_load_dwordx4 v[88:91], v136, s[28:29] offset:1024 nt
	global_load_dwordx4 v[92:95], v136, s[30:31] offset:1024 nt
	global_load_dwordx4 v[96:99], v136, s[38:39] offset:1024 nt
	global_load_dwordx4 v[100:103], v136, s[40:41] offset:1024 nt
	global_load_dwordx4 v[104:107], v136, s[42:43] offset:1024 nt
	global_load_dwordx4 v[108:111], v136, s[44:45] offset:1024 nt
	global_load_dwordx4 v[112:115], v136, s[46:47] offset:1024 nt
	global_load_dwordx4 v[116:119], v136, s[48:49] offset:1024 nt
	global_load_dwordx4 v[120:123], v136, s[60:61] offset:1024 nt
	global_load_dwordx4 v[124:127], v136, s[62:63] offset:1024 nt
	global_load_dwordx4 v[128:131], v136, s[16:17] offset:2048 nt
	global_load_dwordx4 v[132:135], v136, s[18:19] offset:2048 nt
	global_load_dwordx4 v[148:151], v136, s[20:21] offset:2048 nt
	global_load_dwordx4 v[152:155], v136, s[22:23] offset:2048 nt
	global_load_dwordx4 v[156:159], v136, s[24:25] offset:2048 nt
	global_load_dwordx4 v[160:163], v136, s[26:27] offset:2048 nt
	global_load_dwordx4 v[164:167], v136, s[28:29] offset:2048 nt
	global_load_dwordx4 v[168:171], v136, s[30:31] offset:2048 nt
	global_load_dwordx4 v[172:175], v136, s[38:39] offset:2048 nt
	global_load_dwordx4 v[176:179], v136, s[40:41] offset:2048 nt
	global_load_dwordx4 v[180:183], v136, s[42:43] offset:2048 nt
	global_load_dwordx4 v[184:187], v136, s[44:45] offset:2048 nt
	global_load_dwordx4 v[188:191], v136, s[46:47] offset:2048 nt
	global_load_dwordx4 v[192:195], v136, s[48:49] offset:2048 nt
	global_load_dwordx4 v[196:199], v136, s[60:61] offset:2048 nt
	global_load_dwordx4 v[200:203], v136, s[62:63] offset:2048 nt
	s_waitcnt vmcnt(32)
; #define LAS __attribute__((address_space(3)))
; __device__ __forceinline__ unsigned pack4_fp8(float a, float b, float c, float d) { int r = 0; r = __builtin_amdgcn_cvt_pk_fp8_f32(a, b, r, false); r = __builtin_amdgcn_cvt_pk_fp8_f32(c, d, r, true); return (unsigned)r; }
; #define CVT_LDS_BAR() do { asm volatile("s_waitcnt lgkmcnt(0)" ::: "memory"); __builtin_amdgcn_s_barrier(); asm volatile("" ::: "memory"); } while (0)
; __device__ __forceinline__ void cvt8_to_lds(const f32x4 (&v)[16], LAS unsigned char* tile, int lane, int wv) {
; #pragma unroll
;     for (int i = 0; i < 4; ++i) { u32x4 w; w.x = pack4_fp8(v[0][i] * W8_SCALE, v[1][i] * W8_SCALE, v[2][i] * W8_SCALE, v[3][i] * W8_SCALE); w.y = pack4_fp8(v[4][i] * W8_SCALE, v[5][i] * W8_SCALE, v[6][i] * W8_SCALE, v[7][i] * W8_SCALE);
;         w.z = pack4_fp8(v[8][i] * W8_SCALE, v[9][i] * W8_SCALE, v[10][i] * W8_SCALE, v[11][i] * W8_SCALE); w.w = pack4_fp8(v[12][i] * W8_SCALE, v[13][i] * W8_SCALE, v[14][i] * W8_SCALE, v[15][i] * W8_SCALE);
;         *(LAS u32x4*)(tile + (4 * lane + i) * 128 + ((wv ^ (lane & 7)) << 4)) = w; }
; }
; __device__ __forceinline__ void cvt8_from_lds(const LAS unsigned char* tile, fp8_t* d, int ld_dst, int tid) {
;     const int c = tid & 7;
; #pragma unroll
;     for (int q = 0; q < 4; ++q) { const int r = (tid >> 3) + 64 * q; const u32x4 w = *(const LAS u32x4*)(tile + r * 128 + ((c ^ ((r >> 2) & 7)) << 4));
;         __builtin_nontemporal_store(w, (u32x4*)(d + (size_t)r * ld_dst + 16 * c)); }
; __device__ __forceinline__ void cvt_item_lds(const float* src, int ld_src, fp8_t* dst, int ld_dst, LAS unsigned char* lds, int tid, int wv) {
;     ...
;     for (int t = 0; t < 8; t += 2) {
;         cvt8_load(vb, s + (t + 1) * 256, ld_src); __builtin_amdgcn_sched_barrier(0);
;         cvt8_to_lds(va, lds, lane, wv); CVT_LDS_BAR(); __builtin_amdgcn_sched_barrier(0);
;         cvt8_from_lds(lds, dst + (size_t)(t * 256) * ld_dst, ld_dst, tid); __builtin_amdgcn_sched_barrier(0);
;         if (t + 2 < 8) { cvt8_load(va, s + (t + 2) * 256, ld_src); __builtin_amdgcn_sched_barrier(0); }
	v_mul_f32_e32 v0, 0x42800000, v0
	v_mul_f32_e32 v4, 0x42800000, v4
	v_mul_f32_e32 v8, 0x42800000, v8
	v_mul_f32_e32 v12, 0x42800000, v12
	v_mul_f32_e32 v16, 0x42800000, v16
	v_mul_f32_e32 v20, 0x42800000, v20
	v_mul_f32_e32 v24, 0x42800000, v24
	v_mul_f32_e32 v28, 0x42800000, v28
	v_mul_f32_e32 v32, 0x42800000, v32
	v_mul_f32_e32 v36, 0x42800000, v36
	v_mul_f32_e32 v40, 0x42800000, v40
	v_mul_f32_e32 v44, 0x42800000, v44
	v_mul_f32_e32 v48, 0x42800000, v48
	v_mul_f32_e32 v52, 0x42800000, v52
	v_mul_f32_e32 v56, 0x42800000, v56
	v_mul_f32_e32 v60, 0x42800000, v60
	v_cvt_pk_fp8_f32 v210, v0, v4
	v_cvt_pk_fp8_f32 v211, v16, v20
	v_cvt_pk_fp8_f32 v212, v32, v36
	v_cvt_pk_fp8_f32 v213, v48, v52
	v_cvt_pk_fp8_f32 v210, v8, v12 op_sel:[0,0,1]
	v_cvt_pk_fp8_f32 v211, v24, v28 op_sel:[0,0,1]
	v_cvt_pk_fp8_f32 v212, v40, v44 op_sel:[0,0,1]
	v_cvt_pk_fp8_f32 v213, v56, v60 op_sel:[0,0,1]
	ds_write_b128 v205, v[210:213] offset:0
	v_mul_f32_e32 v1, 0x42800000, v1
	v_mul_f32_e32 v5, 0x42800000, v5
	v_mul_f32_e32 v9, 0x42800000, v9
	v_mul_f32_e32 v13, 0x42800000, v13
	v_mul_f32_e32 v17, 0x42800000, v17
	v_mul_f32_e32 v21, 0x42800000, v21
	v_mul_f32_e32 v25, 0x42800000, v25
	v_mul_f32_e32 v29, 0x42800000, v29
	v_mul_f32_e32 v33, 0x42800000, v33
	v_mul_f32_e32 v37, 0x42800000, v37
	v_mul_f32_e32 v41, 0x42800000, v41
	v_mul_f32_e32 v45, 0x42800000, v45
	v_mul_f32_e32 v49, 0x42800000, v49
	v_mul_f32_e32 v53, 0x42800000, v53
	v_mul_f32_e32 v57, 0x42800000, v57
	v_mul_f32_e32 v61, 0x42800000, v61
	v_cvt_pk_fp8_f32 v210, v1, v5
	v_cvt_pk_fp8_f32 v211, v17, v21
	v_cvt_pk_fp8_f32 v212, v33, v37
	v_cvt_pk_fp8_f32 v213, v49, v53
	v_cvt_pk_fp8_f32 v210, v9, v13 op_sel:[0,0,1]
	v_cvt_pk_fp8_f32 v211, v25, v29 op_sel:[0,0,1]
	v_cvt_pk_fp8_f32 v212, v41, v45 op_sel:[0,0,1]
	v_cvt_pk_fp8_f32 v213, v57, v61 op_sel:[0,0,1]
	ds_write_b128 v205, v[210:213] offset:128
	v_mul_f32_e32 v2, 0x42800000, v2
	v_mul_f32_e32 v6, 0x42800000, v6
	v_mul_f32_e32 v10, 0x42800000, v10
	v_mul_f32_e32 v14, 0x42800000, v14
	v_mul_f32_e32 v18, 0x42800000, v18
	v_mul_f32_e32 v22, 0x42800000, v22
	v_mul_f32_e32 v26, 0x42800000, v26
	v_mul_f32_e32 v30, 0x42800000, v30
	v_mul_f32_e32 v34, 0x42800000, v34
	v_mul_f32_e32 v38, 0x42800000, v38
	v_mul_f32_e32 v42, 0x42800000, v42
	v_mul_f32_e32 v46, 0x42800000, v46
	v_mul_f32_e32 v50, 0x42800000, v50
	v_mul_f32_e32 v54, 0x42800000, v54
	v_mul_f32_e32 v58, 0x42800000, v58
	v_mul_f32_e32 v62, 0x42800000, v62
	v_cvt_pk_fp8_f32 v210, v2, v6
	v_cvt_pk_fp8_f32 v211, v18, v22
	v_cvt_pk_fp8_f32 v212, v34, v38
	v_cvt_pk_fp8_f32 v213, v50, v54
	v_cvt_pk_fp8_f32 v210, v10, v14 op_sel:[0,0,1]
	v_cvt_pk_fp8_f32 v211, v26, v30 op_sel:[0,0,1]
	v_cvt_pk_fp8_f32 v212, v42, v46 op_sel:[0,0,1]
	v_cvt_pk_fp8_f32 v213, v58, v62 op_sel:[0,0,1]
	ds_write_b128 v205, v[210:213] offset:256
	v_mul_f32_e32 v3, 0x42800000, v3
	v_mul_f32_e32 v7, 0x42800000, v7
	v_mul_f32_e32 v11, 0x42800000, v11
	v_mul_f32_e32 v15, 0x42800000, v15
	v_mul_f32_e32 v19, 0x42800000, v19
	v_mul_f32_e32 v23, 0x42800000, v23
	v_mul_f32_e32 v27, 0x42800000, v27
	v_mul_f32_e32 v31, 0x42800000, v31
	v_mul_f32_e32 v35, 0x42800000, v35
	v_mul_f32_e32 v39, 0x42800000, v39
	v_mul_f32_e32 v43, 0x42800000, v43
	v_mul_f32_e32 v47, 0x42800000, v47
	v_mul_f32_e32 v51, 0x42800000, v51
	v_mul_f32_e32 v55, 0x42800000, v55
	v_mul_f32_e32 v59, 0x42800000, v59
	v_mul_f32_e32 v63, 0x42800000, v63
	v_cvt_pk_fp8_f32 v210, v3, v7
	v_cvt_pk_fp8_f32 v211, v19, v23
	v_cvt_pk_fp8_f32 v212, v35, v39
	v_cvt_pk_fp8_f32 v213, v51, v55
	v_cvt_pk_fp8_f32 v210, v11, v15 op_sel:[0,0,1]
	v_cvt_pk_fp8_f32 v211, v27, v31 op_sel:[0,0,1]
	v_cvt_pk_fp8_f32 v212, v43, v47 op_sel:[0,0,1]
	v_cvt_pk_fp8_f32 v213, v59, v63 op_sel:[0,0,1]
	ds_write_b128 v205, v[210:213] offset:384
	s_waitcnt lgkmcnt(0)
	s_barrier
	ds_read_b128 v[0:3], v206
	ds_read_b128 v[4:7], v207
	ds_read_b128 v[8:11], v208
	ds_read_b128 v[12:15], v209
	v_add_u32_e32 v16, v140, v138
	v_add_u32_e32 v17, v142, v138
	v_add_u32_e32 v18, v144, v138
	v_add_u32_e32 v19, v146, v138
	s_waitcnt lgkmcnt(3)
	global_store_dwordx4 v16, v[0:3], s[64:65] nt
	s_waitcnt lgkmcnt(2)
	global_store_dwordx4 v17, v[4:7], s[64:65] nt
	s_waitcnt lgkmcnt(1)
	global_store_dwordx4 v18, v[8:11], s[64:65] nt
	s_waitcnt lgkmcnt(0)
	global_store_dwordx4 v19, v[12:15], s[64:65] nt
	s_add_u32 s64, s64, 0x80000
	s_addc_u32 s65, s65, 0
	s_nop 1
	global_load_dwordx4 v[0:3], v136, s[16:17] offset:3072 nt
	global_load_dwordx4 v[4:7], v136, s[18:19] offset:3072 nt
	global_load_dwordx4 v[8:11], v136, s[20:21] offset:3072 nt
	global_load_dwordx4 v[12:15], v136, s[22:23] offset:3072 nt
	global_load_dwordx4 v[16:19], v136, s[24:25] offset:3072 nt
	global_load_dwordx4 v[20:23], v136, s[26:27] offset:3072 nt
	global_load_dwordx4 v[24:27], v136, s[28:29] offset:3072 nt
	global_load_dwordx4 v[28:31], v136, s[30:31] offset:3072 nt
	global_load_dwordx4 v[32:35], v136, s[38:39] offset:3072 nt
	global_load_dwordx4 v[36:39], v136, s[40:41] offset:3072 nt
	global_load_dwordx4 v[40:43], v136, s[42:43] offset:3072 nt
	global_load_dwordx4 v[44:47], v136, s[44:45] offset:3072 nt
	global_load_dwordx4 v[48:51], v136, s[46:47] offset:3072 nt
	global_load_dwordx4 v[52:55], v136, s[48:49] offset:3072 nt
	global_load_dwordx4 v[56:59], v136, s[60:61] offset:3072 nt
	global_load_dwordx4 v[60:63], v136, s[62:63] offset:3072 nt
	s_waitcnt vmcnt(36)
; #define LAS __attribute__((address_space(3)))
; __device__ __forceinline__ unsigned pack4_fp8(float a, float b, float c, float d) { int r = 0; r = __builtin_amdgcn_cvt_pk_fp8_f32(a, b, r, false); r = __builtin_amdgcn_cvt_pk_fp8_f32(c, d, r, true); return (unsigned)r; }
; #define CVT_LDS_BAR() do { asm volatile("s_waitcnt lgkmcnt(0)" ::: "memory"); __builtin_amdgcn_s_barrier(); asm volatile("" ::: "memory"); } while (0)
; __device__ __forceinline__ void cvt8_to_lds(const f32x4 (&v)[16], LAS unsigned char* tile, int lane, int wv) {
; #pragma unroll
;     for (int i = 0; i < 4; ++i) { u32x4 w; w.x = pack4_fp8(v[0][i] * W8_SCALE, v[1][i] * W8_SCALE, v[2][i] * W8_SCALE, v[3][i] * W8_SCALE); w.y = pack4_fp8(v[4][i] * W8_SCALE, v[5][i] * W8_SCALE, v[6][i] * W8_SCALE, v[7][i] * W8_SCALE);
;         w.z = pack4_fp8(v[8][i] * W8_SCALE, v[9][i] * W8_SCALE, v[10][i] * W8_SCALE, v[11][i] * W8_SCALE); w.w = pack4_fp8(v[12][i] * W8_SCALE, v[13][i] * W8_SCALE, v[14][i] * W8_SCALE, v[15][i] * W8_SCALE);
;         *(LAS u32x4*)(tile + (4 * lane + i) * 128 + ((wv ^ (lane & 7)) << 4)) = w; }
; }
; __device__ __forceinline__ void cvt8_from_lds(const LAS unsigned char* tile, fp8_t* d, int ld_dst, int tid) {
;     const int c = tid & 7;
; #pragma unroll
;     for (int q = 0; q < 4; ++q) { const int r = (tid >> 3) + 64 * q; const u32x4 w = *(const LAS u32x4*)(tile + r * 128 + ((c ^ ((r >> 2) & 7)) << 4));
;         __builtin_nontemporal_store(w, (u32x4*)(d + (size_t)r * ld_dst + 16 * c)); }
; __device__ __forceinline__ void cvt_item_lds(const float* src, int ld_src, fp8_t* dst, int ld_dst, LAS unsigned char* lds, int tid, int wv) {
;     ...
;     for (int t = 0; t < 8; t += 2) {
;         cvt8_load(vb, s + (t + 1) * 256, ld_src); __builtin_amdgcn_sched_barrier(0);
;         cvt8_to_lds(va, lds, lane, wv); CVT_LDS_BAR(); __builtin_amdgcn_sched_barrier(0);
;         cvt8_from_lds(lds, dst + (size_t)(t * 256) * ld_dst, ld_dst, tid); __builtin_amdgcn_sched_barrier(0);
;         if (t + 2 < 8) { cvt8_load(va, s + (t + 2) * 256, ld_src); __builtin_amdgcn_sched_barrier(0); }
;         cvt8_to_lds(vb, lds + 32768, lane, wv); CVT_LDS_BAR(); __builtin_amdgcn_sched_barrier(0);
;         cvt8_from_lds(lds + 32768, dst + (size_t)((t + 1) * 256) * ld_dst, ld_dst, tid); __builtin_amdgcn_sched_barrier(0);
	v_mul_f32_e32 v64, 0x42800000, v64
	v_mul_f32_e32 v68, 0x42800000, v68
	v_mul_f32_e32 v72, 0x42800000, v72
	v_mul_f32_e32 v76, 0x42800000, v76
	v_mul_f32_e32 v80, 0x42800000, v80
	v_mul_f32_e32 v84, 0x42800000, v84
	v_mul_f32_e32 v88, 0x42800000, v88
	v_mul_f32_e32 v92, 0x42800000, v92
	v_mul_f32_e32 v96, 0x42800000, v96
	v_mul_f32_e32 v100, 0x42800000, v100
	v_mul_f32_e32 v104, 0x42800000, v104
	v_mul_f32_e32 v108, 0x42800000, v108
	v_mul_f32_e32 v112, 0x42800000, v112
	v_mul_f32_e32 v116, 0x42800000, v116
	v_mul_f32_e32 v120, 0x42800000, v120
	v_mul_f32_e32 v124, 0x42800000, v124
	v_cvt_pk_fp8_f32 v210, v64, v68
	v_cvt_pk_fp8_f32 v211, v80, v84
	v_cvt_pk_fp8_f32 v212, v96, v100
	v_cvt_pk_fp8_f32 v213, v112, v116
	v_cvt_pk_fp8_f32 v210, v72, v76 op_sel:[0,0,1]
	v_cvt_pk_fp8_f32 v211, v88, v92 op_sel:[0,0,1]
	v_cvt_pk_fp8_f32 v212, v104, v108 op_sel:[0,0,1]
	v_cvt_pk_fp8_f32 v213, v120, v124 op_sel:[0,0,1]
	ds_write_b128 v205, v[210:213] offset:32768
	v_mul_f32_e32 v65, 0x42800000, v65
	v_mul_f32_e32 v69, 0x42800000, v69
	v_mul_f32_e32 v73, 0x42800000, v73
	v_mul_f32_e32 v77, 0x42800000, v77
	v_mul_f32_e32 v81, 0x42800000, v81
	v_mul_f32_e32 v85, 0x42800000, v85
	v_mul_f32_e32 v89, 0x42800000, v89
	v_mul_f32_e32 v93, 0x42800000, v93
	v_mul_f32_e32 v97, 0x42800000, v97
	v_mul_f32_e32 v101, 0x42800000, v101
	v_mul_f32_e32 v105, 0x42800000, v105
	v_mul_f32_e32 v109, 0x42800000, v109
	v_mul_f32_e32 v113, 0x42800000, v113
	v_mul_f32_e32 v117, 0x42800000, v117
	v_mul_f32_e32 v121, 0x42800000, v121
	v_mul_f32_e32 v125, 0x42800000, v125
	v_cvt_pk_fp8_f32 v210, v65, v69
	v_cvt_pk_fp8_f32 v211, v81, v85
	v_cvt_pk_fp8_f32 v212, v97, v101
	v_cvt_pk_fp8_f32 v213, v113, v117
	v_cvt_pk_fp8_f32 v210, v73, v77 op_sel:[0,0,1]
	v_cvt_pk_fp8_f32 v211, v89, v93 op_sel:[0,0,1]
	v_cvt_pk_fp8_f32 v212, v105, v109 op_sel:[0,0,1]
	v_cvt_pk_fp8_f32 v213, v121, v125 op_sel:[0,0,1]
	ds_write_b128 v205, v[210:213] offset:32896
	v_mul_f32_e32 v66, 0x42800000, v66
	v_mul_f32_e32 v70, 0x42800000, v70
	v_mul_f32_e32 v74, 0x42800000, v74
	v_mul_f32_e32 v78, 0x42800000, v78
	v_mul_f32_e32 v82, 0x42800000, v82
	v_mul_f32_e32 v86, 0x42800000, v86
	v_mul_f32_e32 v90, 0x42800000, v90
	v_mul_f32_e32 v94, 0x42800000, v94
	v_mul_f32_e32 v98, 0x42800000, v98
	v_mul_f32_e32 v102, 0x42800000, v102
	v_mul_f32_e32 v106, 0x42800000, v106
	v_mul_f32_e32 v110, 0x42800000, v110
	v_mul_f32_e32 v114, 0x42800000, v114
	v_mul_f32_e32 v118, 0x42800000, v118
	v_mul_f32_e32 v122, 0x42800000, v122
	v_mul_f32_e32 v126, 0x42800000, v126
	v_cvt_pk_fp8_f32 v210, v66, v70
	v_cvt_pk_fp8_f32 v211, v82, v86
	v_cvt_pk_fp8_f32 v212, v98, v102
	v_cvt_pk_fp8_f32 v213, v114, v118
	v_cvt_pk_fp8_f32 v210, v74, v78 op_sel:[0,0,1]
	v_cvt_pk_fp8_f32 v211, v90, v94 op_sel:[0,0,1]
	v_cvt_pk_fp8_f32 v212, v106, v110 op_sel:[0,0,1]
	v_cvt_pk_fp8_f32 v213, v122, v126 op_sel:[0,0,1]
	ds_write_b128 v205, v[210:213] offset:33024
	v_mul_f32_e32 v67, 0x42800000, v67
	v_mul_f32_e32 v71, 0x42800000, v71
	v_mul_f32_e32 v75, 0x42800000, v75
	v_mul_f32_e32 v79, 0x42800000, v79
	v_mul_f32_e32 v83, 0x42800000, v83
	v_mul_f32_e32 v87, 0x42800000, v87
	v_mul_f32_e32 v91, 0x42800000, v91
	v_mul_f32_e32 v95, 0x42800000, v95
	v_mul_f32_e32 v99, 0x42800000, v99
	v_mul_f32_e32 v103, 0x42800000, v103
	v_mul_f32_e32 v107, 0x42800000, v107
	v_mul_f32_e32 v111, 0x42800000, v111
	v_mul_f32_e32 v115, 0x42800000, v115
	v_mul_f32_e32 v119, 0x42800000, v119
	v_mul_f32_e32 v123, 0x42800000, v123
	v_mul_f32_e32 v127, 0x42800000, v127
	v_cvt_pk_fp8_f32 v210, v67, v71
	v_cvt_pk_fp8_f32 v211, v83, v87
	v_cvt_pk_fp8_f32 v212, v99, v103
	v_cvt_pk_fp8_f32 v213, v115, v119
	v_cvt_pk_fp8_f32 v210, v75, v79 op_sel:[0,0,1]
	v_cvt_pk_fp8_f32 v211, v91, v95 op_sel:[0,0,1]
	v_cvt_pk_fp8_f32 v212, v107, v111 op_sel:[0,0,1]
	v_cvt_pk_fp8_f32 v213, v123, v127 op_sel:[0,0,1]
	ds_write_b128 v205, v[210:213] offset:33152
	s_waitcnt lgkmcnt(0)
	s_barrier
	ds_read_b128 v[64:67], v206 offset:32768
	ds_read_b128 v[68:71], v207 offset:32768
	ds_read_b128 v[72:75], v208 offset:32768
	ds_read_b128 v[76:79], v209 offset:32768
	v_add_u32_e32 v80, v140, v138
	v_add_u32_e32 v81, v142, v138
	v_add_u32_e32 v82, v144, v138
	v_add_u32_e32 v83, v146, v138
	s_waitcnt lgkmcnt(3)
	global_store_dwordx4 v80, v[64:67], s[64:65] nt
	s_waitcnt lgkmcnt(2)
	global_store_dwordx4 v81, v[68:71], s[64:65] nt
	s_waitcnt lgkmcnt(1)
	global_store_dwordx4 v82, v[72:75], s[64:65] nt
	s_waitcnt lgkmcnt(0)
	global_store_dwordx4 v83, v[76:79], s[64:65] nt
	s_add_u32 s64, s64, 0x80000
	s_addc_u32 s65, s65, 0
	s_nop 1
	s_add_u32 s16, s16, 0x1000
	s_addc_u32 s17, s17, 0
	s_add_u32 s18, s18, 0x1000
	s_addc_u32 s19, s19, 0
	s_add_u32 s20, s20, 0x1000
	s_addc_u32 s21, s21, 0
	s_add_u32 s22, s22, 0x1000
	s_addc_u32 s23, s23, 0
	s_add_u32 s24, s24, 0x1000
	s_addc_u32 s25, s25, 0
	s_add_u32 s26, s26, 0x1000
	s_addc_u32 s27, s27, 0
	s_add_u32 s28, s28, 0x1000
	s_addc_u32 s29, s29, 0
	s_add_u32 s30, s30, 0x1000
	s_addc_u32 s31, s31, 0
	s_add_u32 s38, s38, 0x1000
	s_addc_u32 s39, s39, 0
	s_add_u32 s40, s40, 0x1000
	s_addc_u32 s41, s41, 0
	s_add_u32 s42, s42, 0x1000
	s_addc_u32 s43, s43, 0
	s_add_u32 s44, s44, 0x1000
	s_addc_u32 s45, s45, 0
	s_add_u32 s46, s46, 0x1000
	s_addc_u32 s47, s47, 0
	s_add_u32 s48, s48, 0x1000
	s_addc_u32 s49, s49, 0
	s_add_u32 s60, s60, 0x1000
	s_addc_u32 s61, s61, 0
	s_add_u32 s62, s62, 0x1000
	s_addc_u32 s63, s63, 0
	global_load_dwordx4 v[64:67], v136, s[16:17] nt
	global_load_dwordx4 v[68:71], v136, s[18:19] nt
	global_load_dwordx4 v[72:75], v136, s[20:21] nt
	global_load_dwordx4 v[76:79], v136, s[22:23] nt
	global_load_dwordx4 v[80:83], v136, s[24:25] nt
	global_load_dwordx4 v[84:87], v136, s[26:27] nt
	global_load_dwordx4 v[88:91], v136, s[28:29] nt
	global_load_dwordx4 v[92:95], v136, s[30:31] nt
	global_load_dwordx4 v[96:99], v136, s[38:39] nt
	global_load_dwordx4 v[100:103], v136, s[40:41] nt
	global_load_dwordx4 v[104:107], v136, s[42:43] nt
	global_load_dwordx4 v[108:111], v136, s[44:45] nt
	global_load_dwordx4 v[112:115], v136, s[46:47] nt
	global_load_dwordx4 v[116:119], v136, s[48:49] nt
	global_load_dwordx4 v[120:123], v136, s[60:61] nt
	global_load_dwordx4 v[124:127], v136, s[62:63] nt
	s_waitcnt vmcnt(40)
; #define LAS __attribute__((address_space(3)))
; __device__ __forceinline__ unsigned pack4_fp8(float a, float b, float c, float d) { int r = 0; r = __builtin_amdgcn_cvt_pk_fp8_f32(a, b, r, false); r = __builtin_amdgcn_cvt_pk_fp8_f32(c, d, r, true); return (unsigned)r; }
; #define CVT_LDS_BAR() do { asm volatile("s_waitcnt lgkmcnt(0)" ::: "memory"); __builtin_amdgcn_s_barrier(); asm volatile("" ::: "memory"); } while (0)
; __device__ __forceinline__ void cvt8_to_lds(const f32x4 (&v)[16], LAS unsigned char* tile, int lane, int wv) {
; #pragma unroll
;     for (int i = 0; i < 4; ++i) { u32x4 w; w.x = pack4_fp8(v[0][i] * W8_SCALE, v[1][i] * W8_SCALE, v[2][i] * W8_SCALE, v[3][i] * W8_SCALE); w.y = pack4_fp8(v[4][i] * W8_SCALE, v[5][i] * W8_SCALE, v[6][i] * W8_SCALE, v[7][i] * W8_SCALE);
;         w.z = pack4_fp8(v[8][i] * W8_SCALE, v[9][i] * W8_SCALE, v[10][i] * W8_SCALE, v[11][i] * W8_SCALE); w.w = pack4_fp8(v[12][i] * W8_SCALE, v[13][i] * W8_SCALE, v[14][i] * W8_SCALE, v[15][i] * W8_SCALE);
;         *(LAS u32x4*)(tile + (4 * lane + i) * 128 + ((wv ^ (lane & 7)) << 4)) = w; }
; }
; __device__ __forceinline__ void cvt8_from_lds(const LAS unsigned char* tile, fp8_t* d, int ld_dst, int tid) {
;     const int c = tid & 7;
; #pragma unroll
;     for (int q = 0; q < 4; ++q) { const int r = (tid >> 3) + 64 * q; const u32x4 w = *(const LAS u32x4*)(tile + r * 128 + ((c ^ ((r >> 2) & 7)) << 4));
;         __builtin_nontemporal_store(w, (u32x4*)(d + (size_t)r * ld_dst + 16 * c)); }
; __device__ __forceinline__ void cvt_item_lds(const float* src, int ld_src, fp8_t* dst, int ld_dst, LAS unsigned char* lds, int tid, int wv) {
;     ...
;     for (int t = 0; t < 8; t += 2) {
;         cvt8_load(vb, s + (t + 1) * 256, ld_src); __builtin_amdgcn_sched_barrier(0);
;         cvt8_to_lds(va, lds, lane, wv); CVT_LDS_BAR(); __builtin_amdgcn_sched_barrier(0);
;         cvt8_from_lds(lds, dst + (size_t)(t * 256) * ld_dst, ld_dst, tid); __builtin_amdgcn_sched_barrier(0);
;         if (t + 2 < 8) { cvt8_load(va, s + (t + 2) * 256, ld_src); __builtin_amdgcn_sched_barrier(0); }
;         cvt8_to_lds(vb, lds + 32768, lane, wv); CVT_LDS_BAR(); __builtin_amdgcn_sched_barrier(0);
;         cvt8_from_lds(lds + 32768, dst + (size_t)((t + 1) * 256) * ld_dst, ld_dst, tid); __builtin_amdgcn_sched_barrier(0);
	v_mul_f32_e32 v128, 0x42800000, v128
	v_mul_f32_e32 v132, 0x42800000, v132
	v_mul_f32_e32 v148, 0x42800000, v148
	v_mul_f32_e32 v152, 0x42800000, v152
	v_mul_f32_e32 v156, 0x42800000, v156
	v_mul_f32_e32 v160, 0x42800000, v160
	v_mul_f32_e32 v164, 0x42800000, v164
	v_mul_f32_e32 v168, 0x42800000, v168
	v_mul_f32_e32 v172, 0x42800000, v172
	v_mul_f32_e32 v176, 0x42800000, v176
	v_mul_f32_e32 v180, 0x42800000, v180
	v_mul_f32_e32 v184, 0x42800000, v184
	v_mul_f32_e32 v188, 0x42800000, v188
	v_mul_f32_e32 v192, 0x42800000, v192
	v_mul_f32_e32 v196, 0x42800000, v196
	v_mul_f32_e32 v200, 0x42800000, v200
	v_cvt_pk_fp8_f32 v210, v128, v132
	v_cvt_pk_fp8_f32 v211, v156, v160
	v_cvt_pk_fp8_f32 v212, v172, v176
	v_cvt_pk_fp8_f32 v213, v188, v192
	v_cvt_pk_fp8_f32 v210, v148, v152 op_sel:[0,0,1]
	v_cvt_pk_fp8_f32 v211, v164, v168 op_sel:[0,0,1]
	v_cvt_pk_fp8_f32 v212, v180, v184 op_sel:[0,0,1]
	v_cvt_pk_fp8_f32 v213, v196, v200 op_sel:[0,0,1]
	ds_write_b128 v205, v[210:213] offset:0
	v_mul_f32_e32 v129, 0x42800000, v129
	v_mul_f32_e32 v133, 0x42800000, v133
	v_mul_f32_e32 v149, 0x42800000, v149
	v_mul_f32_e32 v153, 0x42800000, v153
	v_mul_f32_e32 v157, 0x42800000, v157
	v_mul_f32_e32 v161, 0x42800000, v161
	v_mul_f32_e32 v165, 0x42800000, v165
	v_mul_f32_e32 v169, 0x42800000, v169
	v_mul_f32_e32 v173, 0x42800000, v173
	v_mul_f32_e32 v177, 0x42800000, v177
	v_mul_f32_e32 v181, 0x42800000, v181
	v_mul_f32_e32 v185, 0x42800000, v185
	v_mul_f32_e32 v189, 0x42800000, v189
	v_mul_f32_e32 v193, 0x42800000, v193
	v_mul_f32_e32 v197, 0x42800000, v197
	v_mul_f32_e32 v201, 0x42800000, v201
	v_cvt_pk_fp8_f32 v210, v129, v133
	v_cvt_pk_fp8_f32 v211, v157, v161
	v_cvt_pk_fp8_f32 v212, v173, v177
	v_cvt_pk_fp8_f32 v213, v189, v193
	v_cvt_pk_fp8_f32 v210, v149, v153 op_sel:[0,0,1]
	v_cvt_pk_fp8_f32 v211, v165, v169 op_sel:[0,0,1]
	v_cvt_pk_fp8_f32 v212, v181, v185 op_sel:[0,0,1]
	v_cvt_pk_fp8_f32 v213, v197, v201 op_sel:[0,0,1]
	ds_write_b128 v205, v[210:213] offset:128
	v_mul_f32_e32 v130, 0x42800000, v130
	v_mul_f32_e32 v134, 0x42800000, v134
	v_mul_f32_e32 v150, 0x42800000, v150
	v_mul_f32_e32 v154, 0x42800000, v154
	v_mul_f32_e32 v158, 0x42800000, v158
	v_mul_f32_e32 v162, 0x42800000, v162
	v_mul_f32_e32 v166, 0x42800000, v166
	v_mul_f32_e32 v170, 0x42800000, v170
	v_mul_f32_e32 v174, 0x42800000, v174
	v_mul_f32_e32 v178, 0x42800000, v178
	v_mul_f32_e32 v182, 0x42800000, v182
	v_mul_f32_e32 v186, 0x42800000, v186
	v_mul_f32_e32 v190, 0x42800000, v190
	v_mul_f32_e32 v194, 0x42800000, v194
	v_mul_f32_e32 v198, 0x42800000, v198
	v_mul_f32_e32 v202, 0x42800000, v202
	v_cvt_pk_fp8_f32 v210, v130, v134
	v_cvt_pk_fp8_f32 v211, v158, v162
	v_cvt_pk_fp8_f32 v212, v174, v178
	v_cvt_pk_fp8_f32 v213, v190, v194
	v_cvt_pk_fp8_f32 v210, v150, v154 op_sel:[0,0,1]
	v_cvt_pk_fp8_f32 v211, v166, v170 op_sel:[0,0,1]
	v_cvt_pk_fp8_f32 v212, v182, v186 op_sel:[0,0,1]
	v_cvt_pk_fp8_f32 v213, v198, v202 op_sel:[0,0,1]
	ds_write_b128 v205, v[210:213] offset:256
	v_mul_f32_e32 v131, 0x42800000, v131
	v_mul_f32_e32 v135, 0x42800000, v135
	v_mul_f32_e32 v151, 0x42800000, v151
	v_mul_f32_e32 v155, 0x42800000, v155
	v_mul_f32_e32 v159, 0x42800000, v159
	v_mul_f32_e32 v163, 0x42800000, v163
	v_mul_f32_e32 v167, 0x42800000, v167
	v_mul_f32_e32 v171, 0x42800000, v171
	v_mul_f32_e32 v175, 0x42800000, v175
	v_mul_f32_e32 v179, 0x42800000, v179
	v_mul_f32_e32 v183, 0x42800000, v183
	v_mul_f32_e32 v187, 0x42800000, v187
	v_mul_f32_e32 v191, 0x42800000, v191
	v_mul_f32_e32 v195, 0x42800000, v195
	v_mul_f32_e32 v199, 0x42800000, v199
	v_mul_f32_e32 v203, 0x42800000, v203
	v_cvt_pk_fp8_f32 v210, v131, v135
	v_cvt_pk_fp8_f32 v211, v159, v163
	v_cvt_pk_fp8_f32 v212, v175, v179
	v_cvt_pk_fp8_f32 v213, v191, v195
	v_cvt_pk_fp8_f32 v210, v151, v155 op_sel:[0,0,1]
	v_cvt_pk_fp8_f32 v211, v167, v171 op_sel:[0,0,1]
	v_cvt_pk_fp8_f32 v212, v183, v187 op_sel:[0,0,1]
	v_cvt_pk_fp8_f32 v213, v199, v203 op_sel:[0,0,1]
	ds_write_b128 v205, v[210:213] offset:384
	s_waitcnt lgkmcnt(0)
	s_barrier
	ds_read_b128 v[128:131], v206
	ds_read_b128 v[132:135], v207
	ds_read_b128 v[148:151], v208
	ds_read_b128 v[152:155], v209
	v_add_u32_e32 v156, v140, v138
	v_add_u32_e32 v157, v142, v138
	v_add_u32_e32 v158, v144, v138
	v_add_u32_e32 v159, v146, v138
	s_waitcnt lgkmcnt(3)
	global_store_dwordx4 v156, v[128:131], s[64:65] nt
	s_waitcnt lgkmcnt(2)
	global_store_dwordx4 v157, v[132:135], s[64:65] nt
	s_waitcnt lgkmcnt(1)
	global_store_dwordx4 v158, v[148:151], s[64:65] nt
	s_waitcnt lgkmcnt(0)
	global_store_dwordx4 v159, v[152:155], s[64:65] nt
	s_add_u32 s64, s64, 0x80000
	s_addc_u32 s65, s65, 0
	s_nop 1
	global_load_dwordx4 v[128:131], v136, s[16:17] offset:1024 nt
	global_load_dwordx4 v[132:135], v136, s[18:19] offset:1024 nt
	global_load_dwordx4 v[148:151], v136, s[20:21] offset:1024 nt
	global_load_dwordx4 v[152:155], v136, s[22:23] offset:1024 nt
	global_load_dwordx4 v[156:159], v136, s[24:25] offset:1024 nt
	global_load_dwordx4 v[160:163], v136, s[26:27] offset:1024 nt
	global_load_dwordx4 v[164:167], v136, s[28:29] offset:1024 nt
	global_load_dwordx4 v[168:171], v136, s[30:31] offset:1024 nt
	global_load_dwordx4 v[172:175], v136, s[38:39] offset:1024 nt
	global_load_dwordx4 v[176:179], v136, s[40:41] offset:1024 nt
	global_load_dwordx4 v[180:183], v136, s[42:43] offset:1024 nt
	global_load_dwordx4 v[184:187], v136, s[44:45] offset:1024 nt
	global_load_dwordx4 v[188:191], v136, s[46:47] offset:1024 nt
	global_load_dwordx4 v[192:195], v136, s[48:49] offset:1024 nt
	global_load_dwordx4 v[196:199], v136, s[60:61] offset:1024 nt
	global_load_dwordx4 v[200:203], v136, s[62:63] offset:1024 nt
	s_waitcnt vmcnt(40)
; #define LAS __attribute__((address_space(3)))
; __device__ __forceinline__ unsigned pack4_fp8(float a, float b, float c, float d) { int r = 0; r = __builtin_amdgcn_cvt_pk_fp8_f32(a, b, r, false); r = __builtin_amdgcn_cvt_pk_fp8_f32(c, d, r, true); return (unsigned)r; }
; #define CVT_LDS_BAR() do { asm volatile("s_waitcnt lgkmcnt(0)" ::: "memory"); __builtin_amdgcn_s_barrier(); asm volatile("" ::: "memory"); } while (0)
; __device__ __forceinline__ void cvt8_to_lds(const f32x4 (&v)[16], LAS unsigned char* tile, int lane, int wv) {
; #pragma unroll
;     for (int i = 0; i < 4; ++i) { u32x4 w; w.x = pack4_fp8(v[0][i] * W8_SCALE, v[1][i] * W8_SCALE, v[2][i] * W8_SCALE, v[3][i] * W8_SCALE); w.y = pack4_fp8(v[4][i] * W8_SCALE, v[5][i] * W8_SCALE, v[6][i] * W8_SCALE, v[7][i] * W8_SCALE);
;         w.z = pack4_fp8(v[8][i] * W8_SCALE, v[9][i] * W8_SCALE, v[10][i] * W8_SCALE, v[11][i] * W8_SCALE); w.w = pack4_fp8(v[12][i] * W8_SCALE, v[13][i] * W8_SCALE, v[14][i] * W8_SCALE, v[15][i] * W8_SCALE);
;         *(LAS u32x4*)(tile + (4 * lane + i) * 128 + ((wv ^ (lane & 7)) << 4)) = w; }
; }
; __device__ __forceinline__ void cvt8_from_lds(const LAS unsigned char* tile, fp8_t* d, int ld_dst, int tid) {
;     const int c = tid & 7;
; #pragma unroll
;     for (int q = 0; q < 4; ++q) { const int r = (tid >> 3) + 64 * q; const u32x4 w = *(const LAS u32x4*)(tile + r * 128 + ((c ^ ((r >> 2) & 7)) << 4));
;         __builtin_nontemporal_store(w, (u32x4*)(d + (size_t)r * ld_dst + 16 * c)); }
; __device__ __forceinline__ void cvt_item_lds(const float* src, int ld_src, fp8_t* dst, int ld_dst, LAS unsigned char* lds, int tid, int wv) {
;     ...
;     for (int t = 0; t < 8; t += 2) {
;         cvt8_load(vb, s + (t + 1) * 256, ld_src); __builtin_amdgcn_sched_barrier(0);
;         cvt8_to_lds(va, lds, lane, wv); CVT_LDS_BAR(); __builtin_amdgcn_sched_barrier(0);
;         cvt8_from_lds(lds, dst + (size_t)(t * 256) * ld_dst, ld_dst, tid); __builtin_amdgcn_sched_barrier(0);
;         if (t + 2 < 8) { cvt8_load(va, s + (t + 2) * 256, ld_src); __builtin_amdgcn_sched_barrier(0); }
;         cvt8_to_lds(vb, lds + 32768, lane, wv); CVT_LDS_BAR(); __builtin_amdgcn_sched_barrier(0);
;         cvt8_from_lds(lds + 32768, dst + (size_t)((t + 1) * 256) * ld_dst, ld_dst, tid); __builtin_amdgcn_sched_barrier(0);
	v_mul_f32_e32 v0, 0x42800000, v0
	v_mul_f32_e32 v4, 0x42800000, v4
	v_mul_f32_e32 v8, 0x42800000, v8
	v_mul_f32_e32 v12, 0x42800000, v12
	v_mul_f32_e32 v16, 0x42800000, v16
	v_mul_f32_e32 v20, 0x42800000, v20
	v_mul_f32_e32 v24, 0x42800000, v24
	v_mul_f32_e32 v28, 0x42800000, v28
	v_mul_f32_e32 v32, 0x42800000, v32
	v_mul_f32_e32 v36, 0x42800000, v36
	v_mul_f32_e32 v40, 0x42800000, v40
	v_mul_f32_e32 v44, 0x42800000, v44
	v_mul_f32_e32 v48, 0x42800000, v48
	v_mul_f32_e32 v52, 0x42800000, v52
	v_mul_f32_e32 v56, 0x42800000, v56
	v_mul_f32_e32 v60, 0x42800000, v60
	v_cvt_pk_fp8_f32 v210, v0, v4
	v_cvt_pk_fp8_f32 v211, v16, v20
	v_cvt_pk_fp8_f32 v212, v32, v36
	v_cvt_pk_fp8_f32 v213, v48, v52
	v_cvt_pk_fp8_f32 v210, v8, v12 op_sel:[0,0,1]
	v_cvt_pk_fp8_f32 v211, v24, v28 op_sel:[0,0,1]
	v_cvt_pk_fp8_f32 v212, v40, v44 op_sel:[0,0,1]
	v_cvt_pk_fp8_f32 v213, v56, v60 op_sel:[0,0,1]
	ds_write_b128 v205, v[210:213] offset:32768
	v_mul_f32_e32 v1, 0x42800000, v1
	v_mul_f32_e32 v5, 0x42800000, v5
	v_mul_f32_e32 v9, 0x42800000, v9
	v_mul_f32_e32 v13, 0x42800000, v13
	v_mul_f32_e32 v17, 0x42800000, v17
	v_mul_f32_e32 v21, 0x42800000, v21
	v_mul_f32_e32 v25, 0x42800000, v25
	v_mul_f32_e32 v29, 0x42800000, v29
	v_mul_f32_e32 v33, 0x42800000, v33
	v_mul_f32_e32 v37, 0x42800000, v37
	v_mul_f32_e32 v41, 0x42800000, v41
	v_mul_f32_e32 v45, 0x42800000, v45
	v_mul_f32_e32 v49, 0x42800000, v49
	v_mul_f32_e32 v53, 0x42800000, v53
	v_mul_f32_e32 v57, 0x42800000, v57
	v_mul_f32_e32 v61, 0x42800000, v61
	v_cvt_pk_fp8_f32 v210, v1, v5
	v_cvt_pk_fp8_f32 v211, v17, v21
	v_cvt_pk_fp8_f32 v212, v33, v37
	v_cvt_pk_fp8_f32 v213, v49, v53
	v_cvt_pk_fp8_f32 v210, v9, v13 op_sel:[0,0,1]
	v_cvt_pk_fp8_f32 v211, v25, v29 op_sel:[0,0,1]
	v_cvt_pk_fp8_f32 v212, v41, v45 op_sel:[0,0,1]
	v_cvt_pk_fp8_f32 v213, v57, v61 op_sel:[0,0,1]
	ds_write_b128 v205, v[210:213] offset:32896
	v_mul_f32_e32 v2, 0x42800000, v2
	v_mul_f32_e32 v6, 0x42800000, v6
	v_mul_f32_e32 v10, 0x42800000, v10
	v_mul_f32_e32 v14, 0x42800000, v14
	v_mul_f32_e32 v18, 0x42800000, v18
	v_mul_f32_e32 v22, 0x42800000, v22
	v_mul_f32_e32 v26, 0x42800000, v26
	v_mul_f32_e32 v30, 0x42800000, v30
	v_mul_f32_e32 v34, 0x42800000, v34
	v_mul_f32_e32 v38, 0x42800000, v38
	v_mul_f32_e32 v42, 0x42800000, v42
	v_mul_f32_e32 v46, 0x42800000, v46
	v_mul_f32_e32 v50, 0x42800000, v50
	v_mul_f32_e32 v54, 0x42800000, v54
	v_mul_f32_e32 v58, 0x42800000, v58
	v_mul_f32_e32 v62, 0x42800000, v62
	v_cvt_pk_fp8_f32 v210, v2, v6
	v_cvt_pk_fp8_f32 v211, v18, v22
	v_cvt_pk_fp8_f32 v212, v34, v38
	v_cvt_pk_fp8_f32 v213, v50, v54
	v_cvt_pk_fp8_f32 v210, v10, v14 op_sel:[0,0,1]
	v_cvt_pk_fp8_f32 v211, v26, v30 op_sel:[0,0,1]
	v_cvt_pk_fp8_f32 v212, v42, v46 op_sel:[0,0,1]
	v_cvt_pk_fp8_f32 v213, v58, v62 op_sel:[0,0,1]
	ds_write_b128 v205, v[210:213] offset:33024
	v_mul_f32_e32 v3, 0x42800000, v3
	v_mul_f32_e32 v7, 0x42800000, v7
	v_mul_f32_e32 v11, 0x42800000, v11
	v_mul_f32_e32 v15, 0x42800000, v15
	v_mul_f32_e32 v19, 0x42800000, v19
	v_mul_f32_e32 v23, 0x42800000, v23
	v_mul_f32_e32 v27, 0x42800000, v27
	v_mul_f32_e32 v31, 0x42800000, v31
	v_mul_f32_e32 v35, 0x42800000, v35
	v_mul_f32_e32 v39, 0x42800000, v39
	v_mul_f32_e32 v43, 0x42800000, v43
	v_mul_f32_e32 v47, 0x42800000, v47
	v_mul_f32_e32 v51, 0x42800000, v51
	v_mul_f32_e32 v55, 0x42800000, v55
	v_mul_f32_e32 v59, 0x42800000, v59
	v_mul_f32_e32 v63, 0x42800000, v63
	v_cvt_pk_fp8_f32 v210, v3, v7
	v_cvt_pk_fp8_f32 v211, v19, v23
	v_cvt_pk_fp8_f32 v212, v35, v39
	v_cvt_pk_fp8_f32 v213, v51, v55
	v_cvt_pk_fp8_f32 v210, v11, v15 op_sel:[0,0,1]
	v_cvt_pk_fp8_f32 v211, v27, v31 op_sel:[0,0,1]
	v_cvt_pk_fp8_f32 v212, v43, v47 op_sel:[0,0,1]
	v_cvt_pk_fp8_f32 v213, v59, v63 op_sel:[0,0,1]
	ds_write_b128 v205, v[210:213] offset:33152
	s_waitcnt lgkmcnt(0)
	s_barrier
	ds_read_b128 v[0:3], v206 offset:32768
	ds_read_b128 v[4:7], v207 offset:32768
	ds_read_b128 v[8:11], v208 offset:32768
	ds_read_b128 v[12:15], v209 offset:32768
	v_add_u32_e32 v16, v140, v138
	v_add_u32_e32 v17, v142, v138
	v_add_u32_e32 v18, v144, v138
	v_add_u32_e32 v19, v146, v138
	s_waitcnt lgkmcnt(3)
	global_store_dwordx4 v16, v[0:3], s[64:65] nt
	s_waitcnt lgkmcnt(2)
	global_store_dwordx4 v17, v[4:7], s[64:65] nt
	s_waitcnt lgkmcnt(1)
	global_store_dwordx4 v18, v[8:11], s[64:65] nt
	s_waitcnt lgkmcnt(0)
	global_store_dwordx4 v19, v[12:15], s[64:65] nt
	s_add_u32 s64, s64, 0x80000
	s_addc_u32 s65, s65, 0
	s_nop 1
	global_load_dwordx4 v[0:3], v136, s[16:17] offset:2048 nt
	global_load_dwordx4 v[4:7], v136, s[18:19] offset:2048 nt
	global_load_dwordx4 v[8:11], v136, s[20:21] offset:2048 nt
	global_load_dwordx4 v[12:15], v136, s[22:23] offset:2048 nt
	global_load_dwordx4 v[16:19], v136, s[24:25] offset:2048 nt
	global_load_dwordx4 v[20:23], v136, s[26:27] offset:2048 nt
	global_load_dwordx4 v[24:27], v136, s[28:29] offset:2048 nt
	global_load_dwordx4 v[28:31], v136, s[30:31] offset:2048 nt
	global_load_dwordx4 v[32:35], v136, s[38:39] offset:2048 nt
	global_load_dwordx4 v[36:39], v136, s[40:41] offset:2048 nt
	global_load_dwordx4 v[40:43], v136, s[42:43] offset:2048 nt
	global_load_dwordx4 v[44:47], v136, s[44:45] offset:2048 nt
	global_load_dwordx4 v[48:51], v136, s[46:47] offset:2048 nt
	global_load_dwordx4 v[52:55], v136, s[48:49] offset:2048 nt
	global_load_dwordx4 v[56:59], v136, s[60:61] offset:2048 nt
	global_load_dwordx4 v[60:63], v136, s[62:63] offset:2048 nt
	s_waitcnt vmcnt(40)
; #define LAS __attribute__((address_space(3)))
; __device__ __forceinline__ unsigned pack4_fp8(float a, float b, float c, float d) { int r = 0; r = __builtin_amdgcn_cvt_pk_fp8_f32(a, b, r, false); r = __builtin_amdgcn_cvt_pk_fp8_f32(c, d, r, true); return (unsigned)r; }
; #define CVT_LDS_BAR() do { asm volatile("s_waitcnt lgkmcnt(0)" ::: "memory"); __builtin_amdgcn_s_barrier(); asm volatile("" ::: "memory"); } while (0)
; __device__ __forceinline__ void cvt8_to_lds(const f32x4 (&v)[16], LAS unsigned char* tile, int lane, int wv) {
; #pragma unroll
;     for (int i = 0; i < 4; ++i) { u32x4 w; w.x = pack4_fp8(v[0][i] * W8_SCALE, v[1][i] * W8_SCALE, v[2][i] * W8_SCALE, v[3][i] * W8_SCALE); w.y = pack4_fp8(v[4][i] * W8_SCALE, v[5][i] * W8_SCALE, v[6][i] * W8_SCALE, v[7][i] * W8_SCALE);
;         w.z = pack4_fp8(v[8][i] * W8_SCALE, v[9][i] * W8_SCALE, v[10][i] * W8_SCALE, v[11][i] * W8_SCALE); w.w = pack4_fp8(v[12][i] * W8_SCALE, v[13][i] * W8_SCALE, v[14][i] * W8_SCALE, v[15][i] * W8_SCALE);
;         *(LAS u32x4*)(tile + (4 * lane + i) * 128 + ((wv ^ (lane & 7)) << 4)) = w; }
; }
; __device__ __forceinline__ void cvt8_from_lds(const LAS unsigned char* tile, fp8_t* d, int ld_dst, int tid) {
;     const int c = tid & 7;
; #pragma unroll
;     for (int q = 0; q < 4; ++q) { const int r = (tid >> 3) + 64 * q; const u32x4 w = *(const LAS u32x4*)(tile + r * 128 + ((c ^ ((r >> 2) & 7)) << 4));
;         __builtin_nontemporal_store(w, (u32x4*)(d + (size_t)r * ld_dst + 16 * c)); }
; __device__ __forceinline__ void cvt_item_lds(const float* src, int ld_src, fp8_t* dst, int ld_dst, LAS unsigned char* lds, int tid, int wv) {
;     ...
;     for (int t = 0; t < 8; t += 2) {
;         cvt8_load(vb, s + (t + 1) * 256, ld_src); __builtin_amdgcn_sched_barrier(0);
;         cvt8_to_lds(va, lds, lane, wv); CVT_LDS_BAR(); __builtin_amdgcn_sched_barrier(0);
;         cvt8_from_lds(lds, dst + (size_t)(t * 256) * ld_dst, ld_dst, tid); __builtin_amdgcn_sched_barrier(0);
;         if (t + 2 < 8) { cvt8_load(va, s + (t + 2) * 256, ld_src); __builtin_amdgcn_sched_barrier(0); }
;         cvt8_to_lds(vb, lds + 32768, lane, wv); CVT_LDS_BAR(); __builtin_amdgcn_sched_barrier(0);
;         cvt8_from_lds(lds + 32768, dst + (size_t)((t + 1) * 256) * ld_dst, ld_dst, tid); __builtin_amdgcn_sched_barrier(0);
	v_mul_f32_e32 v64, 0x42800000, v64
	v_mul_f32_e32 v68, 0x42800000, v68
	v_mul_f32_e32 v72, 0x42800000, v72
	v_mul_f32_e32 v76, 0x42800000, v76
	v_mul_f32_e32 v80, 0x42800000, v80
	v_mul_f32_e32 v84, 0x42800000, v84
	v_mul_f32_e32 v88, 0x42800000, v88
	v_mul_f32_e32 v92, 0x42800000, v92
	v_mul_f32_e32 v96, 0x42800000, v96
	v_mul_f32_e32 v100, 0x42800000, v100
	v_mul_f32_e32 v104, 0x42800000, v104
	v_mul_f32_e32 v108, 0x42800000, v108
	v_mul_f32_e32 v112, 0x42800000, v112
	v_mul_f32_e32 v116, 0x42800000, v116
	v_mul_f32_e32 v120, 0x42800000, v120
	v_mul_f32_e32 v124, 0x42800000, v124
	v_cvt_pk_fp8_f32 v210, v64, v68
	v_cvt_pk_fp8_f32 v211, v80, v84
	v_cvt_pk_fp8_f32 v212, v96, v100
	v_cvt_pk_fp8_f32 v213, v112, v116
	v_cvt_pk_fp8_f32 v210, v72, v76 op_sel:[0,0,1]
	v_cvt_pk_fp8_f32 v211, v88, v92 op_sel:[0,0,1]
	v_cvt_pk_fp8_f32 v212, v104, v108 op_sel:[0,0,1]
	v_cvt_pk_fp8_f32 v213, v120, v124 op_sel:[0,0,1]
	ds_write_b128 v205, v[210:213] offset:0
	v_mul_f32_e32 v65, 0x42800000, v65
	v_mul_f32_e32 v69, 0x42800000, v69
	v_mul_f32_e32 v73, 0x42800000, v73
	v_mul_f32_e32 v77, 0x42800000, v77
	v_mul_f32_e32 v81, 0x42800000, v81
	v_mul_f32_e32 v85, 0x42800000, v85
	v_mul_f32_e32 v89, 0x42800000, v89
	v_mul_f32_e32 v93, 0x42800000, v93
	v_mul_f32_e32 v97, 0x42800000, v97
	v_mul_f32_e32 v101, 0x42800000, v101
	v_mul_f32_e32 v105, 0x42800000, v105
	v_mul_f32_e32 v109, 0x42800000, v109
	v_mul_f32_e32 v113, 0x42800000, v113
	v_mul_f32_e32 v117, 0x42800000, v117
	v_mul_f32_e32 v121, 0x42800000, v121
	v_mul_f32_e32 v125, 0x42800000, v125
	v_cvt_pk_fp8_f32 v210, v65, v69
	v_cvt_pk_fp8_f32 v211, v81, v85
	v_cvt_pk_fp8_f32 v212, v97, v101
	v_cvt_pk_fp8_f32 v213, v113, v117
	v_cvt_pk_fp8_f32 v210, v73, v77 op_sel:[0,0,1]
	v_cvt_pk_fp8_f32 v211, v89, v93 op_sel:[0,0,1]
	v_cvt_pk_fp8_f32 v212, v105, v109 op_sel:[0,0,1]
	v_cvt_pk_fp8_f32 v213, v121, v125 op_sel:[0,0,1]
	ds_write_b128 v205, v[210:213] offset:128
	v_mul_f32_e32 v66, 0x42800000, v66
	v_mul_f32_e32 v70, 0x42800000, v70
	v_mul_f32_e32 v74, 0x42800000, v74
	v_mul_f32_e32 v78, 0x42800000, v78
	v_mul_f32_e32 v82, 0x42800000, v82
	v_mul_f32_e32 v86, 0x42800000, v86
	v_mul_f32_e32 v90, 0x42800000, v90
	v_mul_f32_e32 v94, 0x42800000, v94
	v_mul_f32_e32 v98, 0x42800000, v98
	v_mul_f32_e32 v102, 0x42800000, v102
	v_mul_f32_e32 v106, 0x42800000, v106
	v_mul_f32_e32 v110, 0x42800000, v110
	v_mul_f32_e32 v114, 0x42800000, v114
	v_mul_f32_e32 v118, 0x42800000, v118
	v_mul_f32_e32 v122, 0x42800000, v122
	v_mul_f32_e32 v126, 0x42800000, v126
	v_cvt_pk_fp8_f32 v210, v66, v70
	v_cvt_pk_fp8_f32 v211, v82, v86
	v_cvt_pk_fp8_f32 v212, v98, v102
	v_cvt_pk_fp8_f32 v213, v114, v118
	v_cvt_pk_fp8_f32 v210, v74, v78 op_sel:[0,0,1]
	v_cvt_pk_fp8_f32 v211, v90, v94 op_sel:[0,0,1]
	v_cvt_pk_fp8_f32 v212, v106, v110 op_sel:[0,0,1]
	v_cvt_pk_fp8_f32 v213, v122, v126 op_sel:[0,0,1]
	ds_write_b128 v205, v[210:213] offset:256
	v_mul_f32_e32 v67, 0x42800000, v67
	v_mul_f32_e32 v71, 0x42800000, v71
	v_mul_f32_e32 v75, 0x42800000, v75
	v_mul_f32_e32 v79, 0x42800000, v79
	v_mul_f32_e32 v83, 0x42800000, v83
	v_mul_f32_e32 v87, 0x42800000, v87
	v_mul_f32_e32 v91, 0x42800000, v91
	v_mul_f32_e32 v95, 0x42800000, v95
	v_mul_f32_e32 v99, 0x42800000, v99
	v_mul_f32_e32 v103, 0x42800000, v103
	v_mul_f32_e32 v107, 0x42800000, v107
	v_mul_f32_e32 v111, 0x42800000, v111
	v_mul_f32_e32 v115, 0x42800000, v115
	v_mul_f32_e32 v119, 0x42800000, v119
	v_mul_f32_e32 v123, 0x42800000, v123
	v_mul_f32_e32 v127, 0x42800000, v127
	v_cvt_pk_fp8_f32 v210, v67, v71
	v_cvt_pk_fp8_f32 v211, v83, v87
	v_cvt_pk_fp8_f32 v212, v99, v103
	v_cvt_pk_fp8_f32 v213, v115, v119
	v_cvt_pk_fp8_f32 v210, v75, v79 op_sel:[0,0,1]
	v_cvt_pk_fp8_f32 v211, v91, v95 op_sel:[0,0,1]
	v_cvt_pk_fp8_f32 v212, v107, v111 op_sel:[0,0,1]
	v_cvt_pk_fp8_f32 v213, v123, v127 op_sel:[0,0,1]
	ds_write_b128 v205, v[210:213] offset:384
	s_waitcnt lgkmcnt(0)
	s_barrier
	ds_read_b128 v[64:67], v206
	ds_read_b128 v[68:71], v207
	ds_read_b128 v[72:75], v208
	ds_read_b128 v[76:79], v209
	v_add_u32_e32 v80, v140, v138
	v_add_u32_e32 v81, v142, v138
	v_add_u32_e32 v82, v144, v138
	v_add_u32_e32 v83, v146, v138
	s_waitcnt lgkmcnt(3)
	global_store_dwordx4 v80, v[64:67], s[64:65] nt
	s_waitcnt lgkmcnt(2)
	global_store_dwordx4 v81, v[68:71], s[64:65] nt
	s_waitcnt lgkmcnt(1)
	global_store_dwordx4 v82, v[72:75], s[64:65] nt
	s_waitcnt lgkmcnt(0)
	global_store_dwordx4 v83, v[76:79], s[64:65] nt
	s_add_u32 s64, s64, 0x80000
	s_addc_u32 s65, s65, 0
	s_nop 1
	global_load_dwordx4 v[64:67], v136, s[16:17] offset:3072 nt
	global_load_dwordx4 v[68:71], v136, s[18:19] offset:3072 nt
	global_load_dwordx4 v[72:75], v136, s[20:21] offset:3072 nt
	global_load_dwordx4 v[76:79], v136, s[22:23] offset:3072 nt
	global_load_dwordx4 v[80:83], v136, s[24:25] offset:3072 nt
	global_load_dwordx4 v[84:87], v136, s[26:27] offset:3072 nt
	global_load_dwordx4 v[88:91], v136, s[28:29] offset:3072 nt
	global_load_dwordx4 v[92:95], v136, s[30:31] offset:3072 nt
	global_load_dwordx4 v[96:99], v136, s[38:39] offset:3072 nt
	global_load_dwordx4 v[100:103], v136, s[40:41] offset:3072 nt
	global_load_dwordx4 v[104:107], v136, s[42:43] offset:3072 nt
	global_load_dwordx4 v[108:111], v136, s[44:45] offset:3072 nt
	global_load_dwordx4 v[112:115], v136, s[46:47] offset:3072 nt
	global_load_dwordx4 v[116:119], v136, s[48:49] offset:3072 nt
	global_load_dwordx4 v[120:123], v136, s[60:61] offset:3072 nt
	global_load_dwordx4 v[124:127], v136, s[62:63] offset:3072 nt
	s_waitcnt vmcnt(40)
; #define LAS __attribute__((address_space(3)))
; __device__ __forceinline__ unsigned pack4_fp8(float a, float b, float c, float d) { int r = 0; r = __builtin_amdgcn_cvt_pk_fp8_f32(a, b, r, false); r = __builtin_amdgcn_cvt_pk_fp8_f32(c, d, r, true); return (unsigned)r; }
; #define CVT_LDS_BAR() do { asm volatile("s_waitcnt lgkmcnt(0)" ::: "memory"); __builtin_amdgcn_s_barrier(); asm volatile("" ::: "memory"); } while (0)
; __device__ __forceinline__ void cvt8_to_lds(const f32x4 (&v)[16], LAS unsigned char* tile, int lane, int wv) {
; #pragma unroll
;     for (int i = 0; i < 4; ++i) { u32x4 w; w.x = pack4_fp8(v[0][i] * W8_SCALE, v[1][i] * W8_SCALE, v[2][i] * W8_SCALE, v[3][i] * W8_SCALE); w.y = pack4_fp8(v[4][i] * W8_SCALE, v[5][i] * W8_SCALE, v[6][i] * W8_SCALE, v[7][i] * W8_SCALE);
;         w.z = pack4_fp8(v[8][i] * W8_SCALE, v[9][i] * W8_SCALE, v[10][i] * W8_SCALE, v[11][i] * W8_SCALE); w.w = pack4_fp8(v[12][i] * W8_SCALE, v[13][i] * W8_SCALE, v[14][i] * W8_SCALE, v[15][i] * W8_SCALE);
;         *(LAS u32x4*)(tile + (4 * lane + i) * 128 + ((wv ^ (lane & 7)) << 4)) = w; }
; }
; __device__ __forceinline__ void cvt8_from_lds(const LAS unsigned char* tile, fp8_t* d, int ld_dst, int tid) {
;     const int c = tid & 7;
; #pragma unroll
;     for (int q = 0; q < 4; ++q) { const int r = (tid >> 3) + 64 * q; const u32x4 w = *(const LAS u32x4*)(tile + r * 128 + ((c ^ ((r >> 2) & 7)) << 4));
;         __builtin_nontemporal_store(w, (u32x4*)(d + (size_t)r * ld_dst + 16 * c)); }
; __device__ __forceinline__ void cvt_item_lds(const float* src, int ld_src, fp8_t* dst, int ld_dst, LAS unsigned char* lds, int tid, int wv) {
;     ...
;     for (int t = 0; t < 8; t += 2) {
;         cvt8_load(vb, s + (t + 1) * 256, ld_src); __builtin_amdgcn_sched_barrier(0);
;         cvt8_to_lds(va, lds, lane, wv); CVT_LDS_BAR(); __builtin_amdgcn_sched_barrier(0);
;         cvt8_from_lds(lds, dst + (size_t)(t * 256) * ld_dst, ld_dst, tid); __builtin_amdgcn_sched_barrier(0);
;         if (t + 2 < 8) { cvt8_load(va, s + (t + 2) * 256, ld_src); __builtin_amdgcn_sched_barrier(0); }
;         cvt8_to_lds(vb, lds + 32768, lane, wv); CVT_LDS_BAR(); __builtin_amdgcn_sched_barrier(0);
	v_mul_f32_e32 v128, 0x42800000, v128
	v_mul_f32_e32 v132, 0x42800000, v132
	v_mul_f32_e32 v148, 0x42800000, v148
	v_mul_f32_e32 v152, 0x42800000, v152
	v_mul_f32_e32 v156, 0x42800000, v156
	v_mul_f32_e32 v160, 0x42800000, v160
	v_mul_f32_e32 v164, 0x42800000, v164
	v_mul_f32_e32 v168, 0x42800000, v168
	v_mul_f32_e32 v172, 0x42800000, v172
	v_mul_f32_e32 v176, 0x42800000, v176
	v_mul_f32_e32 v180, 0x42800000, v180
	v_mul_f32_e32 v184, 0x42800000, v184
	v_mul_f32_e32 v188, 0x42800000, v188
	v_mul_f32_e32 v192, 0x42800000, v192
	v_mul_f32_e32 v196, 0x42800000, v196
	v_mul_f32_e32 v200, 0x42800000, v200
	v_cvt_pk_fp8_f32 v210, v128, v132
	v_cvt_pk_fp8_f32 v211, v156, v160
	v_cvt_pk_fp8_f32 v212, v172, v176
	v_cvt_pk_fp8_f32 v213, v188, v192
	v_cvt_pk_fp8_f32 v210, v148, v152 op_sel:[0,0,1]
	v_cvt_pk_fp8_f32 v211, v164, v168 op_sel:[0,0,1]
	v_cvt_pk_fp8_f32 v212, v180, v184 op_sel:[0,0,1]
	v_cvt_pk_fp8_f32 v213, v196, v200 op_sel:[0,0,1]
	ds_write_b128 v205, v[210:213] offset:32768
	v_mul_f32_e32 v129, 0x42800000, v129
	v_mul_f32_e32 v133, 0x42800000, v133
	v_mul_f32_e32 v149, 0x42800000, v149
	v_mul_f32_e32 v153, 0x42800000, v153
	v_mul_f32_e32 v157, 0x42800000, v157
	v_mul_f32_e32 v161, 0x42800000, v161
	v_mul_f32_e32 v165, 0x42800000, v165
	v_mul_f32_e32 v169, 0x42800000, v169
	v_mul_f32_e32 v173, 0x42800000, v173
	v_mul_f32_e32 v177, 0x42800000, v177
	v_mul_f32_e32 v181, 0x42800000, v181
	v_mul_f32_e32 v185, 0x42800000, v185
	v_mul_f32_e32 v189, 0x42800000, v189
	v_mul_f32_e32 v193, 0x42800000, v193
	v_mul_f32_e32 v197, 0x42800000, v197
	v_mul_f32_e32 v201, 0x42800000, v201
	v_cvt_pk_fp8_f32 v210, v129, v133
	v_cvt_pk_fp8_f32 v211, v157, v161
	v_cvt_pk_fp8_f32 v212, v173, v177
	v_cvt_pk_fp8_f32 v213, v189, v193
	v_cvt_pk_fp8_f32 v210, v149, v153 op_sel:[0,0,1]
	v_cvt_pk_fp8_f32 v211, v165, v169 op_sel:[0,0,1]
	v_cvt_pk_fp8_f32 v212, v181, v185 op_sel:[0,0,1]
	v_cvt_pk_fp8_f32 v213, v197, v201 op_sel:[0,0,1]
	ds_write_b128 v205, v[210:213] offset:32896
	v_mul_f32_e32 v130, 0x42800000, v130
	v_mul_f32_e32 v134, 0x42800000, v134
	v_mul_f32_e32 v150, 0x42800000, v150
	v_mul_f32_e32 v154, 0x42800000, v154
	v_mul_f32_e32 v158, 0x42800000, v158
	v_mul_f32_e32 v162, 0x42800000, v162
	v_mul_f32_e32 v166, 0x42800000, v166
	v_mul_f32_e32 v170, 0x42800000, v170
	v_mul_f32_e32 v174, 0x42800000, v174
	v_mul_f32_e32 v178, 0x42800000, v178
	v_mul_f32_e32 v182, 0x42800000, v182
	v_mul_f32_e32 v186, 0x42800000, v186
	v_mul_f32_e32 v190, 0x42800000, v190
	v_mul_f32_e32 v194, 0x42800000, v194
	v_mul_f32_e32 v198, 0x42800000, v198
	v_mul_f32_e32 v202, 0x42800000, v202
	v_cvt_pk_fp8_f32 v210, v130, v134
	v_cvt_pk_fp8_f32 v211, v158, v162
	v_cvt_pk_fp8_f32 v212, v174, v178
	v_cvt_pk_fp8_f32 v213, v190, v194
	v_cvt_pk_fp8_f32 v210, v150, v154 op_sel:[0,0,1]
	v_cvt_pk_fp8_f32 v211, v166, v170 op_sel:[0,0,1]
	v_cvt_pk_fp8_f32 v212, v182, v186 op_sel:[0,0,1]
	v_cvt_pk_fp8_f32 v213, v198, v202 op_sel:[0,0,1]
	ds_write_b128 v205, v[210:213] offset:33024
	v_mul_f32_e32 v131, 0x42800000, v131
	v_mul_f32_e32 v135, 0x42800000, v135
	v_mul_f32_e32 v151, 0x42800000, v151
	v_mul_f32_e32 v155, 0x42800000, v155
	v_mul_f32_e32 v159, 0x42800000, v159
	v_mul_f32_e32 v163, 0x42800000, v163
	v_mul_f32_e32 v167, 0x42800000, v167
	v_mul_f32_e32 v171, 0x42800000, v171
	v_mul_f32_e32 v175, 0x42800000, v175
	v_mul_f32_e32 v179, 0x42800000, v179
	v_mul_f32_e32 v183, 0x42800000, v183
	v_mul_f32_e32 v187, 0x42800000, v187
	v_mul_f32_e32 v191, 0x42800000, v191
	v_mul_f32_e32 v195, 0x42800000, v195
	v_mul_f32_e32 v199, 0x42800000, v199
	v_mul_f32_e32 v203, 0x42800000, v203
	v_cvt_pk_fp8_f32 v210, v131, v135
	v_cvt_pk_fp8_f32 v211, v159, v163
	v_cvt_pk_fp8_f32 v212, v175, v179
	v_cvt_pk_fp8_f32 v213, v191, v195
	v_cvt_pk_fp8_f32 v210, v151, v155 op_sel:[0,0,1]
	v_cvt_pk_fp8_f32 v211, v167, v171 op_sel:[0,0,1]
	v_cvt_pk_fp8_f32 v212, v183, v187 op_sel:[0,0,1]
	v_cvt_pk_fp8_f32 v213, v199, v203 op_sel:[0,0,1]
	ds_write_b128 v205, v[210:213] offset:33152
	s_waitcnt lgkmcnt(0)
	s_barrier
	ds_read_b128 v[128:131], v206 offset:32768
	ds_read_b128 v[132:135], v207 offset:32768
	ds_read_b128 v[148:151], v208 offset:32768
	ds_read_b128 v[152:155], v209 offset:32768
	v_add_u32_e32 v156, v140, v138
	v_add_u32_e32 v157, v142, v138
	v_add_u32_e32 v158, v144, v138
	v_add_u32_e32 v159, v146, v138
	s_waitcnt lgkmcnt(3)
	global_store_dwordx4 v156, v[128:131], s[64:65] nt
	s_waitcnt lgkmcnt(2)
	global_store_dwordx4 v157, v[132:135], s[64:65] nt
	s_waitcnt lgkmcnt(1)
	global_store_dwordx4 v158, v[148:151], s[64:65] nt
	s_waitcnt lgkmcnt(0)
	global_store_dwordx4 v159, v[152:155], s[64:65] nt
	s_add_u32 s64, s64, 0x80000
	s_addc_u32 s65, s65, 0
	s_waitcnt vmcnt(24)
; #define LAS __attribute__((address_space(3)))
; __device__ __forceinline__ unsigned pack4_fp8(float a, float b, float c, float d) { int r = 0; r = __builtin_amdgcn_cvt_pk_fp8_f32(a, b, r, false); r = __builtin_amdgcn_cvt_pk_fp8_f32(c, d, r, true); return (unsigned)r; }
; #define CVT_LDS_BAR() do { asm volatile("s_waitcnt lgkmcnt(0)" ::: "memory"); __builtin_amdgcn_s_barrier(); asm volatile("" ::: "memory"); } while (0)
; __device__ __forceinline__ void cvt8_to_lds(const f32x4 (&v)[16], LAS unsigned char* tile, int lane, int wv) {
; #pragma unroll
;     for (int i = 0; i < 4; ++i) { u32x4 w; w.x = pack4_fp8(v[0][i] * W8_SCALE, v[1][i] * W8_SCALE, v[2][i] * W8_SCALE, v[3][i] * W8_SCALE); w.y = pack4_fp8(v[4][i] * W8_SCALE, v[5][i] * W8_SCALE, v[6][i] * W8_SCALE, v[7][i] * W8_SCALE);
;         w.z = pack4_fp8(v[8][i] * W8_SCALE, v[9][i] * W8_SCALE, v[10][i] * W8_SCALE, v[11][i] * W8_SCALE); w.w = pack4_fp8(v[12][i] * W8_SCALE, v[13][i] * W8_SCALE, v[14][i] * W8_SCALE, v[15][i] * W8_SCALE);
;         *(LAS u32x4*)(tile + (4 * lane + i) * 128 + ((wv ^ (lane & 7)) << 4)) = w; }
; __device__ __forceinline__ void cvt_item_lds(const float* src, int ld_src, fp8_t* dst, int ld_dst, LAS unsigned char* lds, int tid, int wv) {
;     ...
;     for (int t = 0; t < 8; t += 2) {
;         cvt8_load(vb, s + (t + 1) * 256, ld_src); __builtin_amdgcn_sched_barrier(0);
;         cvt8_to_lds(va, lds, lane, wv); CVT_LDS_BAR(); __builtin_amdgcn_sched_barrier(0);
;         cvt8_from_lds(lds, dst + (size_t)(t * 256) * ld_dst, ld_dst, tid); __builtin_amdgcn_sched_barrier(0);
;         if (t + 2 < 8) { cvt8_load(va, s + (t + 2) * 256, ld_src); __builtin_amdgcn_sched_barrier(0); }
;         cvt8_to_lds(vb, lds + 32768, lane, wv); CVT_LDS_BAR(); __builtin_amdgcn_sched_barrier(0);
	v_mul_f32_e32 v0, 0x42800000, v0
	v_mul_f32_e32 v4, 0x42800000, v4
	v_mul_f32_e32 v8, 0x42800000, v8
	v_mul_f32_e32 v12, 0x42800000, v12
	v_mul_f32_e32 v16, 0x42800000, v16
	v_mul_f32_e32 v20, 0x42800000, v20
	v_mul_f32_e32 v24, 0x42800000, v24
	v_mul_f32_e32 v28, 0x42800000, v28
	v_mul_f32_e32 v32, 0x42800000, v32
	v_mul_f32_e32 v36, 0x42800000, v36
	v_mul_f32_e32 v40, 0x42800000, v40
	v_mul_f32_e32 v44, 0x42800000, v44
	v_mul_f32_e32 v48, 0x42800000, v48
	v_mul_f32_e32 v52, 0x42800000, v52
	v_mul_f32_e32 v56, 0x42800000, v56
	v_mul_f32_e32 v60, 0x42800000, v60
	v_cvt_pk_fp8_f32 v210, v0, v4
	v_cvt_pk_fp8_f32 v211, v16, v20
	v_cvt_pk_fp8_f32 v212, v32, v36
	v_cvt_pk_fp8_f32 v213, v48, v52
	v_cvt_pk_fp8_f32 v210, v8, v12 op_sel:[0,0,1]
	v_cvt_pk_fp8_f32 v211, v24, v28 op_sel:[0,0,1]
	v_cvt_pk_fp8_f32 v212, v40, v44 op_sel:[0,0,1]
	v_cvt_pk_fp8_f32 v213, v56, v60 op_sel:[0,0,1]
	ds_write_b128 v205, v[210:213] offset:0
	v_mul_f32_e32 v1, 0x42800000, v1
	v_mul_f32_e32 v5, 0x42800000, v5
	v_mul_f32_e32 v9, 0x42800000, v9
	v_mul_f32_e32 v13, 0x42800000, v13
	v_mul_f32_e32 v17, 0x42800000, v17
	v_mul_f32_e32 v21, 0x42800000, v21
	v_mul_f32_e32 v25, 0x42800000, v25
	v_mul_f32_e32 v29, 0x42800000, v29
	v_mul_f32_e32 v33, 0x42800000, v33
	v_mul_f32_e32 v37, 0x42800000, v37
	v_mul_f32_e32 v41, 0x42800000, v41
	v_mul_f32_e32 v45, 0x42800000, v45
	v_mul_f32_e32 v49, 0x42800000, v49
	v_mul_f32_e32 v53, 0x42800000, v53
	v_mul_f32_e32 v57, 0x42800000, v57
	v_mul_f32_e32 v61, 0x42800000, v61
	v_cvt_pk_fp8_f32 v210, v1, v5
	v_cvt_pk_fp8_f32 v211, v17, v21
	v_cvt_pk_fp8_f32 v212, v33, v37
	v_cvt_pk_fp8_f32 v213, v49, v53
	v_cvt_pk_fp8_f32 v210, v9, v13 op_sel:[0,0,1]
	v_cvt_pk_fp8_f32 v211, v25, v29 op_sel:[0,0,1]
	v_cvt_pk_fp8_f32 v212, v41, v45 op_sel:[0,0,1]
	v_cvt_pk_fp8_f32 v213, v57, v61 op_sel:[0,0,1]
	ds_write_b128 v205, v[210:213] offset:128
	v_mul_f32_e32 v2, 0x42800000, v2
	v_mul_f32_e32 v6, 0x42800000, v6
	v_mul_f32_e32 v10, 0x42800000, v10
	v_mul_f32_e32 v14, 0x42800000, v14
	v_mul_f32_e32 v18, 0x42800000, v18
	v_mul_f32_e32 v22, 0x42800000, v22
	v_mul_f32_e32 v26, 0x42800000, v26
	v_mul_f32_e32 v30, 0x42800000, v30
	v_mul_f32_e32 v34, 0x42800000, v34
	v_mul_f32_e32 v38, 0x42800000, v38
	v_mul_f32_e32 v42, 0x42800000, v42
	v_mul_f32_e32 v46, 0x42800000, v46
	v_mul_f32_e32 v50, 0x42800000, v50
	v_mul_f32_e32 v54, 0x42800000, v54
	v_mul_f32_e32 v58, 0x42800000, v58
	v_mul_f32_e32 v62, 0x42800000, v62
	v_cvt_pk_fp8_f32 v210, v2, v6
	v_cvt_pk_fp8_f32 v211, v18, v22
	v_cvt_pk_fp8_f32 v212, v34, v38
	v_cvt_pk_fp8_f32 v213, v50, v54
	v_cvt_pk_fp8_f32 v210, v10, v14 op_sel:[0,0,1]
	v_cvt_pk_fp8_f32 v211, v26, v30 op_sel:[0,0,1]
	v_cvt_pk_fp8_f32 v212, v42, v46 op_sel:[0,0,1]
	v_cvt_pk_fp8_f32 v213, v58, v62 op_sel:[0,0,1]
	ds_write_b128 v205, v[210:213] offset:256
	v_mul_f32_e32 v3, 0x42800000, v3
	v_mul_f32_e32 v7, 0x42800000, v7
	v_mul_f32_e32 v11, 0x42800000, v11
	v_mul_f32_e32 v15, 0x42800000, v15
	v_mul_f32_e32 v19, 0x42800000, v19
	v_mul_f32_e32 v23, 0x42800000, v23
	v_mul_f32_e32 v27, 0x42800000, v27
	v_mul_f32_e32 v31, 0x42800000, v31
	v_mul_f32_e32 v35, 0x42800000, v35
	v_mul_f32_e32 v39, 0x42800000, v39
	v_mul_f32_e32 v43, 0x42800000, v43
	v_mul_f32_e32 v47, 0x42800000, v47
	v_mul_f32_e32 v51, 0x42800000, v51
	v_mul_f32_e32 v55, 0x42800000, v55
	v_mul_f32_e32 v59, 0x42800000, v59
	v_mul_f32_e32 v63, 0x42800000, v63
	v_cvt_pk_fp8_f32 v210, v3, v7
	v_cvt_pk_fp8_f32 v211, v19, v23
	v_cvt_pk_fp8_f32 v212, v35, v39
	v_cvt_pk_fp8_f32 v213, v51, v55
	v_cvt_pk_fp8_f32 v210, v11, v15 op_sel:[0,0,1]
	v_cvt_pk_fp8_f32 v211, v27, v31 op_sel:[0,0,1]
	v_cvt_pk_fp8_f32 v212, v43, v47 op_sel:[0,0,1]
	v_cvt_pk_fp8_f32 v213, v59, v63 op_sel:[0,0,1]
	ds_write_b128 v205, v[210:213] offset:384
	s_waitcnt lgkmcnt(0)
	s_barrier
; #define LAS __attribute__((address_space(3)))
; __device__ __forceinline__ unsigned pack4_fp8(float a, float b, float c, float d) { int r = 0; r = __builtin_amdgcn_cvt_pk_fp8_f32(a, b, r, false); r = __builtin_amdgcn_cvt_pk_fp8_f32(c, d, r, true); return (unsigned)r; }
; #define CVT_LDS_BAR() do { asm volatile("s_waitcnt lgkmcnt(0)" ::: "memory"); __builtin_amdgcn_s_barrier(); asm volatile("" ::: "memory"); } while (0)
; __device__ __forceinline__ void cvt8_to_lds(const f32x4 (&v)[16], LAS unsigned char* tile, int lane, int wv) {
; #pragma unroll
;     for (int i = 0; i < 4; ++i) { u32x4 w; w.x = pack4_fp8(v[0][i] * W8_SCALE, v[1][i] * W8_SCALE, v[2][i] * W8_SCALE, v[3][i] * W8_SCALE); w.y = pack4_fp8(v[4][i] * W8_SCALE, v[5][i] * W8_SCALE, v[6][i] * W8_SCALE, v[7][i] * W8_SCALE);
;         w.z = pack4_fp8(v[8][i] * W8_SCALE, v[9][i] * W8_SCALE, v[10][i] * W8_SCALE, v[11][i] * W8_SCALE); w.w = pack4_fp8(v[12][i] * W8_SCALE, v[13][i] * W8_SCALE, v[14][i] * W8_SCALE, v[15][i] * W8_SCALE);
;         *(LAS u32x4*)(tile + (4 * lane + i) * 128 + ((wv ^ (lane & 7)) << 4)) = w; }
; }
; __device__ __forceinline__ void cvt8_from_lds(const LAS unsigned char* tile, fp8_t* d, int ld_dst, int tid) {
;     const int c = tid & 7;
; #pragma unroll
;     for (int q = 0; q < 4; ++q) { const int r = (tid >> 3) + 64 * q; const u32x4 w = *(const LAS u32x4*)(tile + r * 128 + ((c ^ ((r >> 2) & 7)) << 4));
;         __builtin_nontemporal_store(w, (u32x4*)(d + (size_t)r * ld_dst + 16 * c)); }
; __device__ __forceinline__ void cvt_item_lds(const float* src, int ld_src, fp8_t* dst, int ld_dst, LAS unsigned char* lds, int tid, int wv) {
;     ...
;         cvt8_to_lds(vb, lds + 32768, lane, wv); CVT_LDS_BAR(); __builtin_amdgcn_sched_barrier(0);
;         cvt8_from_lds(lds + 32768, dst + (size_t)((t + 1) * 256) * ld_dst, ld_dst, tid); __builtin_amdgcn_sched_barrier(0);
;     }
	ds_read_b128 v[0:3], v206
	ds_read_b128 v[4:7], v207
	ds_read_b128 v[8:11], v208
	ds_read_b128 v[12:15], v209
	v_add_u32_e32 v16, v140, v138
	v_add_u32_e32 v17, v142, v138
	v_add_u32_e32 v18, v144, v138
	v_add_u32_e32 v19, v146, v138
	s_waitcnt lgkmcnt(3)
	global_store_dwordx4 v16, v[0:3], s[64:65] nt
	s_waitcnt lgkmcnt(2)
	global_store_dwordx4 v17, v[4:7], s[64:65] nt
	s_waitcnt lgkmcnt(1)
	global_store_dwordx4 v18, v[8:11], s[64:65] nt
	s_waitcnt lgkmcnt(0)
	global_store_dwordx4 v19, v[12:15], s[64:65] nt
	s_add_u32 s64, s64, 0x80000
	s_addc_u32 s65, s65, 0
	s_waitcnt vmcnt(8)
	v_mul_f32_e32 v64, 0x42800000, v64
	v_mul_f32_e32 v68, 0x42800000, v68
	v_mul_f32_e32 v72, 0x42800000, v72
	v_mul_f32_e32 v76, 0x42800000, v76
	v_mul_f32_e32 v80, 0x42800000, v80
	v_mul_f32_e32 v84, 0x42800000, v84
	v_mul_f32_e32 v88, 0x42800000, v88
	v_mul_f32_e32 v92, 0x42800000, v92
	v_mul_f32_e32 v96, 0x42800000, v96
	v_mul_f32_e32 v100, 0x42800000, v100
	v_mul_f32_e32 v104, 0x42800000, v104
	v_mul_f32_e32 v108, 0x42800000, v108
	v_mul_f32_e32 v112, 0x42800000, v112
	v_mul_f32_e32 v116, 0x42800000, v116
	v_mul_f32_e32 v120, 0x42800000, v120
	v_mul_f32_e32 v124, 0x42800000, v124
	v_cvt_pk_fp8_f32 v210, v64, v68
	v_cvt_pk_fp8_f32 v211, v80, v84
	v_cvt_pk_fp8_f32 v212, v96, v100
	v_cvt_pk_fp8_f32 v213, v112, v116
	v_cvt_pk_fp8_f32 v210, v72, v76 op_sel:[0,0,1]
	v_cvt_pk_fp8_f32 v211, v88, v92 op_sel:[0,0,1]
	v_cvt_pk_fp8_f32 v212, v104, v108 op_sel:[0,0,1]
	v_cvt_pk_fp8_f32 v213, v120, v124 op_sel:[0,0,1]
	ds_write_b128 v205, v[210:213] offset:32768
	v_mul_f32_e32 v65, 0x42800000, v65
	v_mul_f32_e32 v69, 0x42800000, v69
	v_mul_f32_e32 v73, 0x42800000, v73
	v_mul_f32_e32 v77, 0x42800000, v77
	v_mul_f32_e32 v81, 0x42800000, v81
	v_mul_f32_e32 v85, 0x42800000, v85
	v_mul_f32_e32 v89, 0x42800000, v89
	v_mul_f32_e32 v93, 0x42800000, v93
	v_mul_f32_e32 v97, 0x42800000, v97
	v_mul_f32_e32 v101, 0x42800000, v101
	v_mul_f32_e32 v105, 0x42800000, v105
	v_mul_f32_e32 v109, 0x42800000, v109
	v_mul_f32_e32 v113, 0x42800000, v113
	v_mul_f32_e32 v117, 0x42800000, v117
	v_mul_f32_e32 v121, 0x42800000, v121
	v_mul_f32_e32 v125, 0x42800000, v125
	v_cvt_pk_fp8_f32 v210, v65, v69
	v_cvt_pk_fp8_f32 v211, v81, v85
	v_cvt_pk_fp8_f32 v212, v97, v101
	v_cvt_pk_fp8_f32 v213, v113, v117
	v_cvt_pk_fp8_f32 v210, v73, v77 op_sel:[0,0,1]
	v_cvt_pk_fp8_f32 v211, v89, v93 op_sel:[0,0,1]
	v_cvt_pk_fp8_f32 v212, v105, v109 op_sel:[0,0,1]
	v_cvt_pk_fp8_f32 v213, v121, v125 op_sel:[0,0,1]
	ds_write_b128 v205, v[210:213] offset:32896
	v_mul_f32_e32 v66, 0x42800000, v66
	v_mul_f32_e32 v70, 0x42800000, v70
	v_mul_f32_e32 v74, 0x42800000, v74
	v_mul_f32_e32 v78, 0x42800000, v78
	v_mul_f32_e32 v82, 0x42800000, v82
	v_mul_f32_e32 v86, 0x42800000, v86
	v_mul_f32_e32 v90, 0x42800000, v90
	v_mul_f32_e32 v94, 0x42800000, v94
	v_mul_f32_e32 v98, 0x42800000, v98
	v_mul_f32_e32 v102, 0x42800000, v102
	v_mul_f32_e32 v106, 0x42800000, v106
	v_mul_f32_e32 v110, 0x42800000, v110
	v_mul_f32_e32 v114, 0x42800000, v114
	v_mul_f32_e32 v118, 0x42800000, v118
	v_mul_f32_e32 v122, 0x42800000, v122
	v_mul_f32_e32 v126, 0x42800000, v126
	v_cvt_pk_fp8_f32 v210, v66, v70
	v_cvt_pk_fp8_f32 v211, v82, v86
	v_cvt_pk_fp8_f32 v212, v98, v102
	v_cvt_pk_fp8_f32 v213, v114, v118
	v_cvt_pk_fp8_f32 v210, v74, v78 op_sel:[0,0,1]
	v_cvt_pk_fp8_f32 v211, v90, v94 op_sel:[0,0,1]
	v_cvt_pk_fp8_f32 v212, v106, v110 op_sel:[0,0,1]
	v_cvt_pk_fp8_f32 v213, v122, v126 op_sel:[0,0,1]
	ds_write_b128 v205, v[210:213] offset:33024
	v_mul_f32_e32 v67, 0x42800000, v67
	v_mul_f32_e32 v71, 0x42800000, v71
	v_mul_f32_e32 v75, 0x42800000, v75
	v_mul_f32_e32 v79, 0x42800000, v79
	v_mul_f32_e32 v83, 0x42800000, v83
	v_mul_f32_e32 v87, 0x42800000, v87
	v_mul_f32_e32 v91, 0x42800000, v91
	v_mul_f32_e32 v95, 0x42800000, v95
	v_mul_f32_e32 v99, 0x42800000, v99
	v_mul_f32_e32 v103, 0x42800000, v103
	v_mul_f32_e32 v107, 0x42800000, v107
	v_mul_f32_e32 v111, 0x42800000, v111
	v_mul_f32_e32 v115, 0x42800000, v115
	v_mul_f32_e32 v119, 0x42800000, v119
	v_mul_f32_e32 v123, 0x42800000, v123
	v_mul_f32_e32 v127, 0x42800000, v127
	v_cvt_pk_fp8_f32 v210, v67, v71
	v_cvt_pk_fp8_f32 v211, v83, v87
	v_cvt_pk_fp8_f32 v212, v99, v103
	v_cvt_pk_fp8_f32 v213, v115, v119
	v_cvt_pk_fp8_f32 v210, v75, v79 op_sel:[0,0,1]
	v_cvt_pk_fp8_f32 v211, v91, v95 op_sel:[0,0,1]
	v_cvt_pk_fp8_f32 v212, v107, v111 op_sel:[0,0,1]
	v_cvt_pk_fp8_f32 v213, v123, v127 op_sel:[0,0,1]
	ds_write_b128 v205, v[210:213] offset:33152
	s_waitcnt lgkmcnt(0)
	s_barrier
	ds_read_b128 v[64:67], v206 offset:32768
	ds_read_b128 v[68:71], v207 offset:32768
	ds_read_b128 v[72:75], v208 offset:32768
	ds_read_b128 v[76:79], v209 offset:32768
	v_add_u32_e32 v80, v140, v138
	v_add_u32_e32 v81, v142, v138
	v_add_u32_e32 v82, v144, v138
	v_add_u32_e32 v83, v146, v138
	s_waitcnt lgkmcnt(3)
	global_store_dwordx4 v80, v[64:67], s[64:65] nt
	s_waitcnt lgkmcnt(2)
	global_store_dwordx4 v81, v[68:71], s[64:65] nt
	s_waitcnt lgkmcnt(1)
	global_store_dwordx4 v82, v[72:75], s[64:65] nt
	s_waitcnt lgkmcnt(0)
	global_store_dwordx4 v83, v[76:79], s[64:65] nt
	s_mov_b64 s[50:51], 0

; #define PG8_STAGE(bufoff, rs, soff, voff) do { _Pragma("unroll") for (int _i = 0; _i < 2; ++_i) \
;         __builtin_amdgcn_raw_ptr_buffer_load_lds(rs, (LAS void*)(lds + (bufoff) + ldsw + _i * 8192), 16, (voff), (soff) + _i * ((&(voff) == &voffA) ? pieceA : pieceB), 0, 0); } while (0)
; #define PG8_WAIT_V(n) asm volatile("s_waitcnt vmcnt(" #n ")" ::: "memory")
; #define PG8_BAR __builtin_amdgcn_s_barrier()
; template <class Epi, class Sched, bool FP8 = false>
; __device__ __forceinline__ void gemm_phase(LAS unsigned char* lds, const Gemm g, const Sched& S, const Epi& E, const int wave) {
;     ...
;     Unit cur, nxt; int ui = 0;
;     if (!S.next(0, cur)) return;
;     f32x4 acc[2][2][4][2];
; #pragma unroll
;     for (int a = 0; a < 2; ++a)
; #pragma unroll
;         for (int b = 0; b < 2; ++b)
; #pragma unroll
;             for (int m = 0; m < 4; ++m)
; #pragma unroll
;                 for (int n = 0; n < 2; ++n) acc[a][b][m][n] = (f32x4){0.f, 0.f, 0.f, 0.f};
;     bf16x8 At[4][2], B0[2][2], B1[2][2];
;     unsigned cA = cur.aoff, cB = cur.boff;
;     PG8_STAGE(PG8_SB(0, 0), rsB, cB, voffB); PG8_STAGE(PG8_SA(0, 0), rsA, cA, voffA); PG8_STAGE(PG8_SB(0, 1), rsB, cB + hstepB, voffB); PG8_STAGE(PG8_SA(0, 1), rsA, cA + hstepA, voffA);
;     if (wr == 1) PG8_BAR;
;     PG8_WAIT_V(4); PG8_BAR;
;     PG8_STAGE(PG8_SB(1, 0), rsB, cB + kstep, voffB); PG8_STAGE(PG8_SA(1, 0), rsA, cA + kstep, voffA); PG8_STAGE(PG8_SB(1, 1), rsB, cB + hstepB + kstep, voffB);
;     PG8_WAIT_V(6); PG8_BAR;
;     __device__ bool next(int i, Unit& u) const {
;         const int L = i * (G - ncv) + (c - ncv); if (c < ncv || L >= ntiles * nN) return false;
;         u.pm = __builtin_amdgcn_readfirstlane((int)tile_e[L / nN]); u.pn = L % nN; u.e = u.pm >> 5;
;         u.aoff = (unsigned)((size_t)u.pm * a_tile); u.boff = (unsigned)((size_t)u.e * b_expert + (size_t)u.pn * b_tile); return true;
.LBB0_1257:
	v_mbcnt_lo_u32_b32 v0, -1, 0
	v_mbcnt_hi_u32_b32 v0, -1, v0
	s_mov_b32 s4, s86
	v_add_u32_e32 v1, s91, v0
	s_mov_b32 s5, s87
	s_andn2_b64 vcc, exec, s[6:7]
	v_readfirstlane_b32 s1, v1
	v_readlane_b32 s86, v254, 3
	v_readlane_b32 s87, v254, 4
	s_cbranch_vccnz .LBB0_1270
	s_sub_i32 s13, s86, 40
	s_lshl_b32 s33, s3, 4
	s_cmp_ge_i32 s13, s33
	s_cbranch_scc1 .LBB0_1270
	v_ashrrev_i32_e32 v3, 31, v1
	v_lshrrev_b32_e32 v3, 26, v3
	v_lshlrev_b32_e32 v2, 4, v1
	v_add_u32_e32 v3, v1, v3
	v_bfe_i32 v1, v1, 27, 1
	v_lshrrev_b32_e32 v1, 22, v1
	v_add_u32_e32 v1, v2, v1
	v_and_b32_e32 v1, 0xfffffc00, v1
	v_sub_u32_e32 v1, v2, v1
	v_lshrrev_b32_e32 v2, 4, v1
	v_bitop3_b32 v1, v2, v1, 32 bitop3:0x6c
	v_ashrrev_i32_e32 v4, 31, v1
	v_ashrrev_i32_e32 v3, 6, v3
	v_lshrrev_b32_e32 v4, 26, v4
	v_lshlrev_b32_e32 v2, 3, v3
	v_add_u32_e32 v4, v1, v4
	v_and_b32_e32 v2, -16, v2
	v_ashrrev_i32_e32 v5, 6, v4
	v_add_u32_e32 v2, v5, v2
	v_and_b32_e32 v4, 0xc0, v4
	v_and_b32_e32 v5, 3, v5
	s_mov_b32 s2, 0x1fffe0
	v_sub_u32_e32 v1, v1, v4
	v_mov_b32_e32 v4, 1
	v_and_or_b32 v5, v2, s2, v5
	s_lshr_b32 s2, s13, 2
	v_lshlrev_b32_e32 v3, 5, v3
	v_ashrrev_i16_sdwa v1, v4, sext(v1) dst_sel:DWORD dst_unused:UNUSED_PAD src0_sel:DWORD src1_sel:BYTE_0
	v_lshlrev_b32_e32 v4, 1, v2
	v_lshrrev_b32_e32 v6, 2, v2
	s_and_b32 s2, s2, 0x3ffffffc
	v_and_b32_e32 v3, 32, v3
	v_bfe_i32 v1, v1, 0, 16
	v_and_b32_e32 v4, 24, v4
	v_and_b32_e32 v6, 4, v6
	s_add_i32 s2, s2, 0
	v_or3_b32 v4, v5, v6, v4
	v_add_lshl_u32 v1, v3, v1, 1
	s_add_i32 s2, s2, 0x20000
	v_lshl_add_u32 v138, v2, 11, v1
	v_lshl_add_u32 v139, v4, 11, v1
	v_mov_b32_e32 v1, s2
	ds_read_b32 v1, v1
	s_ashr_i32 s0, s1, 6
	s_and_b32 s71, s13, 15
	s_lshl_b32 s6, s0, 10
	s_lshl_b32 s34, s71, 19
	s_waitcnt lgkmcnt(0)
	v_readfirstlane_b32 s72, v1
	s_ashr_i32 s38, s72, 5
	s_lshl_b32 s7, s38, 23
	s_or_b32 s75, s7, s34
	s_add_i32 s34, s6, 0
	s_mov_b32 s87, 0x20000
	s_mov_b32 s86, -1
	s_add_i32 s35, s34, 0x10000
	s_and_b32 s9, s55, 0xffff
	s_mov_b32 s8, s54
	s_mov_b32 s10, s86
	s_mov_b32 s11, s87
	s_mov_b32 m0, s35
	s_add_i32 s40, s34, 0x12000
	buffer_load_dwordx4 v139, s[8:11], s75 offen lds
	s_or_b32 s6, s75, 0x20000
	s_mov_b32 m0, s40
	s_and_b32 s85, s85, 0xffff
	s_lshl_b32 s2, s72, 19
	buffer_load_dwordx4 v139, s[8:11], s6 offen lds
	s_mov_b32 m0, s34
	s_add_i32 s41, s34, 0x2000
	buffer_load_dwordx4 v138, s[84:87], s2 offen lds
	s_or_b32 s6, s2, 0x20000
	s_mov_b32 m0, s41
	s_add_i32 s42, s34, 0x14000
	buffer_load_dwordx4 v138, s[84:87], s6 offen lds
	s_or_b32 s6, s75, 0x40000
	s_mov_b32 m0, s42
	s_add_i32 s43, s34, 0x16000
	buffer_load_dwordx4 v139, s[8:11], s6 offen lds
	s_or_b32 s6, s75, 0x60000
	s_mov_b32 m0, s43
	s_add_i32 s44, s34, 0x4000
	buffer_load_dwordx4 v139, s[8:11], s6 offen lds
	s_or_b32 s6, s2, 0x40000
	s_mov_b32 m0, s44
	s_add_i32 s45, s34, 0x6000
	buffer_load_dwordx4 v138, s[84:87], s6 offen lds
	s_or_b32 s6, s2, 0x60000
	s_mov_b32 m0, s45
	s_mov_b32 s46, 0
	buffer_load_dwordx4 v138, s[84:87], s6 offen lds
	s_ashr_i32 s6, s1, 8
	s_cmp_lg_u32 s6, 1
	s_cbranch_scc1 .LBB0_1261
	s_barrier
.LBB0_1261:
	s_add_i32 s47, s34, 0x18000
	s_or_b32 s7, s75, 0x80
	s_mov_b32 s8, s54
	s_mov_b32 s10, s86
	s_mov_b32 s11, s87
	s_mov_b32 m0, s47
	s_add_i32 s48, s34, 0x1a000
	s_waitcnt vmcnt(4)
	s_barrier
	buffer_load_dwordx4 v139, s[8:11], s7 offen lds
	s_or_b32 s7, s75, 0x20080
	s_mov_b32 m0, s48
	s_add_i32 s49, s34, 0x8000
	buffer_load_dwordx4 v139, s[8:11], s7 offen lds
	s_or_b32 s7, s2, 0x80
	s_mov_b32 m0, s49
	s_add_i32 s50, s34, 0xa000
	buffer_load_dwordx4 v138, s[84:87], s7 offen lds
	s_or_b32 s7, s2, 0x20080
	s_mov_b32 m0, s50
	s_add_i32 s51, s34, 0x1c000
	buffer_load_dwordx4 v138, s[84:87], s7 offen lds
	s_or_b32 s7, s75, 0x40080
	s_mov_b32 m0, s51
	s_add_i32 s52, s34, 0x1e000
	buffer_load_dwordx4 v139, s[8:11], s7 offen lds
	s_or_b32 s7, s75, 0x60080
	s_mov_b32 m0, s52
	s_and_b32 s0, s0, 3
	buffer_load_dwordx4 v139, s[8:11], s7 offen lds
	v_and_b32_e32 v1, 48, v0
	v_lshlrev_b32_e32 v2, 6, v0
	s_movk_i32 s8, 0x3c0
	v_lshlrev_b32_e32 v0, 2, v0
	s_lshl_b32 s53, s6, 6
	s_lshl_b32 s7, s6, 13
	v_and_or_b32 v1, v2, s8, v1
	v_and_b32_e32 v0, 32, v0
	s_lshl_b32 s8, s0, 12
	s_mulk_i32 s6, 0x2400
	v_bitop3_b32 v2, v1, s7, v0 bitop3:0xde
	v_bitop3_b32 v0, v1, s8, v0 bitop3:0xde
	s_waitcnt vmcnt(6)
	s_add_i32 s62, s6, 0
	s_lshl_b32 s7, s0, 5
	s_lshl_b32 s8, s0, 4
	s_add_i32 s62, s62, 0x20800
	v_add_u32_e32 v0, 0, v0
	s_add_i32 s58, s34, 0xc000
	s_lshl_b32 s59, s0, 6
	s_add_i32 s60, s34, 0xe000
	s_sub_i32 s61, s89, 40
	s_add_i32 s63, s62, s8
	v_add_u32_e32 v140, 0x10000, v0
	v_add_u32_e32 v141, 0, v2
	v_mov_b32_e32 v142, 0x7f7f7f7f
	v_add_u32_e32 v143, 0x14000, v0
	v_add_u32_e32 v144, 0x18000, v0
	v_add_u32_e32 v145, 0x1c000, v0
	s_lshl_b32 s64, s7, 2
	v_mov_b32_e32 v137, 0
	s_mov_b32 s0, 0x3c800000
	s_mov_b32 s65, 0xc0e00000
	v_mov_b32_e32 v146, 0x40e00000
	s_barrier

; #define LAS __attribute__((address_space(3)))
; __device__ __forceinline__ void cvt_item_lds(const float* src, int ld_src, fp8_t* dst, int ld_dst, LAS unsigned char* lds, int tid, int wv) {
;     const int lane = tid & 63;
;     const float* s = src + (size_t)(16 * wv) * ld_src + 4 * lane;
;     f32x4 va[16], vb[16];
;     cvt8_load(va, s, ld_src);
; __device__ __forceinline__ void conv_queue(const Params& p, LAS unsigned char* lds, const int wave, const int cw, const int first, const int last, const int slot_off = LDS_MISC) {
;     ...
;     for (;;) {
;         __syncthreads();
;         if (tid == 0) *slot = first + (int)atomicAdd(&p.ctl[cw], 1u);
;         __syncthreads();
;         const int it = *slot;
;         if (it >= last) break;
;         if (it < N_GU) { const int e = it >> 5, rem = it & 31, kb = rem >> 1, nh = rem & 1;
;             const float* src = p.w_gu + (size_t)e * ND * (2 * DFF) + (size_t)(kb * 128) * (2 * DFF) + nh * 2048;
;             fp8_t* dst = p.wt_gu + (size_t)e * (2 * DFF) * ND + (size_t)(nh * 2048) * ND + kb * 128;
;             cvt_item_lds(src, 2 * DFF, dst, ND, lds, tid, wave); }
;         else { const int j = it - N_GU, e = j >> 4, kb = j & 15;
;             const float* src = p.w_down + (size_t)e * DFF * ND + (size_t)(kb * 128) * ND;
;             fp8_t* dst = p.wt_down + (size_t)e * ND * DFF + kb * 128;
;             cvt_item_lds(src, ND, dst, DFF, lds, tid, wave); }
.LBB0_1276:
	s_or_b64 exec, exec, s[50:51]
	s_waitcnt vmcnt(0)
	v_readfirstlane_b32 s2, v1
	v_mov_b32_e32 v1, s13
	s_nop 0
	v_add_u32_e32 v0, s2, v0
	v_add_u32_e32 v0, 0x420, v0
	ds_write_b32 v1, v0
.LBB0_1277:
	s_or_b64 exec, exec, s[48:49]
	s_waitcnt lgkmcnt(0)
	s_barrier
	ds_read_b32 v0, v208
	s_movk_i32 s2, 0x5bf
	s_mov_b64 s[48:49], -1
	s_waitcnt lgkmcnt(0)
	v_cmp_lt_i32_e32 vcc, s2, v0
	v_readfirstlane_b32 s33, v0
	s_cbranch_vccnz .LBB0_1272
	s_cmpk_gt_i32 s33, 0x3ff
	s_cbranch_scc0 .LBB0_1280
	s_add_i32 s2, s33, 0xfffffc00
	s_lshr_b32 s6, s2, 4
	v_readlane_b32 s16, v254, 22
	s_lshl_b64 s[34:35], s[6:7], 22
	s_lshl_b64 s[48:49], s[6:7], 24
	v_readlane_b32 s20, v254, 26
	v_readlane_b32 s21, v254, 27
	s_add_u32 s2, s20, s48
	s_addc_u32 s6, s21, s49
	s_lshl_b32 s48, s33, 7
	s_and_b32 s48, s48, 0x780
	s_lshl_b32 s49, s48, 13
	s_add_u32 s2, s2, s49
	s_addc_u32 s6, s6, 0
	s_add_u32 s34, s56, s34
	s_addc_u32 s35, s57, s35
	s_add_u32 s50, s34, s48
	s_addc_u32 s51, s35, 0
	s_add_u32 s48, s2, s14
	s_addc_u32 s49, s6, s15
	v_lshl_add_u64 v[176:177], s[48:49], 0, v[132:133]
	s_movk_i32 s2, 0x2000
	v_add_co_u32_e32 v178, vcc, s2, v176
	s_movk_i32 s2, 0x3000
	s_nop 0
	v_addc_co_u32_e32 v179, vcc, 0, v177, vcc
	v_add_co_u32_e32 v146, vcc, s2, v176
	s_movk_i32 s2, 0x6000
	s_nop 0
	v_addc_co_u32_e32 v147, vcc, 0, v177, vcc
	v_add_co_u32_e32 v180, vcc, s58, v176
	v_readlane_b32 s17, v254, 23
	s_nop 0
	v_addc_co_u32_e32 v181, vcc, 0, v177, vcc
	v_add_co_u32_e32 v148, vcc, s66, v176
	v_readlane_b32 s18, v254, 24
	s_nop 0
	v_addc_co_u32_e32 v149, vcc, 0, v177, vcc
	v_add_co_u32_e32 v182, vcc, s2, v176
	s_movk_i32 s2, 0x7000
	s_nop 0
	v_addc_co_u32_e32 v183, vcc, 0, v177, vcc
	v_add_co_u32_e32 v150, vcc, s2, v176
	s_mov_b32 s2, 0xa000
	s_nop 0
	v_addc_co_u32_e32 v151, vcc, 0, v177, vcc
	v_add_co_u32_e32 v184, vcc, s59, v176
	global_load_dwordx4 v[8:11], v[148:149], off offset:-4096 nt
	global_load_dwordx4 v[12:15], v[150:151], off offset:-4096 nt
	v_addc_co_u32_e32 v185, vcc, 0, v177, vcc
	v_add_co_u32_e32 v152, vcc, s67, v176
	v_readlane_b32 s19, v254, 25
	s_nop 0
	v_addc_co_u32_e32 v153, vcc, 0, v177, vcc
	v_add_co_u32_e32 v186, vcc, s2, v176
	s_mov_b32 s2, 0xb000
	s_nop 0
	v_addc_co_u32_e32 v187, vcc, 0, v177, vcc
	v_add_co_u32_e32 v154, vcc, s2, v176
	s_mov_b32 s2, 0xe000
	s_nop 0
	v_addc_co_u32_e32 v155, vcc, 0, v177, vcc
	v_add_co_u32_e32 v188, vcc, s60, v176
	global_load_dwordx4 v[24:27], v[152:153], off offset:-4096 nt
	global_load_dwordx4 v[28:31], v[154:155], off offset:-4096 nt
	v_addc_co_u32_e32 v189, vcc, 0, v177, vcc
	v_add_co_u32_e32 v156, vcc, s68, v176
	v_readlane_b32 s22, v254, 28
	s_nop 0
	v_addc_co_u32_e32 v157, vcc, 0, v177, vcc
	v_add_co_u32_e32 v190, vcc, s2, v176
	s_mov_b32 s2, 0xf000
	s_nop 0
	v_addc_co_u32_e32 v191, vcc, 0, v177, vcc
	v_add_co_u32_e32 v158, vcc, s2, v176
	s_mov_b32 s2, 0x12000
	s_nop 0
	v_addc_co_u32_e32 v159, vcc, 0, v177, vcc
	v_add_co_u32_e32 v192, vcc, s61, v176
	global_load_dwordx4 v[48:51], v[156:157], off offset:-4096 nt
	global_load_dwordx4 v[52:55], v[158:159], off offset:-4096 nt
	v_addc_co_u32_e32 v193, vcc, 0, v177, vcc
	v_add_co_u32_e32 v160, vcc, s69, v176
	v_readlane_b32 s23, v254, 29
	s_nop 0
	v_addc_co_u32_e32 v161, vcc, 0, v177, vcc
	v_add_co_u32_e32 v194, vcc, s2, v176
	s_mov_b32 s2, 0x13000
	s_nop 0
	v_addc_co_u32_e32 v195, vcc, 0, v177, vcc
	v_add_co_u32_e32 v162, vcc, s2, v176
	s_mov_b32 s2, 0x16000
	s_nop 0
	v_addc_co_u32_e32 v163, vcc, 0, v177, vcc
	v_add_co_u32_e32 v196, vcc, s62, v176
	global_load_dwordx4 v[56:59], v[160:161], off offset:-4096 nt
	global_load_dwordx4 v[60:63], v[162:163], off offset:-4096 nt
	v_addc_co_u32_e32 v197, vcc, 0, v177, vcc
	v_add_co_u32_e32 v164, vcc, s70, v176
	v_readlane_b32 s24, v254, 30
	s_nop 0
	v_addc_co_u32_e32 v165, vcc, 0, v177, vcc
	v_add_co_u32_e32 v198, vcc, s2, v176
	s_mov_b32 s2, 0x17000
	s_nop 0
	v_addc_co_u32_e32 v199, vcc, 0, v177, vcc
	v_add_co_u32_e32 v166, vcc, s2, v176
	s_mov_b32 s2, 0x1a000
	s_nop 0
	v_addc_co_u32_e32 v167, vcc, 0, v177, vcc
	v_add_co_u32_e32 v200, vcc, s63, v176
	global_load_dwordx4 v[72:75], v[164:165], off offset:-4096 nt
	global_load_dwordx4 v[76:79], v[166:167], off offset:-4096 nt
	v_addc_co_u32_e32 v201, vcc, 0, v177, vcc
	v_add_co_u32_e32 v168, vcc, s71, v176
	v_readlane_b32 s25, v254, 31
	s_nop 0
	v_addc_co_u32_e32 v169, vcc, 0, v177, vcc
	v_add_co_u32_e32 v202, vcc, s2, v176
	s_mov_b32 s2, 0x1b000
	s_nop 0
	v_addc_co_u32_e32 v203, vcc, 0, v177, vcc
	v_add_co_u32_e32 v170, vcc, s2, v176
	s_mov_b32 s2, 0x1e000
	s_nop 0
	v_addc_co_u32_e32 v171, vcc, 0, v177, vcc
	v_add_co_u32_e32 v204, vcc, s64, v176
	global_load_dwordx4 v[88:91], v[168:169], off offset:-4096 nt
	global_load_dwordx4 v[92:95], v[170:171], off offset:-4096 nt
	v_addc_co_u32_e32 v205, vcc, 0, v177, vcc
	v_add_co_u32_e32 v172, vcc, s72, v176
	v_readlane_b32 s26, v254, 32
	s_nop 0
	v_addc_co_u32_e32 v173, vcc, 0, v177, vcc
	v_add_co_u32_e32 v206, vcc, s2, v176
	s_mov_b32 s2, 0x1f000
	s_nop 0
	v_addc_co_u32_e32 v207, vcc, 0, v177, vcc
	v_add_co_u32_e32 v174, vcc, s2, v176
	v_readlane_b32 s27, v254, 33
	s_nop 0
	v_addc_co_u32_e32 v175, vcc, 0, v177, vcc
	global_load_dwordx4 v[108:111], v[172:173], off offset:-4096 nt
	global_load_dwordx4 v[112:115], v[174:175], off offset:-4096 nt
	global_load_dwordx4 v[120:123], v[146:147], off offset:-4096 nt
	global_load_dwordx4 v[96:99], v132, s[48:49] offset:1024 nt
	global_load_dwordx4 v[100:103], v[178:179], off offset:1024 nt
	global_load_dwordx4 v[104:107], v[180:181], off offset:1024 nt
	global_load_dwordx4 v[124:127], v[182:183], off offset:1024 nt
	global_load_dwordx4 v[80:83], v[184:185], off offset:1024 nt
	global_load_dwordx4 v[84:87], v[186:187], off offset:1024 nt
	global_load_dwordx4 v[64:67], v[188:189], off offset:1024 nt
	global_load_dwordx4 v[68:71], v[190:191], off offset:1024 nt
	global_load_dwordx4 v[32:35], v[192:193], off offset:1024 nt
	global_load_dwordx4 v[36:39], v[194:195], off offset:1024 nt
	global_load_dwordx4 v[40:43], v[196:197], off offset:1024 nt
	global_load_dwordx4 v[44:47], v[198:199], off offset:1024 nt
	global_load_dwordx4 v[16:19], v[200:201], off offset:1024 nt
	global_load_dwordx4 v[20:23], v[202:203], off offset:1024 nt
	global_load_dwordx4 v[0:3], v[204:205], off offset:1024 nt
	global_load_dwordx4 v[128:131], v132, s[48:49] nt
	global_load_dwordx4 v[4:7], v[206:207], off offset:1024 nt
	v_readlane_b32 s28, v254, 34
	v_readlane_b32 s29, v254, 35
	v_readlane_b32 s30, v254, 36
	v_readlane_b32 s31, v254, 37
	v_lshl_add_u64 v[144:145], s[50:51], 0, v[134:135]
	s_waitcnt vmcnt(1)
; #define LAS __attribute__((address_space(3)))
; __device__ __forceinline__ unsigned pack4_fp8(float a, float b, float c, float d) { int r = 0; r = __builtin_amdgcn_cvt_pk_fp8_f32(a, b, r, false); r = __builtin_amdgcn_cvt_pk_fp8_f32(c, d, r, true); return (unsigned)r; }
; #define CVT_LDS_BAR() do { asm volatile("s_waitcnt lgkmcnt(0)" ::: "memory"); __builtin_amdgcn_s_barrier(); asm volatile("" ::: "memory"); } while (0)
; __device__ __forceinline__ void cvt8_to_lds(const f32x4 (&v)[16], LAS unsigned char* tile, int lane, int wv) {
; #pragma unroll
;     for (int i = 0; i < 4; ++i) { u32x4 w; w.x = pack4_fp8(v[0][i] * W8_SCALE, v[1][i] * W8_SCALE, v[2][i] * W8_SCALE, v[3][i] * W8_SCALE); w.y = pack4_fp8(v[4][i] * W8_SCALE, v[5][i] * W8_SCALE, v[6][i] * W8_SCALE, v[7][i] * W8_SCALE);
;         w.z = pack4_fp8(v[8][i] * W8_SCALE, v[9][i] * W8_SCALE, v[10][i] * W8_SCALE, v[11][i] * W8_SCALE); w.w = pack4_fp8(v[12][i] * W8_SCALE, v[13][i] * W8_SCALE, v[14][i] * W8_SCALE, v[15][i] * W8_SCALE);
;         *(LAS u32x4*)(tile + (4 * lane + i) * 128 + ((wv ^ (lane & 7)) << 4)) = w; }
; }
; __device__ __forceinline__ void cvt8_from_lds(const LAS unsigned char* tile, fp8_t* d, int ld_dst, int tid) {
;     const int c = tid & 7;
; #pragma unroll
;     for (int q = 0; q < 4; ++q) { const int r = (tid >> 3) + 64 * q; const u32x4 w = *(const LAS u32x4*)(tile + r * 128 + ((c ^ ((r >> 2) & 7)) << 4));
;         __builtin_nontemporal_store(w, (u32x4*)(d + (size_t)r * ld_dst + 16 * c)); }
; __device__ __forceinline__ void cvt_item_lds(const float* src, int ld_src, fp8_t* dst, int ld_dst, LAS unsigned char* lds, int tid, int wv) {
;     ...
;         cvt8_load(vb, s + (t + 1) * 256, ld_src); __builtin_amdgcn_sched_barrier(0);
;         cvt8_to_lds(va, lds, lane, wv); CVT_LDS_BAR(); __builtin_amdgcn_sched_barrier(0);
;         cvt8_from_lds(lds, dst + (size_t)(t * 256) * ld_dst, ld_dst, tid); __builtin_amdgcn_sched_barrier(0);
;         if (t + 2 < 8) { cvt8_load(va, s + (t + 2) * 256, ld_src); __builtin_amdgcn_sched_barrier(0); }
	v_mul_f32_e32 v117, 0x42800000, v128
	v_mul_f32_e32 v118, 0x42800000, v120
	v_mov_b32_e32 v116, v133
	v_cvt_pk_fp8_f32 v116, v117, v118
	v_mul_f32_e32 v24, 0x42800000, v24
	v_mul_f32_e32 v28, 0x42800000, v28
	v_mov_b32_e32 v117, v133
	v_cvt_pk_fp8_f32 v117, v24, v28
	v_mul_f32_e32 v8, 0x42800000, v8
	v_mul_f32_e32 v12, 0x42800000, v12
	v_cvt_pk_fp8_f32 v116, v8, v12 op_sel:[0,0,1]
	v_mul_f32_e32 v8, 0x42800000, v48
	v_mul_f32_e32 v12, 0x42800000, v52
	v_cvt_pk_fp8_f32 v117, v8, v12 op_sel:[0,0,1]
	v_mul_f32_e32 v8, 0x42800000, v56
	v_mul_f32_e32 v12, 0x42800000, v60
	v_mov_b32_e32 v118, v133
	v_cvt_pk_fp8_f32 v118, v8, v12
	v_mul_f32_e32 v8, 0x42800000, v88
	v_mul_f32_e32 v12, 0x42800000, v92
	v_mov_b32_e32 v119, v133
	v_cvt_pk_fp8_f32 v119, v8, v12
	v_mul_f32_e32 v8, 0x42800000, v108
	v_mul_f32_e32 v12, 0x42800000, v112
	v_mov_b32_e32 v214, v133
	v_cvt_pk_fp8_f32 v119, v8, v12 op_sel:[0,0,1]
	v_mul_f32_e32 v8, 0x42800000, v129
	v_mul_f32_e32 v12, 0x42800000, v121
	v_cvt_pk_fp8_f32 v214, v8, v12
	v_mul_f32_e32 v8, 0x42800000, v25
	v_mul_f32_e32 v12, 0x42800000, v29
	v_mov_b32_e32 v215, v133
	v_cvt_pk_fp8_f32 v215, v8, v12
	v_mul_f32_e32 v9, 0x42800000, v9
	v_mul_f32_e32 v13, 0x42800000, v13
	v_cvt_pk_fp8_f32 v214, v9, v13 op_sel:[0,0,1]
	v_mul_f32_e32 v8, 0x42800000, v49
	v_mul_f32_e32 v9, 0x42800000, v53
	v_cvt_pk_fp8_f32 v215, v8, v9 op_sel:[0,0,1]
	v_mul_f32_e32 v8, 0x42800000, v57
	v_mul_f32_e32 v9, 0x42800000, v61
	v_mov_b32_e32 v216, v133
	v_cvt_pk_fp8_f32 v216, v8, v9
	v_mul_f32_e32 v8, 0x42800000, v89
	v_mul_f32_e32 v9, 0x42800000, v93
	v_mov_b32_e32 v217, v133
	v_cvt_pk_fp8_f32 v217, v8, v9
	v_mul_f32_e32 v8, 0x42800000, v109
	v_mul_f32_e32 v9, 0x42800000, v113
	v_mov_b32_e32 v218, v133
	v_cvt_pk_fp8_f32 v217, v8, v9 op_sel:[0,0,1]
	v_mul_f32_e32 v8, 0x42800000, v130
	v_mul_f32_e32 v9, 0x42800000, v122
	v_cvt_pk_fp8_f32 v218, v8, v9
	v_mul_f32_e32 v8, 0x42800000, v26
	v_mul_f32_e32 v9, 0x42800000, v30
	v_mov_b32_e32 v219, v133
	v_cvt_pk_fp8_f32 v219, v8, v9
	v_mul_f32_e32 v8, 0x42800000, v50
	v_mul_f32_e32 v9, 0x42800000, v54
	v_mov_b32_e32 v220, v133
	v_cvt_pk_fp8_f32 v219, v8, v9 op_sel:[0,0,1]
	v_mul_f32_e32 v8, 0x42800000, v58
	v_mul_f32_e32 v9, 0x42800000, v62
	v_cvt_pk_fp8_f32 v220, v8, v9
	v_mul_f32_e32 v8, 0x42800000, v90
	v_mul_f32_e32 v9, 0x42800000, v94
	v_mov_b32_e32 v221, v133
	v_cvt_pk_fp8_f32 v221, v8, v9
	v_mul_f32_e32 v12, 0x42800000, v73
	v_mul_f32_e32 v13, 0x42800000, v77
	v_cvt_pk_fp8_f32 v216, v12, v13 op_sel:[0,0,1]
	v_mul_f32_e32 v10, 0x42800000, v10
	v_mul_f32_e32 v12, 0x42800000, v14
	v_cvt_pk_fp8_f32 v218, v10, v12 op_sel:[0,0,1]
	v_mul_f32_e32 v10, 0x42800000, v74
	v_mul_f32_e32 v12, 0x42800000, v78
	v_mul_f32_e32 v8, 0x42800000, v110
	v_mul_f32_e32 v9, 0x42800000, v114
	v_cvt_pk_fp8_f32 v220, v10, v12 op_sel:[0,0,1]
	v_cvt_pk_fp8_f32 v221, v8, v9 op_sel:[0,0,1]
	v_mul_f32_e32 v9, 0x42800000, v131
	v_mul_f32_e32 v10, 0x42800000, v123
	v_mov_b32_e32 v8, v133
	v_cvt_pk_fp8_f32 v8, v9, v10
	v_mul_f32_e32 v10, 0x42800000, v27
	v_mul_f32_e32 v13, 0x42800000, v31
	v_mov_b32_e32 v9, v133
	v_cvt_pk_fp8_f32 v9, v10, v13
	v_mul_f32_e32 v11, 0x42800000, v11
	v_mul_f32_e32 v12, 0x42800000, v15
	v_cvt_pk_fp8_f32 v8, v11, v12 op_sel:[0,0,1]
	v_mul_f32_e32 v10, 0x42800000, v51
	v_mul_f32_e32 v11, 0x42800000, v55
	v_cvt_pk_fp8_f32 v9, v10, v11 op_sel:[0,0,1]
	v_mul_f32_e32 v11, 0x42800000, v59
	v_mul_f32_e32 v12, 0x42800000, v63
	v_mov_b32_e32 v10, v133
	v_cvt_pk_fp8_f32 v10, v11, v12
	v_mul_f32_e32 v12, 0x42800000, v91
	v_mul_f32_e32 v15, 0x42800000, v95
	v_mov_b32_e32 v11, v133
	v_mul_f32_e32 v24, 0x42800000, v72
	v_mul_f32_e32 v28, 0x42800000, v76
	v_cvt_pk_fp8_f32 v11, v12, v15
	v_cvt_pk_fp8_f32 v118, v24, v28 op_sel:[0,0,1]
	v_mul_f32_e32 v13, 0x42800000, v75
	v_mul_f32_e32 v14, 0x42800000, v79
	v_cvt_pk_fp8_f32 v10, v13, v14 op_sel:[0,0,1]
	v_mul_f32_e32 v12, 0x42800000, v111
	v_mul_f32_e32 v13, 0x42800000, v115
	v_cvt_pk_fp8_f32 v11, v12, v13 op_sel:[0,0,1]
	ds_write_b128 v209, v[116:119]
	ds_write_b128 v209, v[214:217] offset:128
	ds_write_b128 v209, v[218:221] offset:256
	ds_write_b128 v209, v[8:11] offset:384
	s_waitcnt lgkmcnt(0)
	s_barrier
	ds_read_b128 v[8:11], v210
	ds_read_b128 v[12:15], v211
	v_lshl_add_u64 v[28:29], v[144:145], 0, v[136:137]
	ds_read_b128 v[24:27], v212
	v_lshl_add_u64 v[30:31], v[144:145], 0, v[138:139]
	s_waitcnt lgkmcnt(2)
	global_store_dwordx4 v[28:29], v[8:11], off nt
	ds_read_b128 v[8:11], v213
	s_waitcnt lgkmcnt(2)
	global_store_dwordx4 v[30:31], v[12:15], off nt
	s_nop 1
	v_lshl_add_u64 v[12:13], v[144:145], 0, v[140:141]
	s_waitcnt lgkmcnt(1)
	global_store_dwordx4 v[12:13], v[24:27], off nt
	v_lshl_add_u64 v[12:13], v[144:145], 0, v[142:143]
	s_waitcnt lgkmcnt(0)
	global_store_dwordx4 v[12:13], v[8:11], off nt
	global_load_dwordx4 v[108:111], v[178:179], off offset:2048 nt
	global_load_dwordx4 v[112:115], v[180:181], off offset:2048 nt
	global_load_dwordx4 v[116:119], v[182:183], off offset:2048 nt
	global_load_dwordx4 v[88:91], v[184:185], off offset:2048 nt
	global_load_dwordx4 v[92:95], v[186:187], off offset:2048 nt
	global_load_dwordx4 v[72:75], v[188:189], off offset:2048 nt
	global_load_dwordx4 v[76:79], v[190:191], off offset:2048 nt
	global_load_dwordx4 v[48:51], v[192:193], off offset:2048 nt
	global_load_dwordx4 v[52:55], v[194:195], off offset:2048 nt
	global_load_dwordx4 v[56:59], v[196:197], off offset:2048 nt
	global_load_dwordx4 v[60:63], v[198:199], off offset:2048 nt
	global_load_dwordx4 v[24:27], v[200:201], off offset:2048 nt
	global_load_dwordx4 v[28:31], v[202:203], off offset:2048 nt
	global_load_dwordx4 v[8:11], v[204:205], off offset:2048 nt
	global_load_dwordx4 v[120:123], v132, s[48:49] offset:2048 nt
	global_load_dwordx4 v[12:15], v[206:207], off offset:2048 nt
	v_mul_f32_e32 v16, 0x42800000, v16
	v_mul_f32_e32 v20, 0x42800000, v20
	v_mov_b32_e32 v131, v133
	v_cvt_pk_fp8_f32 v131, v16, v20
	v_mul_f32_e32 v0, 0x42800000, v0
	s_waitcnt vmcnt(20)
; #define LAS __attribute__((address_space(3)))
; __device__ __forceinline__ unsigned pack4_fp8(float a, float b, float c, float d) { int r = 0; r = __builtin_amdgcn_cvt_pk_fp8_f32(a, b, r, false); r = __builtin_amdgcn_cvt_pk_fp8_f32(c, d, r, true); return (unsigned)r; }
; __device__ __forceinline__ void cvt8_to_lds(const f32x4 (&v)[16], LAS unsigned char* tile, int lane, int wv) {
; #pragma unroll
;     for (int i = 0; i < 4; ++i) { u32x4 w; w.x = pack4_fp8(v[0][i] * W8_SCALE, v[1][i] * W8_SCALE, v[2][i] * W8_SCALE, v[3][i] * W8_SCALE); w.y = pack4_fp8(v[4][i] * W8_SCALE, v[5][i] * W8_SCALE, v[6][i] * W8_SCALE, v[7][i] * W8_SCALE);
;         w.z = pack4_fp8(v[8][i] * W8_SCALE, v[9][i] * W8_SCALE, v[10][i] * W8_SCALE, v[11][i] * W8_SCALE); w.w = pack4_fp8(v[12][i] * W8_SCALE, v[13][i] * W8_SCALE, v[14][i] * W8_SCALE, v[15][i] * W8_SCALE);
;         *(LAS u32x4*)(tile + (4 * lane + i) * 128 + ((wv ^ (lane & 7)) << 4)) = w; }
; }
; __device__ __forceinline__ void cvt8_from_lds(const LAS unsigned char* tile, fp8_t* d, int ld_dst, int tid) {
;     const int c = tid & 7;
; #pragma unroll
;     for (int q = 0; q < 4; ++q) { const int r = (tid >> 3) + 64 * q; const u32x4 w = *(const LAS u32x4*)(tile + r * 128 + ((c ^ ((r >> 2) & 7)) << 4));
;         __builtin_nontemporal_store(w, (u32x4*)(d + (size_t)r * ld_dst + 16 * c)); }
; }
; __device__ __forceinline__ void cvt_item_lds(const float* src, int ld_src, fp8_t* dst, int ld_dst, LAS unsigned char* lds, int tid, int wv) {
;     const int lane = tid & 63;
;     const float* s = src + (size_t)(16 * wv) * ld_src + 4 * lane;
;     f32x4 va[16], vb[16];
;     cvt8_load(va, s, ld_src);
; #pragma unroll
;     for (int t = 0; t < 8; t += 2) {
;         cvt8_load(vb, s + (t + 1) * 256, ld_src); __builtin_amdgcn_sched_barrier(0);
;         cvt8_to_lds(va, lds, lane, wv); CVT_LDS_BAR(); __builtin_amdgcn_sched_barrier(0);
;         cvt8_from_lds(lds, dst + (size_t)(t * 256) * ld_dst, ld_dst, tid); __builtin_amdgcn_sched_barrier(0);
;         if (t + 2 < 8) { cvt8_load(va, s + (t + 2) * 256, ld_src); __builtin_amdgcn_sched_barrier(0); }
;         cvt8_to_lds(vb, lds + 32768, lane, wv); CVT_LDS_BAR(); __builtin_amdgcn_sched_barrier(0);
;         cvt8_from_lds(lds + 32768, dst + (size_t)((t + 1) * 256) * ld_dst, ld_dst, tid); __builtin_amdgcn_sched_barrier(0);
;     }
	v_mul_f32_e32 v4, 0x42800000, v4
	v_mov_b32_e32 v214, v133
	v_cvt_pk_fp8_f32 v131, v0, v4 op_sel:[0,0,1]
	v_mul_f32_e32 v0, 0x42800000, v97
	v_mul_f32_e32 v4, 0x42800000, v101
	v_cvt_pk_fp8_f32 v214, v0, v4
	v_mul_f32_e32 v0, 0x42800000, v81
	v_mul_f32_e32 v4, 0x42800000, v85
	v_mov_b32_e32 v215, v133
	v_cvt_pk_fp8_f32 v215, v0, v4
	v_mul_f32_e32 v0, 0x42800000, v65
	v_mul_f32_e32 v4, 0x42800000, v69
	v_mov_b32_e32 v216, v133
	v_cvt_pk_fp8_f32 v215, v0, v4 op_sel:[0,0,1]
	v_mul_f32_e32 v0, 0x42800000, v33
	v_mul_f32_e32 v4, 0x42800000, v37
	v_cvt_pk_fp8_f32 v216, v0, v4
	v_mul_f32_e32 v0, 0x42800000, v17
	v_mul_f32_e32 v4, 0x42800000, v21
	v_mov_b32_e32 v217, v133
	v_cvt_pk_fp8_f32 v217, v0, v4
	v_mul_f32_e32 v0, 0x42800000, v1
	v_mul_f32_e32 v1, 0x42800000, v5
	v_mov_b32_e32 v218, v133
	v_cvt_pk_fp8_f32 v217, v0, v1 op_sel:[0,0,1]
	v_mul_f32_e32 v0, 0x42800000, v98
	v_mul_f32_e32 v1, 0x42800000, v102
	v_cvt_pk_fp8_f32 v218, v0, v1
	v_mul_f32_e32 v0, 0x42800000, v82
	v_mul_f32_e32 v1, 0x42800000, v86
	v_mov_b32_e32 v219, v133
	v_cvt_pk_fp8_f32 v219, v0, v1
	v_mul_f32_e32 v0, 0x42800000, v66
	v_mul_f32_e32 v1, 0x42800000, v70
	v_mov_b32_e32 v220, v133
	v_cvt_pk_fp8_f32 v219, v0, v1 op_sel:[0,0,1]
	v_mul_f32_e32 v0, 0x42800000, v34
	v_mul_f32_e32 v1, 0x42800000, v38
	v_cvt_pk_fp8_f32 v220, v0, v1
	v_mul_f32_e32 v0, 0x42800000, v18
	v_mul_f32_e32 v1, 0x42800000, v22
	v_mov_b32_e32 v221, v133
	v_cvt_pk_fp8_f32 v221, v0, v1
	v_mul_f32_e32 v16, 0x42800000, v105
	v_mul_f32_e32 v20, 0x42800000, v125
	v_cvt_pk_fp8_f32 v214, v16, v20 op_sel:[0,0,1]
	v_mul_f32_e32 v16, 0x42800000, v41
	v_mul_f32_e32 v20, 0x42800000, v45
	v_mul_f32_e32 v0, 0x42800000, v2
	v_mul_f32_e32 v1, 0x42800000, v6
	v_cvt_pk_fp8_f32 v216, v16, v20 op_sel:[0,0,1]
	v_cvt_pk_fp8_f32 v221, v0, v1 op_sel:[0,0,1]
	v_mul_f32_e32 v0, 0x42800000, v99
	v_mul_f32_e32 v1, 0x42800000, v103
	v_mov_b32_e32 v16, v133
	v_cvt_pk_fp8_f32 v16, v0, v1
	v_mul_f32_e32 v0, 0x42800000, v83
	v_mul_f32_e32 v1, 0x42800000, v87
	v_mov_b32_e32 v17, v133
	v_cvt_pk_fp8_f32 v17, v0, v1
	v_mul_f32_e32 v96, 0x42800000, v96
	v_mul_f32_e32 v100, 0x42800000, v100
	v_mov_b32_e32 v128, v133
	v_mul_f32_e32 v80, 0x42800000, v80
	v_mul_f32_e32 v84, 0x42800000, v84
	v_mov_b32_e32 v129, v133
	v_mul_f32_e32 v32, 0x42800000, v32
	v_mul_f32_e32 v36, 0x42800000, v36
	v_mov_b32_e32 v130, v133
	v_cvt_pk_fp8_f32 v128, v96, v100
	v_cvt_pk_fp8_f32 v129, v80, v84
	v_cvt_pk_fp8_f32 v130, v32, v36
	v_mul_f32_e32 v0, 0x42800000, v67
	v_mul_f32_e32 v1, 0x42800000, v71
	v_cvt_pk_fp8_f32 v17, v0, v1 op_sel:[0,0,1]
	v_mul_f32_e32 v0, 0x42800000, v35
	v_mul_f32_e32 v1, 0x42800000, v39
	v_mov_b32_e32 v18, v133
	v_cvt_pk_fp8_f32 v18, v0, v1
	v_mul_f32_e32 v0, 0x42800000, v19
	v_mul_f32_e32 v1, 0x42800000, v23
	v_mov_b32_e32 v19, v133
	v_mul_f32_e32 v104, 0x42800000, v104
	v_mul_f32_e32 v124, 0x42800000, v124
	v_mul_f32_e32 v64, 0x42800000, v64
	v_mul_f32_e32 v68, 0x42800000, v68
	v_mul_f32_e32 v40, 0x42800000, v40
	v_mul_f32_e32 v44, 0x42800000, v44
	v_mul_f32_e32 v4, 0x42800000, v106
	v_mul_f32_e32 v5, 0x42800000, v126
	v_cvt_pk_fp8_f32 v19, v0, v1
	v_cvt_pk_fp8_f32 v128, v104, v124 op_sel:[0,0,1]
	v_cvt_pk_fp8_f32 v129, v64, v68 op_sel:[0,0,1]
	v_cvt_pk_fp8_f32 v130, v40, v44 op_sel:[0,0,1]
	v_cvt_pk_fp8_f32 v218, v4, v5 op_sel:[0,0,1]
	v_mul_f32_e32 v4, 0x42800000, v42
	v_mul_f32_e32 v5, 0x42800000, v46
	v_cvt_pk_fp8_f32 v220, v4, v5 op_sel:[0,0,1]
	v_mul_f32_e32 v2, 0x42800000, v107
	v_mul_f32_e32 v4, 0x42800000, v127
	v_cvt_pk_fp8_f32 v16, v2, v4 op_sel:[0,0,1]
	v_mul_f32_e32 v2, 0x42800000, v43
	v_mul_f32_e32 v4, 0x42800000, v47
	v_mul_f32_e32 v0, 0x42800000, v3
	v_mul_f32_e32 v1, 0x42800000, v7
	v_cvt_pk_fp8_f32 v18, v2, v4 op_sel:[0,0,1]
	v_cvt_pk_fp8_f32 v19, v0, v1 op_sel:[0,0,1]
	ds_write_b128 v209, v[128:131] offset:32768
	ds_write_b128 v209, v[214:217] offset:32896
	ds_write_b128 v209, v[218:221] offset:33024
	ds_write_b128 v209, v[16:19] offset:33152
	s_waitcnt lgkmcnt(0)
	s_barrier
	ds_read_b128 v[0:3], v210 offset:32768
	v_lshl_add_u64 v[20:21], v[144:145], 0, s[10:11]
	ds_read_b128 v[4:7], v211 offset:32768
	ds_read_b128 v[16:19], v212 offset:32768
	v_lshl_add_u64 v[22:23], v[20:21], 0, v[136:137]
	s_waitcnt lgkmcnt(2)
	global_store_dwordx4 v[22:23], v[0:3], off nt
	ds_read_b128 v[0:3], v213 offset:32768
	v_lshl_add_u64 v[22:23], v[20:21], 0, v[138:139]
	s_waitcnt lgkmcnt(2)
	global_store_dwordx4 v[22:23], v[4:7], off nt
	s_nop 1
	v_lshl_add_u64 v[4:5], v[20:21], 0, v[140:141]
	s_waitcnt lgkmcnt(1)
	global_store_dwordx4 v[4:5], v[16:19], off nt
	v_lshl_add_u64 v[4:5], v[20:21], 0, v[142:143]
	s_waitcnt lgkmcnt(0)
	global_store_dwordx4 v[4:5], v[0:3], off nt
	global_load_dwordx4 v[96:99], v[178:179], off offset:3072 nt
	global_load_dwordx4 v[100:103], v[180:181], off offset:3072 nt
	global_load_dwordx4 v[104:107], v[182:183], off offset:3072 nt
	global_load_dwordx4 v[80:83], v[184:185], off offset:3072 nt
	global_load_dwordx4 v[84:87], v[186:187], off offset:3072 nt
	global_load_dwordx4 v[64:67], v[188:189], off offset:3072 nt
	global_load_dwordx4 v[68:71], v[190:191], off offset:3072 nt
	global_load_dwordx4 v[32:35], v[192:193], off offset:3072 nt
	global_load_dwordx4 v[36:39], v[194:195], off offset:3072 nt
	global_load_dwordx4 v[40:43], v[196:197], off offset:3072 nt
	global_load_dwordx4 v[44:47], v[198:199], off offset:3072 nt
	global_load_dwordx4 v[16:19], v[200:201], off offset:3072 nt
	global_load_dwordx4 v[20:23], v[202:203], off offset:3072 nt
	global_load_dwordx4 v[0:3], v[204:205], off offset:3072 nt
	global_load_dwordx4 v[124:127], v132, s[48:49] offset:3072 nt
	global_load_dwordx4 v[4:7], v[206:207], off offset:3072 nt
	s_waitcnt vmcnt(24)
; #define LAS __attribute__((address_space(3)))
; __device__ __forceinline__ unsigned pack4_fp8(float a, float b, float c, float d) { int r = 0; r = __builtin_amdgcn_cvt_pk_fp8_f32(a, b, r, false); r = __builtin_amdgcn_cvt_pk_fp8_f32(c, d, r, true); return (unsigned)r; }
; __device__ __forceinline__ void cvt8_to_lds(const f32x4 (&v)[16], LAS unsigned char* tile, int lane, int wv) {
; #pragma unroll
;     for (int i = 0; i < 4; ++i) { u32x4 w; w.x = pack4_fp8(v[0][i] * W8_SCALE, v[1][i] * W8_SCALE, v[2][i] * W8_SCALE, v[3][i] * W8_SCALE); w.y = pack4_fp8(v[4][i] * W8_SCALE, v[5][i] * W8_SCALE, v[6][i] * W8_SCALE, v[7][i] * W8_SCALE);
;         w.z = pack4_fp8(v[8][i] * W8_SCALE, v[9][i] * W8_SCALE, v[10][i] * W8_SCALE, v[11][i] * W8_SCALE); w.w = pack4_fp8(v[12][i] * W8_SCALE, v[13][i] * W8_SCALE, v[14][i] * W8_SCALE, v[15][i] * W8_SCALE);
;         *(LAS u32x4*)(tile + (4 * lane + i) * 128 + ((wv ^ (lane & 7)) << 4)) = w; }
; }
; __device__ __forceinline__ void cvt8_from_lds(const LAS unsigned char* tile, fp8_t* d, int ld_dst, int tid) {
;     const int c = tid & 7;
; #pragma unroll
;     for (int q = 0; q < 4; ++q) { const int r = (tid >> 3) + 64 * q; const u32x4 w = *(const LAS u32x4*)(tile + r * 128 + ((c ^ ((r >> 2) & 7)) << 4));
;         __builtin_nontemporal_store(w, (u32x4*)(d + (size_t)r * ld_dst + 16 * c)); }
; }
; __device__ __forceinline__ void cvt_item_lds(const float* src, int ld_src, fp8_t* dst, int ld_dst, LAS unsigned char* lds, int tid, int wv) {
;     const int lane = tid & 63;
;     const float* s = src + (size_t)(16 * wv) * ld_src + 4 * lane;
;     f32x4 va[16], vb[16];
;     cvt8_load(va, s, ld_src);
; #pragma unroll
;     for (int t = 0; t < 8; t += 2) {
;         cvt8_load(vb, s + (t + 1) * 256, ld_src); __builtin_amdgcn_sched_barrier(0);
;         cvt8_to_lds(va, lds, lane, wv); CVT_LDS_BAR(); __builtin_amdgcn_sched_barrier(0);
;         cvt8_from_lds(lds, dst + (size_t)(t * 256) * ld_dst, ld_dst, tid); __builtin_amdgcn_sched_barrier(0);
;         if (t + 2 < 8) { cvt8_load(va, s + (t + 2) * 256, ld_src); __builtin_amdgcn_sched_barrier(0); }
;         cvt8_to_lds(vb, lds + 32768, lane, wv); CVT_LDS_BAR(); __builtin_amdgcn_sched_barrier(0);
;         cvt8_from_lds(lds + 32768, dst + (size_t)((t + 1) * 256) * ld_dst, ld_dst, tid); __builtin_amdgcn_sched_barrier(0);
;     }
	v_mul_f32_e32 v24, 0x42800000, v24
	s_waitcnt vmcnt(23)
	v_mul_f32_e32 v28, 0x42800000, v28
	v_mov_b32_e32 v131, v133
	v_cvt_pk_fp8_f32 v131, v24, v28
	s_waitcnt vmcnt(22)
	v_mul_f32_e32 v8, 0x42800000, v8
	s_waitcnt vmcnt(20)
	v_mul_f32_e32 v12, 0x42800000, v12
	v_mov_b32_e32 v178, v133
	v_cvt_pk_fp8_f32 v131, v8, v12 op_sel:[0,0,1]
	v_mul_f32_e32 v8, 0x42800000, v121
	v_mul_f32_e32 v12, 0x42800000, v109
	v_cvt_pk_fp8_f32 v178, v8, v12
	v_mul_f32_e32 v8, 0x42800000, v89
	v_mul_f32_e32 v12, 0x42800000, v93
	v_mov_b32_e32 v179, v133
	v_cvt_pk_fp8_f32 v179, v8, v12
	v_mul_f32_e32 v8, 0x42800000, v73
	v_mul_f32_e32 v12, 0x42800000, v77
	v_mov_b32_e32 v180, v133
	v_cvt_pk_fp8_f32 v179, v8, v12 op_sel:[0,0,1]
	v_mul_f32_e32 v8, 0x42800000, v49
	v_mul_f32_e32 v12, 0x42800000, v53
	v_cvt_pk_fp8_f32 v180, v8, v12
	v_mul_f32_e32 v8, 0x42800000, v25
	v_mul_f32_e32 v12, 0x42800000, v29
	v_mov_b32_e32 v181, v133
	v_cvt_pk_fp8_f32 v181, v8, v12
	v_mul_f32_e32 v8, 0x42800000, v9
	v_mul_f32_e32 v9, 0x42800000, v13
	v_mov_b32_e32 v182, v133
	v_cvt_pk_fp8_f32 v181, v8, v9 op_sel:[0,0,1]
	v_mul_f32_e32 v8, 0x42800000, v122
	v_mul_f32_e32 v9, 0x42800000, v110
	v_cvt_pk_fp8_f32 v182, v8, v9
	v_mul_f32_e32 v8, 0x42800000, v90
	v_mul_f32_e32 v9, 0x42800000, v94
	v_mov_b32_e32 v183, v133
	v_cvt_pk_fp8_f32 v183, v8, v9
	v_mul_f32_e32 v8, 0x42800000, v74
	v_mul_f32_e32 v9, 0x42800000, v78
	v_mov_b32_e32 v184, v133
	v_cvt_pk_fp8_f32 v183, v8, v9 op_sel:[0,0,1]
	v_mul_f32_e32 v8, 0x42800000, v50
	v_mul_f32_e32 v9, 0x42800000, v54
	v_cvt_pk_fp8_f32 v184, v8, v9
	v_mul_f32_e32 v8, 0x42800000, v26
	v_mul_f32_e32 v9, 0x42800000, v30
	v_mov_b32_e32 v185, v133
	v_cvt_pk_fp8_f32 v185, v8, v9
	v_mul_f32_e32 v24, 0x42800000, v113
	v_mul_f32_e32 v28, 0x42800000, v117
	v_cvt_pk_fp8_f32 v178, v24, v28 op_sel:[0,0,1]
	v_mul_f32_e32 v24, 0x42800000, v57
	v_mul_f32_e32 v28, 0x42800000, v61
	v_mul_f32_e32 v8, 0x42800000, v10
	v_mul_f32_e32 v9, 0x42800000, v14
	v_cvt_pk_fp8_f32 v180, v24, v28 op_sel:[0,0,1]
	v_cvt_pk_fp8_f32 v185, v8, v9 op_sel:[0,0,1]
	v_mul_f32_e32 v8, 0x42800000, v123
	v_mul_f32_e32 v9, 0x42800000, v111
	v_mov_b32_e32 v24, v133
	v_cvt_pk_fp8_f32 v24, v8, v9
	v_mul_f32_e32 v8, 0x42800000, v91
	v_mul_f32_e32 v9, 0x42800000, v95
	v_mov_b32_e32 v25, v133
	v_cvt_pk_fp8_f32 v25, v8, v9
	v_mul_f32_e32 v120, 0x42800000, v120
	v_mul_f32_e32 v108, 0x42800000, v108
	v_mov_b32_e32 v128, v133
	v_mul_f32_e32 v88, 0x42800000, v88
	v_mul_f32_e32 v92, 0x42800000, v92
	v_mov_b32_e32 v129, v133
	v_mul_f32_e32 v48, 0x42800000, v48
	v_mul_f32_e32 v52, 0x42800000, v52
	v_mov_b32_e32 v130, v133
	v_cvt_pk_fp8_f32 v128, v120, v108
	v_cvt_pk_fp8_f32 v129, v88, v92
	v_cvt_pk_fp8_f32 v130, v48, v52
	v_mul_f32_e32 v8, 0x42800000, v75
	v_mul_f32_e32 v9, 0x42800000, v79
	v_cvt_pk_fp8_f32 v25, v8, v9 op_sel:[0,0,1]
	v_mul_f32_e32 v8, 0x42800000, v51
	v_mul_f32_e32 v9, 0x42800000, v55
	v_mov_b32_e32 v26, v133
	v_cvt_pk_fp8_f32 v26, v8, v9
	v_mul_f32_e32 v8, 0x42800000, v27
	v_mul_f32_e32 v9, 0x42800000, v31
	v_mov_b32_e32 v27, v133
	v_mul_f32_e32 v112, 0x42800000, v112
	v_mul_f32_e32 v116, 0x42800000, v116
	v_mul_f32_e32 v72, 0x42800000, v72
	v_mul_f32_e32 v76, 0x42800000, v76
	v_mul_f32_e32 v56, 0x42800000, v56
	v_mul_f32_e32 v60, 0x42800000, v60
	v_mul_f32_e32 v12, 0x42800000, v114
	v_mul_f32_e32 v13, 0x42800000, v118
	v_cvt_pk_fp8_f32 v27, v8, v9
	v_cvt_pk_fp8_f32 v128, v112, v116 op_sel:[0,0,1]
	v_cvt_pk_fp8_f32 v129, v72, v76 op_sel:[0,0,1]
	v_cvt_pk_fp8_f32 v130, v56, v60 op_sel:[0,0,1]
	v_cvt_pk_fp8_f32 v182, v12, v13 op_sel:[0,0,1]
	v_mul_f32_e32 v12, 0x42800000, v58
	v_mul_f32_e32 v13, 0x42800000, v62
	v_cvt_pk_fp8_f32 v184, v12, v13 op_sel:[0,0,1]
	v_mul_f32_e32 v10, 0x42800000, v115
	v_mul_f32_e32 v12, 0x42800000, v119
	v_cvt_pk_fp8_f32 v24, v10, v12 op_sel:[0,0,1]
	v_mul_f32_e32 v10, 0x42800000, v59
	v_mul_f32_e32 v12, 0x42800000, v63
	v_mul_f32_e32 v8, 0x42800000, v11
	v_mul_f32_e32 v9, 0x42800000, v15
	v_cvt_pk_fp8_f32 v26, v10, v12 op_sel:[0,0,1]
	v_cvt_pk_fp8_f32 v27, v8, v9 op_sel:[0,0,1]
	ds_write_b128 v209, v[128:131]
	ds_write_b128 v209, v[178:181] offset:128
	ds_write_b128 v209, v[182:185] offset:256
	ds_write_b128 v209, v[24:27] offset:384
	s_waitcnt lgkmcnt(0)
	s_barrier
	ds_read_b128 v[8:11], v210
	v_lshl_add_u64 v[28:29], v[144:145], 0, s[36:37]
	ds_read_b128 v[12:15], v211
	ds_read_b128 v[24:27], v212
	v_lshl_add_u64 v[30:31], v[28:29], 0, v[136:137]
	s_waitcnt lgkmcnt(2)
	global_store_dwordx4 v[30:31], v[8:11], off nt
	ds_read_b128 v[8:11], v213
	v_lshl_add_u64 v[30:31], v[28:29], 0, v[138:139]
	s_waitcnt lgkmcnt(2)
	global_store_dwordx4 v[30:31], v[12:15], off nt
	s_nop 1
	v_lshl_add_u64 v[12:13], v[28:29], 0, v[140:141]
	s_waitcnt lgkmcnt(1)
	global_store_dwordx4 v[12:13], v[24:27], off nt
	v_lshl_add_u64 v[12:13], v[28:29], 0, v[142:143]
	s_waitcnt lgkmcnt(0)
	global_store_dwordx4 v[12:13], v[8:11], off nt
	v_add_co_u32_e32 v176, vcc, s65, v176
	s_nop 1
	v_addc_co_u32_e32 v177, vcc, 0, v177, vcc
	global_load_dwordx4 v[108:111], v[176:177], off nt
	global_load_dwordx4 v[112:115], v[146:147], off nt
	global_load_dwordx4 v[116:119], v[148:149], off nt
	global_load_dwordx4 v[120:123], v[150:151], off nt
	global_load_dwordx4 v[88:91], v[152:153], off nt
	global_load_dwordx4 v[92:95], v[154:155], off nt
	global_load_dwordx4 v[72:75], v[156:157], off nt
	global_load_dwordx4 v[76:79], v[158:159], off nt
	global_load_dwordx4 v[48:51], v[160:161], off nt
	global_load_dwordx4 v[52:55], v[162:163], off nt
	global_load_dwordx4 v[56:59], v[164:165], off nt
	global_load_dwordx4 v[60:63], v[166:167], off nt
	global_load_dwordx4 v[24:27], v[168:169], off nt
	global_load_dwordx4 v[28:31], v[170:171], off nt
	global_load_dwordx4 v[8:11], v[172:173], off nt
	global_load_dwordx4 v[12:15], v[174:175], off nt
	s_waitcnt vmcnt(24)
; #define LAS __attribute__((address_space(3)))
; __device__ __forceinline__ unsigned pack4_fp8(float a, float b, float c, float d) { int r = 0; r = __builtin_amdgcn_cvt_pk_fp8_f32(a, b, r, false); r = __builtin_amdgcn_cvt_pk_fp8_f32(c, d, r, true); return (unsigned)r; }
; __device__ __forceinline__ void cvt8_to_lds(const f32x4 (&v)[16], LAS unsigned char* tile, int lane, int wv) {
; #pragma unroll
;     for (int i = 0; i < 4; ++i) { u32x4 w; w.x = pack4_fp8(v[0][i] * W8_SCALE, v[1][i] * W8_SCALE, v[2][i] * W8_SCALE, v[3][i] * W8_SCALE); w.y = pack4_fp8(v[4][i] * W8_SCALE, v[5][i] * W8_SCALE, v[6][i] * W8_SCALE, v[7][i] * W8_SCALE);
;         w.z = pack4_fp8(v[8][i] * W8_SCALE, v[9][i] * W8_SCALE, v[10][i] * W8_SCALE, v[11][i] * W8_SCALE); w.w = pack4_fp8(v[12][i] * W8_SCALE, v[13][i] * W8_SCALE, v[14][i] * W8_SCALE, v[15][i] * W8_SCALE);
;         *(LAS u32x4*)(tile + (4 * lane + i) * 128 + ((wv ^ (lane & 7)) << 4)) = w; }
; }
; __device__ __forceinline__ void cvt8_from_lds(const LAS unsigned char* tile, fp8_t* d, int ld_dst, int tid) {
;     const int c = tid & 7;
; #pragma unroll
;     for (int q = 0; q < 4; ++q) { const int r = (tid >> 3) + 64 * q; const u32x4 w = *(const LAS u32x4*)(tile + r * 128 + ((c ^ ((r >> 2) & 7)) << 4));
;         __builtin_nontemporal_store(w, (u32x4*)(d + (size_t)r * ld_dst + 16 * c)); }
; }
; __device__ __forceinline__ void cvt_item_lds(const float* src, int ld_src, fp8_t* dst, int ld_dst, LAS unsigned char* lds, int tid, int wv) {
;     const int lane = tid & 63;
;     const float* s = src + (size_t)(16 * wv) * ld_src + 4 * lane;
;     f32x4 va[16], vb[16];
;     cvt8_load(va, s, ld_src);
; #pragma unroll
;     for (int t = 0; t < 8; t += 2) {
;         cvt8_load(vb, s + (t + 1) * 256, ld_src); __builtin_amdgcn_sched_barrier(0);
;         cvt8_to_lds(va, lds, lane, wv); CVT_LDS_BAR(); __builtin_amdgcn_sched_barrier(0);
;         cvt8_from_lds(lds, dst + (size_t)(t * 256) * ld_dst, ld_dst, tid); __builtin_amdgcn_sched_barrier(0);
;         if (t + 2 < 8) { cvt8_load(va, s + (t + 2) * 256, ld_src); __builtin_amdgcn_sched_barrier(0); }
;         cvt8_to_lds(vb, lds + 32768, lane, wv); CVT_LDS_BAR(); __builtin_amdgcn_sched_barrier(0);
;         cvt8_from_lds(lds + 32768, dst + (size_t)((t + 1) * 256) * ld_dst, ld_dst, tid); __builtin_amdgcn_sched_barrier(0);
;     }
	v_mul_f32_e32 v16, 0x42800000, v16
	s_waitcnt vmcnt(23)
	v_mul_f32_e32 v20, 0x42800000, v20
	v_mov_b32_e32 v131, v133
	v_cvt_pk_fp8_f32 v131, v16, v20
	s_waitcnt vmcnt(22)
	v_mul_f32_e32 v0, 0x42800000, v0
	s_waitcnt vmcnt(20)
	v_mul_f32_e32 v4, 0x42800000, v4
	v_mov_b32_e32 v178, v133
	v_cvt_pk_fp8_f32 v131, v0, v4 op_sel:[0,0,1]
	v_mul_f32_e32 v0, 0x42800000, v125
	v_mul_f32_e32 v4, 0x42800000, v97
	v_cvt_pk_fp8_f32 v178, v0, v4
	v_mul_f32_e32 v0, 0x42800000, v81
	v_mul_f32_e32 v4, 0x42800000, v85
	v_mov_b32_e32 v179, v133
	v_cvt_pk_fp8_f32 v179, v0, v4
	v_mul_f32_e32 v0, 0x42800000, v65
	v_mul_f32_e32 v4, 0x42800000, v69
	v_mov_b32_e32 v180, v133
	v_cvt_pk_fp8_f32 v179, v0, v4 op_sel:[0,0,1]
	v_mul_f32_e32 v0, 0x42800000, v33
	v_mul_f32_e32 v4, 0x42800000, v37
	v_cvt_pk_fp8_f32 v180, v0, v4
	v_mul_f32_e32 v0, 0x42800000, v17
	v_mul_f32_e32 v4, 0x42800000, v21
	v_mov_b32_e32 v181, v133
	v_cvt_pk_fp8_f32 v181, v0, v4
	v_mul_f32_e32 v0, 0x42800000, v1
	v_mul_f32_e32 v1, 0x42800000, v5
	v_mov_b32_e32 v182, v133
	v_cvt_pk_fp8_f32 v181, v0, v1 op_sel:[0,0,1]
	v_mul_f32_e32 v0, 0x42800000, v126
	v_mul_f32_e32 v1, 0x42800000, v98
	v_cvt_pk_fp8_f32 v182, v0, v1
	v_mul_f32_e32 v0, 0x42800000, v82
	v_mul_f32_e32 v1, 0x42800000, v86
	v_mov_b32_e32 v183, v133
	v_cvt_pk_fp8_f32 v183, v0, v1
	v_mul_f32_e32 v0, 0x42800000, v66
	v_mul_f32_e32 v1, 0x42800000, v70
	v_mov_b32_e32 v184, v133
	v_cvt_pk_fp8_f32 v183, v0, v1 op_sel:[0,0,1]
	v_mul_f32_e32 v0, 0x42800000, v34
	v_mul_f32_e32 v1, 0x42800000, v38
	v_cvt_pk_fp8_f32 v184, v0, v1
	v_mul_f32_e32 v0, 0x42800000, v18
	v_mul_f32_e32 v1, 0x42800000, v22
	v_mov_b32_e32 v185, v133
	v_cvt_pk_fp8_f32 v185, v0, v1
	v_mul_f32_e32 v16, 0x42800000, v101
	v_mul_f32_e32 v20, 0x42800000, v105
	v_cvt_pk_fp8_f32 v178, v16, v20 op_sel:[0,0,1]
	v_mul_f32_e32 v16, 0x42800000, v41
	v_mul_f32_e32 v20, 0x42800000, v45
	v_mul_f32_e32 v0, 0x42800000, v2
	v_mul_f32_e32 v1, 0x42800000, v6
	v_cvt_pk_fp8_f32 v180, v16, v20 op_sel:[0,0,1]
	v_cvt_pk_fp8_f32 v185, v0, v1 op_sel:[0,0,1]
	v_mul_f32_e32 v0, 0x42800000, v127
	v_mul_f32_e32 v1, 0x42800000, v99
	v_mov_b32_e32 v16, v133
	v_cvt_pk_fp8_f32 v16, v0, v1
	v_mul_f32_e32 v0, 0x42800000, v83
	v_mul_f32_e32 v1, 0x42800000, v87
	v_mov_b32_e32 v17, v133
	v_cvt_pk_fp8_f32 v17, v0, v1
	v_mul_f32_e32 v124, 0x42800000, v124
	v_mul_f32_e32 v96, 0x42800000, v96
	v_mov_b32_e32 v128, v133
	v_mul_f32_e32 v80, 0x42800000, v80
	v_mul_f32_e32 v84, 0x42800000, v84
	v_mov_b32_e32 v129, v133
	v_mul_f32_e32 v32, 0x42800000, v32
	v_mul_f32_e32 v36, 0x42800000, v36
	v_mov_b32_e32 v130, v133
	v_cvt_pk_fp8_f32 v128, v124, v96
	v_cvt_pk_fp8_f32 v129, v80, v84
	v_cvt_pk_fp8_f32 v130, v32, v36
	v_mul_f32_e32 v0, 0x42800000, v67
	v_mul_f32_e32 v1, 0x42800000, v71
	v_cvt_pk_fp8_f32 v17, v0, v1 op_sel:[0,0,1]
	v_mul_f32_e32 v0, 0x42800000, v35
	v_mul_f32_e32 v1, 0x42800000, v39
	v_mov_b32_e32 v18, v133
	v_cvt_pk_fp8_f32 v18, v0, v1
	v_mul_f32_e32 v0, 0x42800000, v19
	v_mul_f32_e32 v1, 0x42800000, v23
	v_mov_b32_e32 v19, v133
	v_mul_f32_e32 v100, 0x42800000, v100
	v_mul_f32_e32 v104, 0x42800000, v104
	v_mul_f32_e32 v64, 0x42800000, v64
	v_mul_f32_e32 v68, 0x42800000, v68
	v_mul_f32_e32 v40, 0x42800000, v40
	v_mul_f32_e32 v44, 0x42800000, v44
	v_mul_f32_e32 v4, 0x42800000, v102
	v_mul_f32_e32 v5, 0x42800000, v106
	v_cvt_pk_fp8_f32 v19, v0, v1
	v_cvt_pk_fp8_f32 v128, v100, v104 op_sel:[0,0,1]
	v_cvt_pk_fp8_f32 v129, v64, v68 op_sel:[0,0,1]
	v_cvt_pk_fp8_f32 v130, v40, v44 op_sel:[0,0,1]
	v_cvt_pk_fp8_f32 v182, v4, v5 op_sel:[0,0,1]
	v_mul_f32_e32 v4, 0x42800000, v42
	v_mul_f32_e32 v5, 0x42800000, v46
	v_cvt_pk_fp8_f32 v184, v4, v5 op_sel:[0,0,1]
	v_mul_f32_e32 v2, 0x42800000, v103
	v_mul_f32_e32 v4, 0x42800000, v107
	v_cvt_pk_fp8_f32 v16, v2, v4 op_sel:[0,0,1]
	v_mul_f32_e32 v2, 0x42800000, v43
	v_mul_f32_e32 v4, 0x42800000, v47
	v_mul_f32_e32 v0, 0x42800000, v3
	v_mul_f32_e32 v1, 0x42800000, v7
	v_cvt_pk_fp8_f32 v18, v2, v4 op_sel:[0,0,1]
	v_cvt_pk_fp8_f32 v19, v0, v1 op_sel:[0,0,1]
	ds_write_b128 v209, v[128:131] offset:32768
	ds_write_b128 v209, v[178:181] offset:32896
	ds_write_b128 v209, v[182:185] offset:33024
	ds_write_b128 v209, v[16:19] offset:33152
	s_waitcnt lgkmcnt(0)
	s_barrier
	ds_read_b128 v[0:3], v210 offset:32768
	v_lshl_add_u64 v[20:21], v[144:145], 0, s[38:39]
	ds_read_b128 v[4:7], v211 offset:32768
	ds_read_b128 v[16:19], v212 offset:32768
	v_lshl_add_u64 v[22:23], v[20:21], 0, v[136:137]
	s_waitcnt lgkmcnt(2)
	global_store_dwordx4 v[22:23], v[0:3], off nt
	ds_read_b128 v[0:3], v213 offset:32768
	v_lshl_add_u64 v[22:23], v[20:21], 0, v[138:139]
	s_waitcnt lgkmcnt(2)
	global_store_dwordx4 v[22:23], v[4:7], off nt
	s_nop 1
	v_lshl_add_u64 v[4:5], v[20:21], 0, v[140:141]
	s_waitcnt lgkmcnt(1)
	global_store_dwordx4 v[4:5], v[16:19], off nt
	v_lshl_add_u64 v[4:5], v[20:21], 0, v[142:143]
	s_waitcnt lgkmcnt(0)
	global_store_dwordx4 v[4:5], v[0:3], off nt
	global_load_dwordx4 v[96:99], v[176:177], off offset:1024 nt
	global_load_dwordx4 v[100:103], v[146:147], off offset:1024 nt
	global_load_dwordx4 v[104:107], v[148:149], off offset:1024 nt
	global_load_dwordx4 v[124:127], v[150:151], off offset:1024 nt
	global_load_dwordx4 v[80:83], v[152:153], off offset:1024 nt
	global_load_dwordx4 v[84:87], v[154:155], off offset:1024 nt
	global_load_dwordx4 v[64:67], v[156:157], off offset:1024 nt
	global_load_dwordx4 v[68:71], v[158:159], off offset:1024 nt
	global_load_dwordx4 v[32:35], v[160:161], off offset:1024 nt
	global_load_dwordx4 v[36:39], v[162:163], off offset:1024 nt
	global_load_dwordx4 v[40:43], v[164:165], off offset:1024 nt
	global_load_dwordx4 v[44:47], v[166:167], off offset:1024 nt
	global_load_dwordx4 v[16:19], v[168:169], off offset:1024 nt
	global_load_dwordx4 v[20:23], v[170:171], off offset:1024 nt
	global_load_dwordx4 v[0:3], v[172:173], off offset:1024 nt
	global_load_dwordx4 v[4:7], v[174:175], off offset:1024 nt
	s_waitcnt vmcnt(23)
; #define LAS __attribute__((address_space(3)))
; __device__ __forceinline__ unsigned pack4_fp8(float a, float b, float c, float d) { int r = 0; r = __builtin_amdgcn_cvt_pk_fp8_f32(a, b, r, false); r = __builtin_amdgcn_cvt_pk_fp8_f32(c, d, r, true); return (unsigned)r; }
; __device__ __forceinline__ void cvt8_to_lds(const f32x4 (&v)[16], LAS unsigned char* tile, int lane, int wv) {
; #pragma unroll
;     for (int i = 0; i < 4; ++i) { u32x4 w; w.x = pack4_fp8(v[0][i] * W8_SCALE, v[1][i] * W8_SCALE, v[2][i] * W8_SCALE, v[3][i] * W8_SCALE); w.y = pack4_fp8(v[4][i] * W8_SCALE, v[5][i] * W8_SCALE, v[6][i] * W8_SCALE, v[7][i] * W8_SCALE);
;         w.z = pack4_fp8(v[8][i] * W8_SCALE, v[9][i] * W8_SCALE, v[10][i] * W8_SCALE, v[11][i] * W8_SCALE); w.w = pack4_fp8(v[12][i] * W8_SCALE, v[13][i] * W8_SCALE, v[14][i] * W8_SCALE, v[15][i] * W8_SCALE);
;         *(LAS u32x4*)(tile + (4 * lane + i) * 128 + ((wv ^ (lane & 7)) << 4)) = w; }
; }
; __device__ __forceinline__ void cvt8_from_lds(const LAS unsigned char* tile, fp8_t* d, int ld_dst, int tid) {
;     const int c = tid & 7;
; #pragma unroll
;     for (int q = 0; q < 4; ++q) { const int r = (tid >> 3) + 64 * q; const u32x4 w = *(const LAS u32x4*)(tile + r * 128 + ((c ^ ((r >> 2) & 7)) << 4));
;         __builtin_nontemporal_store(w, (u32x4*)(d + (size_t)r * ld_dst + 16 * c)); }
; }
; __device__ __forceinline__ void cvt_item_lds(const float* src, int ld_src, fp8_t* dst, int ld_dst, LAS unsigned char* lds, int tid, int wv) {
;     const int lane = tid & 63;
;     const float* s = src + (size_t)(16 * wv) * ld_src + 4 * lane;
;     f32x4 va[16], vb[16];
;     cvt8_load(va, s, ld_src);
; #pragma unroll
;     for (int t = 0; t < 8; t += 2) {
;         cvt8_load(vb, s + (t + 1) * 256, ld_src); __builtin_amdgcn_sched_barrier(0);
;         cvt8_to_lds(va, lds, lane, wv); CVT_LDS_BAR(); __builtin_amdgcn_sched_barrier(0);
;         cvt8_from_lds(lds, dst + (size_t)(t * 256) * ld_dst, ld_dst, tid); __builtin_amdgcn_sched_barrier(0);
;         if (t + 2 < 8) { cvt8_load(va, s + (t + 2) * 256, ld_src); __builtin_amdgcn_sched_barrier(0); }
;         cvt8_to_lds(vb, lds + 32768, lane, wv); CVT_LDS_BAR(); __builtin_amdgcn_sched_barrier(0);
;         cvt8_from_lds(lds + 32768, dst + (size_t)((t + 1) * 256) * ld_dst, ld_dst, tid); __builtin_amdgcn_sched_barrier(0);
;     }
	v_mul_f32_e32 v24, 0x42800000, v24
	s_waitcnt vmcnt(22)
	v_mul_f32_e32 v28, 0x42800000, v28
	v_mov_b32_e32 v131, v133
	v_cvt_pk_fp8_f32 v131, v24, v28
	s_waitcnt vmcnt(21)
	v_mul_f32_e32 v8, 0x42800000, v8
	s_waitcnt vmcnt(20)
	v_mul_f32_e32 v12, 0x42800000, v12
	v_mov_b32_e32 v178, v133
	v_cvt_pk_fp8_f32 v131, v8, v12 op_sel:[0,0,1]
	v_mul_f32_e32 v8, 0x42800000, v109
	v_mul_f32_e32 v12, 0x42800000, v113
	v_cvt_pk_fp8_f32 v178, v8, v12
	v_mul_f32_e32 v8, 0x42800000, v89
	v_mul_f32_e32 v12, 0x42800000, v93
	v_mov_b32_e32 v179, v133
	v_cvt_pk_fp8_f32 v179, v8, v12
	v_mul_f32_e32 v8, 0x42800000, v73
	v_mul_f32_e32 v12, 0x42800000, v77
	v_mov_b32_e32 v180, v133
	v_cvt_pk_fp8_f32 v179, v8, v12 op_sel:[0,0,1]
	v_mul_f32_e32 v8, 0x42800000, v49
	v_mul_f32_e32 v12, 0x42800000, v53
	v_cvt_pk_fp8_f32 v180, v8, v12
	v_mul_f32_e32 v8, 0x42800000, v25
	v_mul_f32_e32 v12, 0x42800000, v29
	v_mov_b32_e32 v181, v133
	v_cvt_pk_fp8_f32 v181, v8, v12
	v_mul_f32_e32 v8, 0x42800000, v9
	v_mul_f32_e32 v9, 0x42800000, v13
	v_mov_b32_e32 v182, v133
	v_cvt_pk_fp8_f32 v181, v8, v9 op_sel:[0,0,1]
	v_mul_f32_e32 v8, 0x42800000, v110
	v_mul_f32_e32 v9, 0x42800000, v114
	v_cvt_pk_fp8_f32 v182, v8, v9
	v_mul_f32_e32 v8, 0x42800000, v90
	v_mul_f32_e32 v9, 0x42800000, v94
	v_mov_b32_e32 v183, v133
	v_cvt_pk_fp8_f32 v183, v8, v9
	v_mul_f32_e32 v8, 0x42800000, v74
	v_mul_f32_e32 v9, 0x42800000, v78
	v_mov_b32_e32 v184, v133
	v_cvt_pk_fp8_f32 v183, v8, v9 op_sel:[0,0,1]
	v_mul_f32_e32 v8, 0x42800000, v50
	v_mul_f32_e32 v9, 0x42800000, v54
	v_cvt_pk_fp8_f32 v184, v8, v9
	v_mul_f32_e32 v8, 0x42800000, v26
	v_mul_f32_e32 v9, 0x42800000, v30
	v_mov_b32_e32 v185, v133
	v_cvt_pk_fp8_f32 v185, v8, v9
	v_mul_f32_e32 v24, 0x42800000, v117
	v_mul_f32_e32 v28, 0x42800000, v121
	v_cvt_pk_fp8_f32 v178, v24, v28 op_sel:[0,0,1]
	v_mul_f32_e32 v24, 0x42800000, v57
	v_mul_f32_e32 v28, 0x42800000, v61
	v_mul_f32_e32 v8, 0x42800000, v10
	v_mul_f32_e32 v9, 0x42800000, v14
	v_cvt_pk_fp8_f32 v180, v24, v28 op_sel:[0,0,1]
	v_cvt_pk_fp8_f32 v185, v8, v9 op_sel:[0,0,1]
	v_mul_f32_e32 v8, 0x42800000, v111
	v_mul_f32_e32 v9, 0x42800000, v115
	v_mov_b32_e32 v24, v133
	v_cvt_pk_fp8_f32 v24, v8, v9
	v_mul_f32_e32 v8, 0x42800000, v91
	v_mul_f32_e32 v9, 0x42800000, v95
	v_mov_b32_e32 v25, v133
	v_cvt_pk_fp8_f32 v25, v8, v9
	v_mul_f32_e32 v108, 0x42800000, v108
	v_mul_f32_e32 v112, 0x42800000, v112
	v_mov_b32_e32 v128, v133
	v_mul_f32_e32 v88, 0x42800000, v88
	v_mul_f32_e32 v92, 0x42800000, v92
	v_mov_b32_e32 v129, v133
	v_mul_f32_e32 v48, 0x42800000, v48
	v_mul_f32_e32 v52, 0x42800000, v52
	v_mov_b32_e32 v130, v133
	v_cvt_pk_fp8_f32 v128, v108, v112
	v_cvt_pk_fp8_f32 v129, v88, v92
	v_cvt_pk_fp8_f32 v130, v48, v52
	v_mul_f32_e32 v8, 0x42800000, v75
	v_mul_f32_e32 v9, 0x42800000, v79
	v_cvt_pk_fp8_f32 v25, v8, v9 op_sel:[0,0,1]
	v_mul_f32_e32 v8, 0x42800000, v51
	v_mul_f32_e32 v9, 0x42800000, v55
	v_mov_b32_e32 v26, v133
	v_cvt_pk_fp8_f32 v26, v8, v9
	v_mul_f32_e32 v8, 0x42800000, v27
	v_mul_f32_e32 v9, 0x42800000, v31
	v_mov_b32_e32 v27, v133
	v_mul_f32_e32 v116, 0x42800000, v116
	v_mul_f32_e32 v120, 0x42800000, v120
	v_mul_f32_e32 v72, 0x42800000, v72
	v_mul_f32_e32 v76, 0x42800000, v76
	v_mul_f32_e32 v56, 0x42800000, v56
	v_mul_f32_e32 v60, 0x42800000, v60
	v_mul_f32_e32 v12, 0x42800000, v118
	v_mul_f32_e32 v13, 0x42800000, v122
	v_cvt_pk_fp8_f32 v27, v8, v9
	v_cvt_pk_fp8_f32 v128, v116, v120 op_sel:[0,0,1]
	v_cvt_pk_fp8_f32 v129, v72, v76 op_sel:[0,0,1]
	v_cvt_pk_fp8_f32 v130, v56, v60 op_sel:[0,0,1]
	v_cvt_pk_fp8_f32 v182, v12, v13 op_sel:[0,0,1]
	v_mul_f32_e32 v12, 0x42800000, v58
	v_mul_f32_e32 v13, 0x42800000, v62
	v_cvt_pk_fp8_f32 v184, v12, v13 op_sel:[0,0,1]
	v_mul_f32_e32 v10, 0x42800000, v119
	v_mul_f32_e32 v12, 0x42800000, v123
	v_cvt_pk_fp8_f32 v24, v10, v12 op_sel:[0,0,1]
	v_mul_f32_e32 v10, 0x42800000, v59
	v_mul_f32_e32 v12, 0x42800000, v63
	v_mul_f32_e32 v8, 0x42800000, v11
	v_mul_f32_e32 v9, 0x42800000, v15
	v_cvt_pk_fp8_f32 v26, v10, v12 op_sel:[0,0,1]
	v_cvt_pk_fp8_f32 v27, v8, v9 op_sel:[0,0,1]
	ds_write_b128 v209, v[128:131]
	ds_write_b128 v209, v[178:181] offset:128
	ds_write_b128 v209, v[182:185] offset:256
	ds_write_b128 v209, v[24:27] offset:384
	s_waitcnt lgkmcnt(0)
	s_barrier
	ds_read_b128 v[8:11], v210
	v_lshl_add_u64 v[28:29], v[144:145], 0, s[40:41]
	ds_read_b128 v[12:15], v211
	ds_read_b128 v[24:27], v212
	v_lshl_add_u64 v[30:31], v[28:29], 0, v[136:137]
	s_waitcnt lgkmcnt(2)
	global_store_dwordx4 v[30:31], v[8:11], off nt
	ds_read_b128 v[8:11], v213
	v_lshl_add_u64 v[30:31], v[28:29], 0, v[138:139]
	s_waitcnt lgkmcnt(2)
	global_store_dwordx4 v[30:31], v[12:15], off nt
	s_nop 1
	v_lshl_add_u64 v[12:13], v[28:29], 0, v[140:141]
	s_waitcnt lgkmcnt(1)
	global_store_dwordx4 v[12:13], v[24:27], off nt
	v_lshl_add_u64 v[12:13], v[28:29], 0, v[142:143]
	s_waitcnt lgkmcnt(0)
	global_store_dwordx4 v[12:13], v[8:11], off nt
	global_load_dwordx4 v[108:111], v[176:177], off offset:2048 nt
	global_load_dwordx4 v[112:115], v[146:147], off offset:2048 nt
	global_load_dwordx4 v[116:119], v[148:149], off offset:2048 nt
	global_load_dwordx4 v[120:123], v[150:151], off offset:2048 nt
	global_load_dwordx4 v[88:91], v[152:153], off offset:2048 nt
	global_load_dwordx4 v[92:95], v[154:155], off offset:2048 nt
	global_load_dwordx4 v[72:75], v[156:157], off offset:2048 nt
	global_load_dwordx4 v[76:79], v[158:159], off offset:2048 nt
	global_load_dwordx4 v[48:51], v[160:161], off offset:2048 nt
	global_load_dwordx4 v[52:55], v[162:163], off offset:2048 nt
	global_load_dwordx4 v[56:59], v[164:165], off offset:2048 nt
	global_load_dwordx4 v[60:63], v[166:167], off offset:2048 nt
	global_load_dwordx4 v[24:27], v[168:169], off offset:2048 nt
	global_load_dwordx4 v[28:31], v[170:171], off offset:2048 nt
	global_load_dwordx4 v[8:11], v[172:173], off offset:2048 nt
	global_load_dwordx4 v[12:15], v[174:175], off offset:2048 nt
	s_waitcnt vmcnt(23)
; #define LAS __attribute__((address_space(3)))
; __device__ __forceinline__ unsigned pack4_fp8(float a, float b, float c, float d) { int r = 0; r = __builtin_amdgcn_cvt_pk_fp8_f32(a, b, r, false); r = __builtin_amdgcn_cvt_pk_fp8_f32(c, d, r, true); return (unsigned)r; }
; __device__ __forceinline__ void cvt8_to_lds(const f32x4 (&v)[16], LAS unsigned char* tile, int lane, int wv) {
; #pragma unroll
;     for (int i = 0; i < 4; ++i) { u32x4 w; w.x = pack4_fp8(v[0][i] * W8_SCALE, v[1][i] * W8_SCALE, v[2][i] * W8_SCALE, v[3][i] * W8_SCALE); w.y = pack4_fp8(v[4][i] * W8_SCALE, v[5][i] * W8_SCALE, v[6][i] * W8_SCALE, v[7][i] * W8_SCALE);
;         w.z = pack4_fp8(v[8][i] * W8_SCALE, v[9][i] * W8_SCALE, v[10][i] * W8_SCALE, v[11][i] * W8_SCALE); w.w = pack4_fp8(v[12][i] * W8_SCALE, v[13][i] * W8_SCALE, v[14][i] * W8_SCALE, v[15][i] * W8_SCALE);
;         *(LAS u32x4*)(tile + (4 * lane + i) * 128 + ((wv ^ (lane & 7)) << 4)) = w; }
; }
; __device__ __forceinline__ void cvt8_from_lds(const LAS unsigned char* tile, fp8_t* d, int ld_dst, int tid) {
;     const int c = tid & 7;
; #pragma unroll
;     for (int q = 0; q < 4; ++q) { const int r = (tid >> 3) + 64 * q; const u32x4 w = *(const LAS u32x4*)(tile + r * 128 + ((c ^ ((r >> 2) & 7)) << 4));
;         __builtin_nontemporal_store(w, (u32x4*)(d + (size_t)r * ld_dst + 16 * c)); }
; }
; __device__ __forceinline__ void cvt_item_lds(const float* src, int ld_src, fp8_t* dst, int ld_dst, LAS unsigned char* lds, int tid, int wv) {
;     const int lane = tid & 63;
;     const float* s = src + (size_t)(16 * wv) * ld_src + 4 * lane;
;     f32x4 va[16], vb[16];
;     cvt8_load(va, s, ld_src);
; #pragma unroll
;     for (int t = 0; t < 8; t += 2) {
;         cvt8_load(vb, s + (t + 1) * 256, ld_src); __builtin_amdgcn_sched_barrier(0);
;         cvt8_to_lds(va, lds, lane, wv); CVT_LDS_BAR(); __builtin_amdgcn_sched_barrier(0);
;         cvt8_from_lds(lds, dst + (size_t)(t * 256) * ld_dst, ld_dst, tid); __builtin_amdgcn_sched_barrier(0);
;         if (t + 2 < 8) { cvt8_load(va, s + (t + 2) * 256, ld_src); __builtin_amdgcn_sched_barrier(0); }
;         cvt8_to_lds(vb, lds + 32768, lane, wv); CVT_LDS_BAR(); __builtin_amdgcn_sched_barrier(0);
;         cvt8_from_lds(lds + 32768, dst + (size_t)((t + 1) * 256) * ld_dst, ld_dst, tid); __builtin_amdgcn_sched_barrier(0);
;     }
	v_mul_f32_e32 v16, 0x42800000, v16
	s_waitcnt vmcnt(22)
	v_mul_f32_e32 v20, 0x42800000, v20
	v_mov_b32_e32 v131, v133
	v_cvt_pk_fp8_f32 v131, v16, v20
	s_waitcnt vmcnt(21)
	v_mul_f32_e32 v0, 0x42800000, v0
	s_waitcnt vmcnt(20)
	v_mul_f32_e32 v4, 0x42800000, v4
	v_mov_b32_e32 v178, v133
	v_cvt_pk_fp8_f32 v131, v0, v4 op_sel:[0,0,1]
	v_mul_f32_e32 v0, 0x42800000, v97
	v_mul_f32_e32 v4, 0x42800000, v101
	v_cvt_pk_fp8_f32 v178, v0, v4
	v_mul_f32_e32 v0, 0x42800000, v81
	v_mul_f32_e32 v4, 0x42800000, v85
	v_mov_b32_e32 v179, v133
	v_cvt_pk_fp8_f32 v179, v0, v4
	v_mul_f32_e32 v0, 0x42800000, v65
	v_mul_f32_e32 v4, 0x42800000, v69
	v_mov_b32_e32 v180, v133
	v_cvt_pk_fp8_f32 v179, v0, v4 op_sel:[0,0,1]
	v_mul_f32_e32 v0, 0x42800000, v33
	v_mul_f32_e32 v4, 0x42800000, v37
	v_cvt_pk_fp8_f32 v180, v0, v4
	v_mul_f32_e32 v0, 0x42800000, v17
	v_mul_f32_e32 v4, 0x42800000, v21
	v_mov_b32_e32 v181, v133
	v_cvt_pk_fp8_f32 v181, v0, v4
	v_mul_f32_e32 v0, 0x42800000, v1
	v_mul_f32_e32 v1, 0x42800000, v5
	v_mov_b32_e32 v182, v133
	v_cvt_pk_fp8_f32 v181, v0, v1 op_sel:[0,0,1]
	v_mul_f32_e32 v0, 0x42800000, v98
	v_mul_f32_e32 v1, 0x42800000, v102
	v_cvt_pk_fp8_f32 v182, v0, v1
	v_mul_f32_e32 v0, 0x42800000, v82
	v_mul_f32_e32 v1, 0x42800000, v86
	v_mov_b32_e32 v183, v133
	v_cvt_pk_fp8_f32 v183, v0, v1
	v_mul_f32_e32 v0, 0x42800000, v66
	v_mul_f32_e32 v1, 0x42800000, v70
	v_mov_b32_e32 v184, v133
	v_cvt_pk_fp8_f32 v183, v0, v1 op_sel:[0,0,1]
	v_mul_f32_e32 v0, 0x42800000, v34
	v_mul_f32_e32 v1, 0x42800000, v38
	v_cvt_pk_fp8_f32 v184, v0, v1
	v_mul_f32_e32 v0, 0x42800000, v18
	v_mul_f32_e32 v1, 0x42800000, v22
	v_mov_b32_e32 v185, v133
	v_cvt_pk_fp8_f32 v185, v0, v1
	v_mul_f32_e32 v16, 0x42800000, v105
	v_mul_f32_e32 v20, 0x42800000, v125
	v_cvt_pk_fp8_f32 v178, v16, v20 op_sel:[0,0,1]
	v_mul_f32_e32 v16, 0x42800000, v41
	v_mul_f32_e32 v20, 0x42800000, v45
	v_mul_f32_e32 v0, 0x42800000, v2
	v_mul_f32_e32 v1, 0x42800000, v6
	v_cvt_pk_fp8_f32 v180, v16, v20 op_sel:[0,0,1]
	v_cvt_pk_fp8_f32 v185, v0, v1 op_sel:[0,0,1]
	v_mul_f32_e32 v0, 0x42800000, v99
	v_mul_f32_e32 v1, 0x42800000, v103
	v_mov_b32_e32 v16, v133
	v_cvt_pk_fp8_f32 v16, v0, v1
	v_mul_f32_e32 v0, 0x42800000, v83
	v_mul_f32_e32 v1, 0x42800000, v87
	v_mov_b32_e32 v17, v133
	v_cvt_pk_fp8_f32 v17, v0, v1
	v_mul_f32_e32 v96, 0x42800000, v96
	v_mul_f32_e32 v100, 0x42800000, v100
	v_mov_b32_e32 v128, v133
	v_mul_f32_e32 v80, 0x42800000, v80
	v_mul_f32_e32 v84, 0x42800000, v84
	v_mov_b32_e32 v129, v133
	v_mul_f32_e32 v32, 0x42800000, v32
	v_mul_f32_e32 v36, 0x42800000, v36
	v_mov_b32_e32 v130, v133
	v_cvt_pk_fp8_f32 v128, v96, v100
	v_cvt_pk_fp8_f32 v129, v80, v84
	v_cvt_pk_fp8_f32 v130, v32, v36
	v_mul_f32_e32 v0, 0x42800000, v67
	v_mul_f32_e32 v1, 0x42800000, v71
	v_cvt_pk_fp8_f32 v17, v0, v1 op_sel:[0,0,1]
	v_mul_f32_e32 v0, 0x42800000, v35
	v_mul_f32_e32 v1, 0x42800000, v39
	v_mov_b32_e32 v18, v133
	v_cvt_pk_fp8_f32 v18, v0, v1
	v_mul_f32_e32 v0, 0x42800000, v19
	v_mul_f32_e32 v1, 0x42800000, v23
	v_mov_b32_e32 v19, v133
	v_mul_f32_e32 v104, 0x42800000, v104
	v_mul_f32_e32 v124, 0x42800000, v124
	v_mul_f32_e32 v64, 0x42800000, v64
	v_mul_f32_e32 v68, 0x42800000, v68
	v_mul_f32_e32 v40, 0x42800000, v40
	v_mul_f32_e32 v44, 0x42800000, v44
	v_mul_f32_e32 v4, 0x42800000, v106
	v_mul_f32_e32 v5, 0x42800000, v126
	v_cvt_pk_fp8_f32 v19, v0, v1
	v_cvt_pk_fp8_f32 v128, v104, v124 op_sel:[0,0,1]
	v_cvt_pk_fp8_f32 v129, v64, v68 op_sel:[0,0,1]
	v_cvt_pk_fp8_f32 v130, v40, v44 op_sel:[0,0,1]
	v_cvt_pk_fp8_f32 v182, v4, v5 op_sel:[0,0,1]
	v_mul_f32_e32 v4, 0x42800000, v42
	v_mul_f32_e32 v5, 0x42800000, v46
	v_cvt_pk_fp8_f32 v184, v4, v5 op_sel:[0,0,1]
	v_mul_f32_e32 v2, 0x42800000, v107
	v_mul_f32_e32 v4, 0x42800000, v127
	v_cvt_pk_fp8_f32 v16, v2, v4 op_sel:[0,0,1]
	v_mul_f32_e32 v2, 0x42800000, v43
	v_mul_f32_e32 v4, 0x42800000, v47
	v_mul_f32_e32 v0, 0x42800000, v3
	v_mul_f32_e32 v1, 0x42800000, v7
	v_cvt_pk_fp8_f32 v18, v2, v4 op_sel:[0,0,1]
	v_cvt_pk_fp8_f32 v19, v0, v1 op_sel:[0,0,1]
	ds_write_b128 v209, v[128:131] offset:32768
	ds_write_b128 v209, v[178:181] offset:32896
	ds_write_b128 v209, v[182:185] offset:33024
	ds_write_b128 v209, v[16:19] offset:33152
	s_waitcnt lgkmcnt(0)
	s_barrier
	ds_read_b128 v[0:3], v210 offset:32768
	v_lshl_add_u64 v[20:21], v[144:145], 0, s[42:43]
	ds_read_b128 v[4:7], v211 offset:32768
	ds_read_b128 v[16:19], v212 offset:32768
	v_lshl_add_u64 v[22:23], v[20:21], 0, v[136:137]
	s_waitcnt lgkmcnt(2)
	global_store_dwordx4 v[22:23], v[0:3], off nt
	ds_read_b128 v[0:3], v213 offset:32768
	v_lshl_add_u64 v[22:23], v[20:21], 0, v[138:139]
	s_waitcnt lgkmcnt(2)
	global_store_dwordx4 v[22:23], v[4:7], off nt
	s_nop 1
	v_lshl_add_u64 v[4:5], v[20:21], 0, v[140:141]
	s_waitcnt lgkmcnt(1)
	global_store_dwordx4 v[4:5], v[16:19], off nt
	v_lshl_add_u64 v[4:5], v[20:21], 0, v[142:143]
	s_waitcnt lgkmcnt(0)
	global_store_dwordx4 v[4:5], v[0:3], off nt
	global_load_dwordx4 v[96:99], v[176:177], off offset:3072 nt
	global_load_dwordx4 v[100:103], v[146:147], off offset:3072 nt
	global_load_dwordx4 v[104:107], v[148:149], off offset:3072 nt
	global_load_dwordx4 v[124:127], v[150:151], off offset:3072 nt
	global_load_dwordx4 v[80:83], v[152:153], off offset:3072 nt
	global_load_dwordx4 v[84:87], v[154:155], off offset:3072 nt
	global_load_dwordx4 v[64:67], v[156:157], off offset:3072 nt
	global_load_dwordx4 v[68:71], v[158:159], off offset:3072 nt
	global_load_dwordx4 v[32:35], v[160:161], off offset:3072 nt
	global_load_dwordx4 v[36:39], v[162:163], off offset:3072 nt
	global_load_dwordx4 v[40:43], v[164:165], off offset:3072 nt
	global_load_dwordx4 v[44:47], v[166:167], off offset:3072 nt
	global_load_dwordx4 v[16:19], v[168:169], off offset:3072 nt
	global_load_dwordx4 v[20:23], v[170:171], off offset:3072 nt
	global_load_dwordx4 v[0:3], v[172:173], off offset:3072 nt
	global_load_dwordx4 v[4:7], v[174:175], off offset:3072 nt
	s_waitcnt vmcnt(23)
; #define LAS __attribute__((address_space(3)))
; __device__ __forceinline__ unsigned pack4_fp8(float a, float b, float c, float d) { int r = 0; r = __builtin_amdgcn_cvt_pk_fp8_f32(a, b, r, false); r = __builtin_amdgcn_cvt_pk_fp8_f32(c, d, r, true); return (unsigned)r; }
; __device__ __forceinline__ void cvt8_to_lds(const f32x4 (&v)[16], LAS unsigned char* tile, int lane, int wv) {
; #pragma unroll
;     for (int i = 0; i < 4; ++i) { u32x4 w; w.x = pack4_fp8(v[0][i] * W8_SCALE, v[1][i] * W8_SCALE, v[2][i] * W8_SCALE, v[3][i] * W8_SCALE); w.y = pack4_fp8(v[4][i] * W8_SCALE, v[5][i] * W8_SCALE, v[6][i] * W8_SCALE, v[7][i] * W8_SCALE);
;         w.z = pack4_fp8(v[8][i] * W8_SCALE, v[9][i] * W8_SCALE, v[10][i] * W8_SCALE, v[11][i] * W8_SCALE); w.w = pack4_fp8(v[12][i] * W8_SCALE, v[13][i] * W8_SCALE, v[14][i] * W8_SCALE, v[15][i] * W8_SCALE);
;         *(LAS u32x4*)(tile + (4 * lane + i) * 128 + ((wv ^ (lane & 7)) << 4)) = w; }
; }
; __device__ __forceinline__ void cvt8_from_lds(const LAS unsigned char* tile, fp8_t* d, int ld_dst, int tid) {
;     const int c = tid & 7;
; #pragma unroll
;     for (int q = 0; q < 4; ++q) { const int r = (tid >> 3) + 64 * q; const u32x4 w = *(const LAS u32x4*)(tile + r * 128 + ((c ^ ((r >> 2) & 7)) << 4));
;         __builtin_nontemporal_store(w, (u32x4*)(d + (size_t)r * ld_dst + 16 * c)); }
; }
; __device__ __forceinline__ void cvt_item_lds(const float* src, int ld_src, fp8_t* dst, int ld_dst, LAS unsigned char* lds, int tid, int wv) {
;     const int lane = tid & 63;
;     const float* s = src + (size_t)(16 * wv) * ld_src + 4 * lane;
;     f32x4 va[16], vb[16];
;     cvt8_load(va, s, ld_src);
; #pragma unroll
;     for (int t = 0; t < 8; t += 2) {
;         cvt8_load(vb, s + (t + 1) * 256, ld_src); __builtin_amdgcn_sched_barrier(0);
;         cvt8_to_lds(va, lds, lane, wv); CVT_LDS_BAR(); __builtin_amdgcn_sched_barrier(0);
;         cvt8_from_lds(lds, dst + (size_t)(t * 256) * ld_dst, ld_dst, tid); __builtin_amdgcn_sched_barrier(0);
;         if (t + 2 < 8) { cvt8_load(va, s + (t + 2) * 256, ld_src); __builtin_amdgcn_sched_barrier(0); }
;         cvt8_to_lds(vb, lds + 32768, lane, wv); CVT_LDS_BAR(); __builtin_amdgcn_sched_barrier(0);
;         cvt8_from_lds(lds + 32768, dst + (size_t)((t + 1) * 256) * ld_dst, ld_dst, tid); __builtin_amdgcn_sched_barrier(0);
;     }
	v_mul_f32_e32 v24, 0x42800000, v24
	s_waitcnt vmcnt(22)
	v_mul_f32_e32 v28, 0x42800000, v28
	v_mov_b32_e32 v131, v133
	v_cvt_pk_fp8_f32 v131, v24, v28
	s_waitcnt vmcnt(21)
	v_mul_f32_e32 v8, 0x42800000, v8
	s_waitcnt vmcnt(20)
	v_mul_f32_e32 v12, 0x42800000, v12
	v_mov_b32_e32 v146, v133
	v_cvt_pk_fp8_f32 v131, v8, v12 op_sel:[0,0,1]
	v_mul_f32_e32 v8, 0x42800000, v109
	v_mul_f32_e32 v12, 0x42800000, v113
	v_cvt_pk_fp8_f32 v146, v8, v12
	v_mul_f32_e32 v8, 0x42800000, v89
	v_mul_f32_e32 v12, 0x42800000, v93
	v_mov_b32_e32 v147, v133
	v_cvt_pk_fp8_f32 v147, v8, v12
	v_mul_f32_e32 v8, 0x42800000, v73
	v_mul_f32_e32 v12, 0x42800000, v77
	v_mov_b32_e32 v148, v133
	v_cvt_pk_fp8_f32 v147, v8, v12 op_sel:[0,0,1]
	v_mul_f32_e32 v8, 0x42800000, v49
	v_mul_f32_e32 v12, 0x42800000, v53
	v_cvt_pk_fp8_f32 v148, v8, v12
	v_mul_f32_e32 v8, 0x42800000, v25
	v_mul_f32_e32 v12, 0x42800000, v29
	v_mov_b32_e32 v149, v133
	v_cvt_pk_fp8_f32 v149, v8, v12
	v_mul_f32_e32 v8, 0x42800000, v9
	v_mul_f32_e32 v9, 0x42800000, v13
	v_mov_b32_e32 v150, v133
	v_cvt_pk_fp8_f32 v149, v8, v9 op_sel:[0,0,1]
	v_mul_f32_e32 v8, 0x42800000, v110
	v_mul_f32_e32 v9, 0x42800000, v114
	v_cvt_pk_fp8_f32 v150, v8, v9
	v_mul_f32_e32 v8, 0x42800000, v90
	v_mul_f32_e32 v9, 0x42800000, v94
	v_mov_b32_e32 v151, v133
	v_cvt_pk_fp8_f32 v151, v8, v9
	v_mul_f32_e32 v8, 0x42800000, v74
	v_mul_f32_e32 v9, 0x42800000, v78
	v_mov_b32_e32 v152, v133
	v_cvt_pk_fp8_f32 v151, v8, v9 op_sel:[0,0,1]
	v_mul_f32_e32 v8, 0x42800000, v50
	v_mul_f32_e32 v9, 0x42800000, v54
	v_cvt_pk_fp8_f32 v152, v8, v9
	v_mul_f32_e32 v8, 0x42800000, v26
	v_mul_f32_e32 v9, 0x42800000, v30
	v_mov_b32_e32 v153, v133
	v_cvt_pk_fp8_f32 v153, v8, v9
	v_mul_f32_e32 v24, 0x42800000, v117
	v_mul_f32_e32 v28, 0x42800000, v121
	v_cvt_pk_fp8_f32 v146, v24, v28 op_sel:[0,0,1]
	v_mul_f32_e32 v24, 0x42800000, v57
	v_mul_f32_e32 v28, 0x42800000, v61
	v_mul_f32_e32 v8, 0x42800000, v10
	v_mul_f32_e32 v9, 0x42800000, v14
	v_cvt_pk_fp8_f32 v148, v24, v28 op_sel:[0,0,1]
	v_cvt_pk_fp8_f32 v153, v8, v9 op_sel:[0,0,1]
	v_mul_f32_e32 v8, 0x42800000, v111
	v_mul_f32_e32 v9, 0x42800000, v115
	v_mov_b32_e32 v24, v133
	v_cvt_pk_fp8_f32 v24, v8, v9
	v_mul_f32_e32 v8, 0x42800000, v91
	v_mul_f32_e32 v9, 0x42800000, v95
	v_mov_b32_e32 v25, v133
	v_cvt_pk_fp8_f32 v25, v8, v9
	v_mul_f32_e32 v108, 0x42800000, v108
	v_mul_f32_e32 v112, 0x42800000, v112
	v_mov_b32_e32 v128, v133
	v_mul_f32_e32 v88, 0x42800000, v88
	v_mul_f32_e32 v92, 0x42800000, v92
	v_mov_b32_e32 v129, v133
	v_mul_f32_e32 v48, 0x42800000, v48
	v_mul_f32_e32 v52, 0x42800000, v52
	v_mov_b32_e32 v130, v133
	v_cvt_pk_fp8_f32 v128, v108, v112
	v_cvt_pk_fp8_f32 v129, v88, v92
	v_cvt_pk_fp8_f32 v130, v48, v52
	v_mul_f32_e32 v8, 0x42800000, v75
	v_mul_f32_e32 v9, 0x42800000, v79
	v_cvt_pk_fp8_f32 v25, v8, v9 op_sel:[0,0,1]
	v_mul_f32_e32 v8, 0x42800000, v51
	v_mul_f32_e32 v9, 0x42800000, v55
	v_mov_b32_e32 v26, v133
	v_cvt_pk_fp8_f32 v26, v8, v9
	v_mul_f32_e32 v8, 0x42800000, v27
	v_mul_f32_e32 v9, 0x42800000, v31
	v_mov_b32_e32 v27, v133
	v_mul_f32_e32 v116, 0x42800000, v116
	v_mul_f32_e32 v120, 0x42800000, v120
	v_mul_f32_e32 v72, 0x42800000, v72
	v_mul_f32_e32 v76, 0x42800000, v76
	v_mul_f32_e32 v56, 0x42800000, v56
	v_mul_f32_e32 v60, 0x42800000, v60
	v_mul_f32_e32 v12, 0x42800000, v118
	v_mul_f32_e32 v13, 0x42800000, v122
	v_cvt_pk_fp8_f32 v27, v8, v9
	v_cvt_pk_fp8_f32 v128, v116, v120 op_sel:[0,0,1]
	v_cvt_pk_fp8_f32 v129, v72, v76 op_sel:[0,0,1]
	v_cvt_pk_fp8_f32 v130, v56, v60 op_sel:[0,0,1]
	v_cvt_pk_fp8_f32 v150, v12, v13 op_sel:[0,0,1]
	v_mul_f32_e32 v12, 0x42800000, v58
	v_mul_f32_e32 v13, 0x42800000, v62
	v_cvt_pk_fp8_f32 v152, v12, v13 op_sel:[0,0,1]
	v_mul_f32_e32 v10, 0x42800000, v119
	v_mul_f32_e32 v12, 0x42800000, v123
	v_cvt_pk_fp8_f32 v24, v10, v12 op_sel:[0,0,1]
	v_mul_f32_e32 v10, 0x42800000, v59
	v_mul_f32_e32 v12, 0x42800000, v63
	v_mul_f32_e32 v8, 0x42800000, v11
	v_mul_f32_e32 v9, 0x42800000, v15
	v_cvt_pk_fp8_f32 v26, v10, v12 op_sel:[0,0,1]
	v_cvt_pk_fp8_f32 v27, v8, v9 op_sel:[0,0,1]
	ds_write_b128 v209, v[128:131]
	ds_write_b128 v209, v[146:149] offset:128
	ds_write_b128 v209, v[150:153] offset:256
	ds_write_b128 v209, v[24:27] offset:384
	s_waitcnt lgkmcnt(0)
	s_barrier
; #define LAS __attribute__((address_space(3)))
; __device__ __forceinline__ unsigned pack4_fp8(float a, float b, float c, float d) { int r = 0; r = __builtin_amdgcn_cvt_pk_fp8_f32(a, b, r, false); r = __builtin_amdgcn_cvt_pk_fp8_f32(c, d, r, true); return (unsigned)r; }
; __device__ __forceinline__ void cvt8_to_lds(const f32x4 (&v)[16], LAS unsigned char* tile, int lane, int wv) {
; #pragma unroll
;     for (int i = 0; i < 4; ++i) { u32x4 w; w.x = pack4_fp8(v[0][i] * W8_SCALE, v[1][i] * W8_SCALE, v[2][i] * W8_SCALE, v[3][i] * W8_SCALE); w.y = pack4_fp8(v[4][i] * W8_SCALE, v[5][i] * W8_SCALE, v[6][i] * W8_SCALE, v[7][i] * W8_SCALE);
;         w.z = pack4_fp8(v[8][i] * W8_SCALE, v[9][i] * W8_SCALE, v[10][i] * W8_SCALE, v[11][i] * W8_SCALE); w.w = pack4_fp8(v[12][i] * W8_SCALE, v[13][i] * W8_SCALE, v[14][i] * W8_SCALE, v[15][i] * W8_SCALE);
;         *(LAS u32x4*)(tile + (4 * lane + i) * 128 + ((wv ^ (lane & 7)) << 4)) = w; }
; }
; __device__ __forceinline__ void cvt8_from_lds(const LAS unsigned char* tile, fp8_t* d, int ld_dst, int tid) {
;     const int c = tid & 7;
; #pragma unroll
;     for (int q = 0; q < 4; ++q) { const int r = (tid >> 3) + 64 * q; const u32x4 w = *(const LAS u32x4*)(tile + r * 128 + ((c ^ ((r >> 2) & 7)) << 4));
;         __builtin_nontemporal_store(w, (u32x4*)(d + (size_t)r * ld_dst + 16 * c)); }
; }
; __device__ __forceinline__ void cvt_item_lds(const float* src, int ld_src, fp8_t* dst, int ld_dst, LAS unsigned char* lds, int tid, int wv) {
;     const int lane = tid & 63;
;     const float* s = src + (size_t)(16 * wv) * ld_src + 4 * lane;
;     f32x4 va[16], vb[16];
;     cvt8_load(va, s, ld_src);
; #pragma unroll
;     for (int t = 0; t < 8; t += 2) {
;         cvt8_load(vb, s + (t + 1) * 256, ld_src); __builtin_amdgcn_sched_barrier(0);
;         cvt8_to_lds(va, lds, lane, wv); CVT_LDS_BAR(); __builtin_amdgcn_sched_barrier(0);
;         cvt8_from_lds(lds, dst + (size_t)(t * 256) * ld_dst, ld_dst, tid); __builtin_amdgcn_sched_barrier(0);
;         if (t + 2 < 8) { cvt8_load(va, s + (t + 2) * 256, ld_src); __builtin_amdgcn_sched_barrier(0); }
;         cvt8_to_lds(vb, lds + 32768, lane, wv); CVT_LDS_BAR(); __builtin_amdgcn_sched_barrier(0);
;         cvt8_from_lds(lds + 32768, dst + (size_t)((t + 1) * 256) * ld_dst, ld_dst, tid); __builtin_amdgcn_sched_barrier(0);
;     }
	ds_read_b128 v[8:11], v210
	v_lshl_add_u64 v[28:29], v[144:145], 0, s[44:45]
	ds_read_b128 v[12:15], v211
	ds_read_b128 v[24:27], v212
	v_lshl_add_u64 v[30:31], v[28:29], 0, v[136:137]
	s_waitcnt lgkmcnt(2)
	global_store_dwordx4 v[30:31], v[8:11], off nt
	ds_read_b128 v[8:11], v213
	v_lshl_add_u64 v[30:31], v[28:29], 0, v[138:139]
	s_waitcnt lgkmcnt(2)
	global_store_dwordx4 v[30:31], v[12:15], off nt
	s_nop 1
	v_lshl_add_u64 v[12:13], v[28:29], 0, v[140:141]
	s_waitcnt lgkmcnt(1)
	global_store_dwordx4 v[12:13], v[24:27], off nt
	v_lshl_add_u64 v[12:13], v[28:29], 0, v[142:143]
	s_waitcnt lgkmcnt(0)
	global_store_dwordx4 v[12:13], v[8:11], off nt
	s_waitcnt vmcnt(19)
	s_nop 0
	v_mul_f32_e32 v9, 0x42800000, v96
	s_waitcnt vmcnt(18)
	v_mul_f32_e32 v10, 0x42800000, v100
	v_mov_b32_e32 v8, v133
	v_cvt_pk_fp8_f32 v8, v9, v10
	s_waitcnt vmcnt(15)
	v_mul_f32_e32 v10, 0x42800000, v80
	s_waitcnt vmcnt(14)
	v_mul_f32_e32 v13, 0x42800000, v84
	v_mov_b32_e32 v9, v133
	v_cvt_pk_fp8_f32 v9, v10, v13
	v_mul_f32_e32 v11, 0x42800000, v104
	v_mul_f32_e32 v12, 0x42800000, v124
	v_cvt_pk_fp8_f32 v8, v11, v12 op_sel:[0,0,1]
	s_waitcnt vmcnt(13)
	v_mul_f32_e32 v10, 0x42800000, v64
	s_waitcnt vmcnt(12)
	v_mul_f32_e32 v11, 0x42800000, v68
	v_cvt_pk_fp8_f32 v9, v10, v11 op_sel:[0,0,1]
	s_waitcnt vmcnt(11)
	v_mul_f32_e32 v11, 0x42800000, v32
	s_waitcnt vmcnt(10)
	v_mul_f32_e32 v12, 0x42800000, v36
	v_mov_b32_e32 v10, v133
	v_cvt_pk_fp8_f32 v10, v11, v12
	s_waitcnt vmcnt(7)
	v_mul_f32_e32 v12, 0x42800000, v16
	s_waitcnt vmcnt(6)
	v_mul_f32_e32 v15, 0x42800000, v20
	v_mov_b32_e32 v11, v133
	v_cvt_pk_fp8_f32 v11, v12, v15
	s_waitcnt vmcnt(5)
	v_mul_f32_e32 v0, 0x42800000, v0
	s_waitcnt vmcnt(4)
	v_mul_f32_e32 v4, 0x42800000, v4
	v_mul_f32_e32 v13, 0x42800000, v40
	v_mul_f32_e32 v14, 0x42800000, v44
	v_cvt_pk_fp8_f32 v11, v0, v4 op_sel:[0,0,1]
	v_mul_f32_e32 v0, 0x42800000, v97
	v_mul_f32_e32 v4, 0x42800000, v101
	v_mov_b32_e32 v12, v133
	v_cvt_pk_fp8_f32 v10, v13, v14 op_sel:[0,0,1]
	v_cvt_pk_fp8_f32 v12, v0, v4
	v_mul_f32_e32 v0, 0x42800000, v81
	v_mul_f32_e32 v4, 0x42800000, v85
	v_mov_b32_e32 v13, v133
	v_cvt_pk_fp8_f32 v13, v0, v4
	v_mul_f32_e32 v14, 0x42800000, v105
	v_mul_f32_e32 v15, 0x42800000, v125
	v_mul_f32_e32 v0, 0x42800000, v65
	v_mul_f32_e32 v4, 0x42800000, v69
	v_cvt_pk_fp8_f32 v12, v14, v15 op_sel:[0,0,1]
	v_cvt_pk_fp8_f32 v13, v0, v4 op_sel:[0,0,1]
	v_mul_f32_e32 v0, 0x42800000, v33
	v_mul_f32_e32 v4, 0x42800000, v37
	v_mov_b32_e32 v14, v133
	v_cvt_pk_fp8_f32 v14, v0, v4
	v_mul_f32_e32 v0, 0x42800000, v17
	v_mul_f32_e32 v4, 0x42800000, v21
	v_mov_b32_e32 v15, v133
	v_cvt_pk_fp8_f32 v15, v0, v4
	v_mul_f32_e32 v0, 0x42800000, v1
	v_mul_f32_e32 v1, 0x42800000, v5
	v_mov_b32_e32 v24, v133
	v_cvt_pk_fp8_f32 v15, v0, v1 op_sel:[0,0,1]
	v_mul_f32_e32 v0, 0x42800000, v98
	v_mul_f32_e32 v1, 0x42800000, v102
	v_cvt_pk_fp8_f32 v24, v0, v1
	v_mul_f32_e32 v0, 0x42800000, v82
	v_mul_f32_e32 v1, 0x42800000, v86
	v_mov_b32_e32 v25, v133
	v_cvt_pk_fp8_f32 v25, v0, v1
	v_mul_f32_e32 v0, 0x42800000, v66
	v_mul_f32_e32 v1, 0x42800000, v70
	v_mov_b32_e32 v26, v133
	v_cvt_pk_fp8_f32 v25, v0, v1 op_sel:[0,0,1]
	v_mul_f32_e32 v0, 0x42800000, v34
	v_mul_f32_e32 v1, 0x42800000, v38
	v_cvt_pk_fp8_f32 v26, v0, v1
	v_mul_f32_e32 v0, 0x42800000, v18
	v_mul_f32_e32 v1, 0x42800000, v22
	v_mov_b32_e32 v27, v133
	v_cvt_pk_fp8_f32 v27, v0, v1
	v_mul_f32_e32 v16, 0x42800000, v41
	v_mul_f32_e32 v20, 0x42800000, v45
	v_mul_f32_e32 v0, 0x42800000, v2
	v_mul_f32_e32 v1, 0x42800000, v6
	v_cvt_pk_fp8_f32 v14, v16, v20 op_sel:[0,0,1]
	v_cvt_pk_fp8_f32 v27, v0, v1 op_sel:[0,0,1]
	v_mul_f32_e32 v0, 0x42800000, v99
	v_mul_f32_e32 v1, 0x42800000, v103
	v_mov_b32_e32 v16, v133
	v_cvt_pk_fp8_f32 v16, v0, v1
	v_mul_f32_e32 v0, 0x42800000, v83
	v_mul_f32_e32 v1, 0x42800000, v87
	v_mov_b32_e32 v17, v133
	v_cvt_pk_fp8_f32 v17, v0, v1
	v_mul_f32_e32 v0, 0x42800000, v67
	v_mul_f32_e32 v1, 0x42800000, v71
	v_mov_b32_e32 v18, v133
	v_cvt_pk_fp8_f32 v17, v0, v1 op_sel:[0,0,1]
	v_mul_f32_e32 v0, 0x42800000, v35
	v_mul_f32_e32 v1, 0x42800000, v39
	v_cvt_pk_fp8_f32 v18, v0, v1
	v_mul_f32_e32 v0, 0x42800000, v19
	v_mul_f32_e32 v1, 0x42800000, v23
	v_mov_b32_e32 v19, v133
	v_mul_f32_e32 v4, 0x42800000, v106
	v_mul_f32_e32 v5, 0x42800000, v126
	v_cvt_pk_fp8_f32 v19, v0, v1
	v_cvt_pk_fp8_f32 v24, v4, v5 op_sel:[0,0,1]
	v_mul_f32_e32 v4, 0x42800000, v42
	v_mul_f32_e32 v5, 0x42800000, v46
	v_cvt_pk_fp8_f32 v26, v4, v5 op_sel:[0,0,1]
	v_mul_f32_e32 v2, 0x42800000, v107
	v_mul_f32_e32 v4, 0x42800000, v127
	v_cvt_pk_fp8_f32 v16, v2, v4 op_sel:[0,0,1]
	v_mul_f32_e32 v2, 0x42800000, v43
	v_mul_f32_e32 v4, 0x42800000, v47
	v_mul_f32_e32 v0, 0x42800000, v3
	v_mul_f32_e32 v1, 0x42800000, v7
	v_cvt_pk_fp8_f32 v18, v2, v4 op_sel:[0,0,1]
	v_cvt_pk_fp8_f32 v19, v0, v1 op_sel:[0,0,1]
	ds_write_b128 v209, v[8:11] offset:32768
	ds_write_b128 v209, v[12:15] offset:32896
	ds_write_b128 v209, v[24:27] offset:33024
	ds_write_b128 v209, v[16:19] offset:33152
	s_waitcnt lgkmcnt(0)
	s_barrier
	ds_read_b128 v[0:3], v210 offset:32768
	v_lshl_add_u64 v[12:13], v[144:145], 0, s[46:47]
	ds_read_b128 v[4:7], v211 offset:32768
	ds_read_b128 v[8:11], v212 offset:32768
	v_lshl_add_u64 v[14:15], v[12:13], 0, v[136:137]
	s_waitcnt lgkmcnt(2)
	global_store_dwordx4 v[14:15], v[0:3], off nt
	ds_read_b128 v[0:3], v213 offset:32768
	v_lshl_add_u64 v[14:15], v[12:13], 0, v[138:139]
	s_waitcnt lgkmcnt(2)
	global_store_dwordx4 v[14:15], v[4:7], off nt
	s_nop 1
	v_lshl_add_u64 v[4:5], v[12:13], 0, v[140:141]
	s_waitcnt lgkmcnt(1)
	global_store_dwordx4 v[4:5], v[8:11], off nt
	v_lshl_add_u64 v[4:5], v[12:13], 0, v[142:143]
	s_waitcnt lgkmcnt(0)
	global_store_dwordx4 v[4:5], v[0:3], off nt
	s_mov_b64 s[48:49], 0

; #define LAS __attribute__((address_space(3)))
; __device__ __forceinline__ unsigned pack4_fp8(float a, float b, float c, float d) { int r = 0; r = __builtin_amdgcn_cvt_pk_fp8_f32(a, b, r, false); r = __builtin_amdgcn_cvt_pk_fp8_f32(c, d, r, true); return (unsigned)r; }
; __device__ __forceinline__ void cvt8_to_lds(const f32x4 (&v)[16], LAS unsigned char* tile, int lane, int wv) {
; #pragma unroll
;     for (int i = 0; i < 4; ++i) { u32x4 w; w.x = pack4_fp8(v[0][i] * W8_SCALE, v[1][i] * W8_SCALE, v[2][i] * W8_SCALE, v[3][i] * W8_SCALE); w.y = pack4_fp8(v[4][i] * W8_SCALE, v[5][i] * W8_SCALE, v[6][i] * W8_SCALE, v[7][i] * W8_SCALE);
;         w.z = pack4_fp8(v[8][i] * W8_SCALE, v[9][i] * W8_SCALE, v[10][i] * W8_SCALE, v[11][i] * W8_SCALE); w.w = pack4_fp8(v[12][i] * W8_SCALE, v[13][i] * W8_SCALE, v[14][i] * W8_SCALE, v[15][i] * W8_SCALE);
;         *(LAS u32x4*)(tile + (4 * lane + i) * 128 + ((wv ^ (lane & 7)) << 4)) = w; }
; }
; __device__ __forceinline__ void cvt8_from_lds(const LAS unsigned char* tile, fp8_t* d, int ld_dst, int tid) {
;     const int c = tid & 7;
; #pragma unroll
;     for (int q = 0; q < 4; ++q) { const int r = (tid >> 3) + 64 * q; const u32x4 w = *(const LAS u32x4*)(tile + r * 128 + ((c ^ ((r >> 2) & 7)) << 4));
;         __builtin_nontemporal_store(w, (u32x4*)(d + (size_t)r * ld_dst + 16 * c)); }
; __device__ __forceinline__ void conv_queue_tail(const Params& p, LAS unsigned char* lds, const int wave) {
;     const int tid = phase_tid(wave);
;     const int lane = tid & 63, wv = tid >> 6;
;     LAS int* slot = (LAS int*)(lds + LDS_MISC + 1024);
;     for (;;) {
;         __syncthreads();
;         if (tid == 0) *slot = (int)atomicAdd(&p.ctl[CW_CONV3], 1u);
;         __syncthreads();
;         const int it = *slot;
;         if (it >= N_DEFER * 8) break;
;         const int j = NE * 16 - N_DEFER + (it >> 3), sub = it & 7, e = j >> 4, kb = j & 15;
;         const float* src = p.w_down + (size_t)e * DFF * ND + (size_t)(kb * 128 + 16 * wave) * ND + sub * 256 + 4 * lane;
;         fp8_t* dst = p.wt_down + (size_t)e * ND * DFF + (size_t)(sub * 256) * DFF + kb * 128;
;         f32x4 cv[16]; cvt8_load(cv, src, ND); cvt8_to_lds(cv, lds, lane, wave); CVT_LDS_BAR(); cvt8_from_lds(lds, dst, DFF, tid);
.LBB0_1282:
	v_mbcnt_lo_u32_b32 v2, -1, 0
	v_mbcnt_hi_u32_b32 v2, -1, v2
	v_readlane_b32 s16, v254, 5
	v_add_u32_e32 v3, s91, v2
	v_cmp_eq_u32_e64 s[0:1], 0, v3
	v_ashrrev_i32_e32 v10, 3, v3
	v_lshrrev_b32_e32 v3, 5, v3
	v_and_b32_e32 v4, 63, v2
	v_xor_b32_e32 v3, v3, v2
	v_lshlrev_b32_e32 v0, 2, v4
	v_lshl_add_u32 v13, v4, 9, 0
	v_bitop3_b32 v4, v2, s87, 7 bitop3:0x6c
	v_lshlrev_b32_e32 v3, 4, v3
	v_ashrrev_i32_e32 v11, 31, v10
	v_lshlrev_b32_e32 v14, 4, v4
	v_and_b32_e32 v3, 0x70, v3
	v_lshlrev_b32_e32 v15, 7, v10
	v_lshlrev_b64 v[4:5], 11, v[10:11]
	v_add_u32_e32 v6, 64, v10
	v_add_u32_e32 v8, 0x80, v10
	v_add_u32_e32 v10, 0xc0, v10
	v_readlane_b32 s17, v254, 6
	s_add_u32 s8, s16, 0x20c0
	v_mov_b32_e32 v1, 0
	v_add_u32_e32 v17, 0, v3
	v_lshlrev_b32_e32 v2, 4, v2
	v_lshlrev_b32_e32 v16, 7, v6
	v_ashrrev_i32_e32 v7, 31, v6
	v_lshlrev_b32_e32 v18, 7, v8
	v_ashrrev_i32_e32 v9, 31, v8
	v_lshlrev_b32_e32 v19, 7, v10
	v_ashrrev_i32_e32 v11, 31, v10
	v_readlane_b32 s18, v254, 7
	v_readlane_b32 s19, v254, 8
	s_addc_u32 s9, s17, 0
	s_add_i32 s13, 0, 0x20400
	s_mov_b64 s[60:61], s[76:77]
	s_mov_b32 s7, 0
	v_and_b32_e32 v2, 0x70, v2
	v_mov_b32_e32 v3, v1
	v_lshlrev_b64 v[6:7], 11, v[6:7]
	v_lshlrev_b64 v[8:9], 11, v[8:9]
	v_lshlrev_b64 v[10:11], 11, v[10:11]
	v_mov_b32_e32 v12, s13
	s_movk_i32 s18, 0x1ff
	v_lshlrev_b32_e32 v0, 2, v0
	s_movk_i32 s19, 0x2000
	s_movk_i32 s33, 0x4000
	s_movk_i32 s34, 0x6000
	s_mov_b32 s35, 0x8000
	s_mov_b32 s36, 0xa000
	s_mov_b32 s37, 0xc000
	s_mov_b32 s38, 0xe000
	s_mov_b32 s39, 0x10000
	s_mov_b32 s40, 0x12000
	s_mov_b32 s41, 0x14000
	s_mov_b32 s42, 0x16000
	s_mov_b32 s43, 0x18000
	s_mov_b32 s44, 0x1a000
	s_mov_b32 s45, 0x1c000
	s_mov_b32 s46, 0x1e000
	v_add_u32_e32 v13, v13, v14
	v_add_u32_e32 v14, v17, v15
	v_add_u32_e32 v15, v17, v16
	v_add_u32_e32 v16, v17, v18
	v_add_u32_e32 v17, v17, v19
	s_mov_b64 s[62:63], s[78:79]
	s_mov_b64 s[64:65], s[80:81]
	s_mov_b64 s[66:67], s[82:83]
	v_readlane_b32 s20, v254, 9
	v_readlane_b32 s21, v254, 10
	v_readlane_b32 s22, v254, 11
	v_readlane_b32 s23, v254, 12
	v_readlane_b32 s24, v254, 13
	v_readlane_b32 s25, v254, 14
	v_readlane_b32 s26, v254, 15
	v_readlane_b32 s27, v254, 16
	v_readlane_b32 s28, v254, 17
	v_readlane_b32 s29, v254, 18
	v_readlane_b32 s30, v254, 19
	v_readlane_b32 s31, v254, 20
	s_branch .LBB0_1284

; #define CVT_LDS_BAR() do { asm volatile("s_waitcnt lgkmcnt(0)" ::: "memory"); __builtin_amdgcn_s_barrier(); asm volatile("" ::: "memory"); } while (0)
; __device__ __forceinline__ void cvt8_load(f32x4 (&v)[16], const float* s, int ld_src) {
; #pragma unroll
;     for (int j = 0; j < 16; ++j) v[j] = __builtin_nontemporal_load((const f32x4*)(s + (size_t)j * ld_src));
; }
; __device__ __forceinline__ void conv_queue_tail(const Params& p, LAS unsigned char* lds, const int wave) {
;     ...
;         __syncthreads();
;         if (tid == 0) *slot = (int)atomicAdd(&p.ctl[CW_CONV3], 1u);
;         __syncthreads();
;         const int it = *slot;
;         if (it >= N_DEFER * 8) break;
;         const int j = NE * 16 - N_DEFER + (it >> 3), sub = it & 7, e = j >> 4, kb = j & 15;
;         const float* src = p.w_down + (size_t)e * DFF * ND + (size_t)(kb * 128 + 16 * wave) * ND + sub * 256 + 4 * lane;
;         fp8_t* dst = p.wt_down + (size_t)e * ND * DFF + (size_t)(sub * 256) * DFF + kb * 128;
;         f32x4 cv[16]; cvt8_load(cv, src, ND); cvt8_to_lds(cv, lds, lane, wave); CVT_LDS_BAR(); cvt8_from_lds(lds, dst, DFF, tid);
.LBB0_1288:
	s_or_b64 exec, exec, s[10:11]
	s_waitcnt lgkmcnt(0)
	s_barrier
	ds_read_b32 v18, v12
	s_mov_b64 s[10:11], -1
	s_waitcnt lgkmcnt(0)
	v_cmp_lt_i32_e32 vcc, s18, v18
	v_readfirstlane_b32 s2, v18
	s_cbranch_vccnz .LBB0_1283
	s_ashr_i32 s6, s2, 3
	s_add_i32 s10, s6, 0x1c0
	s_ashr_i32 s14, s10, 4
	v_readlane_b32 s60, v254, 22
	s_ashr_i32 s15, s14, 31
	v_readlane_b32 s64, v254, 26
	v_readlane_b32 s65, v254, 27
	s_lshl_b64 s[10:11], s[14:15], 22
	s_lshl_b64 s[14:15], s[14:15], 24
	v_readlane_b32 s66, v254, 28
	v_readlane_b32 s67, v254, 29
	v_readlane_b32 s68, v254, 30
	v_readlane_b32 s69, v254, 31
	v_readlane_b32 s70, v254, 32
	v_readlane_b32 s71, v254, 33
	v_readlane_b32 s72, v254, 34
	v_readlane_b32 s73, v254, 35
	v_readlane_b32 s74, v254, 36
	v_readlane_b32 s75, v254, 37
	s_mov_b64 s[20:21], s[64:65]
	s_add_u32 s16, s20, s14
	s_addc_u32 s17, s21, s15
	s_lshl_b32 s6, s6, 7
	s_and_b32 s47, s6, 0x780
	s_add_i32 s6, s47, s12
	s_lshl_b64 s[14:15], s[6:7], 13
	s_add_u32 s6, s16, s14
	s_addc_u32 s15, s17, s15
	s_lshl_b32 s2, s2, 8
	s_and_b32 s2, s2, 0x700
	s_lshl_b32 s14, s2, 2
	s_add_u32 s14, s6, s14
	s_addc_u32 s15, s15, 0
	v_lshl_add_u64 v[78:79], s[14:15], 0, v[0:1]
	v_add_co_u32_e32 v22, vcc, s19, v78
	global_load_dwordx4 v[18:21], v0, s[14:15] nt
	s_nop 0
	v_addc_co_u32_e32 v23, vcc, 0, v79, vcc
	v_add_co_u32_e32 v26, vcc, s33, v78
	v_mov_b32_e32 v82, v1
	s_nop 0
	v_addc_co_u32_e32 v27, vcc, 0, v79, vcc
	v_add_co_u32_e32 v30, vcc, s34, v78
	global_load_dwordx4 v[22:25], v[22:23], off nt
	s_nop 0
	global_load_dwordx4 v[26:29], v[26:27], off nt
	v_addc_co_u32_e32 v31, vcc, 0, v79, vcc
	v_add_co_u32_e32 v34, vcc, s35, v78
	v_mov_b32_e32 v83, v1
	s_nop 0
	v_addc_co_u32_e32 v35, vcc, 0, v79, vcc
	v_add_co_u32_e32 v38, vcc, s36, v78
	global_load_dwordx4 v[30:33], v[30:31], off nt
	s_nop 0
	global_load_dwordx4 v[34:37], v[34:35], off nt
	v_addc_co_u32_e32 v39, vcc, 0, v79, vcc
	v_add_co_u32_e32 v42, vcc, s37, v78
	v_mov_b32_e32 v84, v1
	s_nop 0
	v_addc_co_u32_e32 v43, vcc, 0, v79, vcc
	v_add_co_u32_e32 v46, vcc, s38, v78
	global_load_dwordx4 v[38:41], v[38:39], off nt
	s_nop 0
	global_load_dwordx4 v[42:45], v[42:43], off nt
	v_addc_co_u32_e32 v47, vcc, 0, v79, vcc
	v_add_co_u32_e32 v50, vcc, s39, v78
	v_mov_b32_e32 v85, v1
	s_nop 0
	v_addc_co_u32_e32 v51, vcc, 0, v79, vcc
	v_add_co_u32_e32 v54, vcc, s40, v78
	global_load_dwordx4 v[46:49], v[46:47], off nt
	s_nop 0
	global_load_dwordx4 v[50:53], v[50:51], off nt
	v_addc_co_u32_e32 v55, vcc, 0, v79, vcc
	v_add_co_u32_e32 v58, vcc, s41, v78
	v_mov_b32_e32 v86, v1
	s_nop 0
	v_addc_co_u32_e32 v59, vcc, 0, v79, vcc
	v_add_co_u32_e32 v62, vcc, s42, v78
	global_load_dwordx4 v[54:57], v[54:55], off nt
	s_nop 0
	global_load_dwordx4 v[58:61], v[58:59], off nt
	v_addc_co_u32_e32 v63, vcc, 0, v79, vcc
	v_add_co_u32_e32 v66, vcc, s43, v78
	v_mov_b32_e32 v87, v1
	s_nop 0
	v_addc_co_u32_e32 v67, vcc, 0, v79, vcc
	v_add_co_u32_e32 v70, vcc, s44, v78
	global_load_dwordx4 v[62:65], v[62:63], off nt
	s_nop 0
	global_load_dwordx4 v[66:69], v[66:67], off nt
	v_addc_co_u32_e32 v71, vcc, 0, v79, vcc
	v_add_co_u32_e32 v74, vcc, s45, v78
	v_mov_b32_e32 v88, v1
	s_nop 0
	v_addc_co_u32_e32 v75, vcc, 0, v79, vcc
	global_load_dwordx4 v[70:73], v[70:71], off nt
	s_nop 0
	global_load_dwordx4 v[74:77], v[74:75], off nt
	v_add_co_u32_e32 v78, vcc, s46, v78
	v_mov_b32_e32 v89, v1
	s_nop 0
	v_addc_co_u32_e32 v79, vcc, 0, v79, vcc
	global_load_dwordx4 v[78:81], v[78:79], off nt
	v_mov_b32_e32 v90, v1
	v_mov_b32_e32 v91, v1
	v_mov_b32_e32 v92, v1
	v_mov_b32_e32 v93, v1
	s_add_u32 s6, s56, s10
	s_waitcnt vmcnt(15)
	v_mul_f32_e32 v18, 0x42800000, v18
	s_addc_u32 s10, s57, s11
	s_lshl_b32 s2, s2, 11
	s_add_u32 s2, s6, s2
	s_addc_u32 s6, s10, 0
	s_add_u32 s10, s2, s47
	s_addc_u32 s11, s6, 0
	v_readlane_b32 s61, v254, 23
	v_readlane_b32 s62, v254, 24
	s_waitcnt vmcnt(14)
	v_mul_f32_e32 v22, 0x42800000, v22
	v_cvt_pk_fp8_f32 v82, v18, v22
	s_waitcnt vmcnt(13)
	v_mul_f32_e32 v26, 0x42800000, v26
	v_readlane_b32 s63, v254, 25
	s_mov_b64 s[22:23], s[66:67]
	s_mov_b64 s[24:25], s[68:69]
	s_mov_b64 s[26:27], s[70:71]
	s_mov_b64 s[28:29], s[72:73]
	s_mov_b64 s[30:31], s[74:75]
	s_mov_b64 s[60:61], s[76:77]
	s_waitcnt vmcnt(12)
	v_mul_f32_e32 v30, 0x42800000, v30
	s_waitcnt vmcnt(11)
	v_mul_f32_e32 v18, 0x42800000, v34
	v_cvt_pk_fp8_f32 v82, v26, v30 op_sel:[0,0,1]
	s_mov_b64 s[62:63], s[78:79]
	s_mov_b64 s[64:65], s[80:81]
	s_mov_b64 s[66:67], s[82:83]
	s_waitcnt vmcnt(10)
; #define LAS __attribute__((address_space(3)))
; __device__ __forceinline__ unsigned pack4_fp8(float a, float b, float c, float d) { int r = 0; r = __builtin_amdgcn_cvt_pk_fp8_f32(a, b, r, false); r = __builtin_amdgcn_cvt_pk_fp8_f32(c, d, r, true); return (unsigned)r; }
; #define CVT_LDS_BAR() do { asm volatile("s_waitcnt lgkmcnt(0)" ::: "memory"); __builtin_amdgcn_s_barrier(); asm volatile("" ::: "memory"); } while (0)
; __device__ __forceinline__ void cvt8_to_lds(const f32x4 (&v)[16], LAS unsigned char* tile, int lane, int wv) {
; #pragma unroll
;     for (int i = 0; i < 4; ++i) { u32x4 w; w.x = pack4_fp8(v[0][i] * W8_SCALE, v[1][i] * W8_SCALE, v[2][i] * W8_SCALE, v[3][i] * W8_SCALE); w.y = pack4_fp8(v[4][i] * W8_SCALE, v[5][i] * W8_SCALE, v[6][i] * W8_SCALE, v[7][i] * W8_SCALE);
;         w.z = pack4_fp8(v[8][i] * W8_SCALE, v[9][i] * W8_SCALE, v[10][i] * W8_SCALE, v[11][i] * W8_SCALE); w.w = pack4_fp8(v[12][i] * W8_SCALE, v[13][i] * W8_SCALE, v[14][i] * W8_SCALE, v[15][i] * W8_SCALE);
;         *(LAS u32x4*)(tile + (4 * lane + i) * 128 + ((wv ^ (lane & 7)) << 4)) = w; }
; }
; __device__ __forceinline__ void cvt8_from_lds(const LAS unsigned char* tile, fp8_t* d, int ld_dst, int tid) {
;     const int c = tid & 7;
; #pragma unroll
;     for (int q = 0; q < 4; ++q) { const int r = (tid >> 3) + 64 * q; const u32x4 w = *(const LAS u32x4*)(tile + r * 128 + ((c ^ ((r >> 2) & 7)) << 4));
;         __builtin_nontemporal_store(w, (u32x4*)(d + (size_t)r * ld_dst + 16 * c)); }
; }
; __device__ __forceinline__ void conv_queue_tail(const Params& p, LAS unsigned char* lds, const int wave) {
;     ...
;         f32x4 cv[16]; cvt8_load(cv, src, ND); cvt8_to_lds(cv, lds, lane, wave); CVT_LDS_BAR(); cvt8_from_lds(lds, dst, DFF, tid);
	v_mul_f32_e32 v22, 0x42800000, v38
	v_cvt_pk_fp8_f32 v83, v18, v22
	s_waitcnt vmcnt(9)
	v_mul_f32_e32 v18, 0x42800000, v42
	s_waitcnt vmcnt(8)
	v_mul_f32_e32 v22, 0x42800000, v46
	v_cvt_pk_fp8_f32 v83, v18, v22 op_sel:[0,0,1]
	s_waitcnt vmcnt(7)
	v_mul_f32_e32 v18, 0x42800000, v50
	s_waitcnt vmcnt(6)
	v_mul_f32_e32 v22, 0x42800000, v54
	v_cvt_pk_fp8_f32 v84, v18, v22
	s_waitcnt vmcnt(5)
	v_mul_f32_e32 v26, 0x42800000, v58
	s_waitcnt vmcnt(4)
	v_mul_f32_e32 v30, 0x42800000, v62
	s_waitcnt vmcnt(3)
	v_mul_f32_e32 v18, 0x42800000, v66
	v_cvt_pk_fp8_f32 v84, v26, v30 op_sel:[0,0,1]
	s_waitcnt vmcnt(2)
	v_mul_f32_e32 v22, 0x42800000, v70
	v_cvt_pk_fp8_f32 v85, v18, v22
	s_waitcnt vmcnt(1)
	v_mul_f32_e32 v18, 0x42800000, v74
	s_waitcnt vmcnt(0)
	v_mul_f32_e32 v22, 0x42800000, v78
	v_cvt_pk_fp8_f32 v85, v18, v22 op_sel:[0,0,1]
	v_mul_f32_e32 v18, 0x42800000, v19
	v_mul_f32_e32 v19, 0x42800000, v23
	v_cvt_pk_fp8_f32 v86, v18, v19
	v_mul_f32_e32 v18, 0x42800000, v35
	v_mul_f32_e32 v19, 0x42800000, v39
	v_cvt_pk_fp8_f32 v87, v18, v19
	v_mul_f32_e32 v18, 0x42800000, v43
	v_mul_f32_e32 v19, 0x42800000, v47
	v_mul_f32_e32 v22, 0x42800000, v27
	v_cvt_pk_fp8_f32 v87, v18, v19 op_sel:[0,0,1]
	v_mul_f32_e32 v18, 0x42800000, v51
	v_mul_f32_e32 v19, 0x42800000, v55
	v_cvt_pk_fp8_f32 v88, v18, v19
	v_mul_f32_e32 v18, 0x42800000, v67
	v_mul_f32_e32 v19, 0x42800000, v71
	v_cvt_pk_fp8_f32 v89, v18, v19
	v_mul_f32_e32 v18, 0x42800000, v75
	v_mul_f32_e32 v19, 0x42800000, v79
	v_mul_f32_e32 v23, 0x42800000, v31
	v_cvt_pk_fp8_f32 v89, v18, v19 op_sel:[0,0,1]
	v_mul_f32_e32 v18, 0x42800000, v20
	v_mul_f32_e32 v19, 0x42800000, v24
	v_cvt_pk_fp8_f32 v90, v18, v19
	v_mul_f32_e32 v18, 0x42800000, v36
	v_mul_f32_e32 v19, 0x42800000, v40
	v_cvt_pk_fp8_f32 v91, v18, v19
	v_mul_f32_e32 v18, 0x42800000, v44
	v_mul_f32_e32 v19, 0x42800000, v48
	v_cvt_pk_fp8_f32 v86, v22, v23 op_sel:[0,0,1]
	v_cvt_pk_fp8_f32 v91, v18, v19 op_sel:[0,0,1]
	v_mul_f32_e32 v18, 0x42800000, v52
	v_mul_f32_e32 v19, 0x42800000, v56
	v_cvt_pk_fp8_f32 v92, v18, v19
	v_mul_f32_e32 v18, 0x42800000, v68
	v_mul_f32_e32 v19, 0x42800000, v72
	v_cvt_pk_fp8_f32 v93, v18, v19
	v_mul_f32_e32 v22, 0x42800000, v59
	v_mul_f32_e32 v23, 0x42800000, v63
	v_cvt_pk_fp8_f32 v88, v22, v23 op_sel:[0,0,1]
	v_mul_f32_e32 v20, 0x42800000, v28
	v_mul_f32_e32 v22, 0x42800000, v32
	v_cvt_pk_fp8_f32 v90, v20, v22 op_sel:[0,0,1]
	v_mul_f32_e32 v20, 0x42800000, v60
	v_mul_f32_e32 v22, 0x42800000, v64
	v_mul_f32_e32 v18, 0x42800000, v76
	v_mul_f32_e32 v19, 0x42800000, v80
	v_cvt_pk_fp8_f32 v92, v20, v22 op_sel:[0,0,1]
	v_cvt_pk_fp8_f32 v93, v18, v19 op_sel:[0,0,1]
	v_mul_f32_e32 v19, 0x42800000, v21
	v_mul_f32_e32 v20, 0x42800000, v25
	v_mov_b32_e32 v18, v1
	v_cvt_pk_fp8_f32 v18, v19, v20
	v_mul_f32_e32 v20, 0x42800000, v37
	v_mul_f32_e32 v23, 0x42800000, v41
	v_mov_b32_e32 v19, v1
	v_cvt_pk_fp8_f32 v19, v20, v23
	v_mul_f32_e32 v21, 0x42800000, v29
	v_mul_f32_e32 v22, 0x42800000, v33
	v_cvt_pk_fp8_f32 v18, v21, v22 op_sel:[0,0,1]
	v_mul_f32_e32 v20, 0x42800000, v45
	v_mul_f32_e32 v21, 0x42800000, v49
	v_cvt_pk_fp8_f32 v19, v20, v21 op_sel:[0,0,1]
	v_mul_f32_e32 v21, 0x42800000, v53
	v_mul_f32_e32 v22, 0x42800000, v57
	v_mov_b32_e32 v20, v1
	v_cvt_pk_fp8_f32 v20, v21, v22
	v_mul_f32_e32 v22, 0x42800000, v69
	v_mul_f32_e32 v25, 0x42800000, v73
	v_mov_b32_e32 v21, v1
	v_cvt_pk_fp8_f32 v21, v22, v25
	v_mul_f32_e32 v23, 0x42800000, v61
	v_mul_f32_e32 v24, 0x42800000, v65
	v_cvt_pk_fp8_f32 v20, v23, v24 op_sel:[0,0,1]
	v_mul_f32_e32 v22, 0x42800000, v77
	v_mul_f32_e32 v23, 0x42800000, v81
	v_cvt_pk_fp8_f32 v21, v22, v23 op_sel:[0,0,1]
	ds_write_b128 v13, v[82:85]
	ds_write_b128 v13, v[86:89] offset:128
	ds_write_b128 v13, v[90:93] offset:256
	ds_write_b128 v13, v[18:21] offset:384
	s_waitcnt lgkmcnt(0)
	s_barrier
	ds_read_b128 v[18:21], v14
	ds_read_b128 v[22:25], v15
	v_lshl_add_u64 v[30:31], s[10:11], 0, v[2:3]
	v_lshl_add_u64 v[26:27], v[30:31], 0, v[4:5]
	v_lshl_add_u64 v[32:33], v[30:31], 0, v[6:7]
	s_waitcnt lgkmcnt(1)
	global_store_dwordx4 v[26:27], v[18:21], off nt
	ds_read_b128 v[18:21], v16
	ds_read_b128 v[26:29], v17
	s_waitcnt lgkmcnt(2)
	global_store_dwordx4 v[32:33], v[22:25], off nt
	s_mov_b64 s[10:11], 0
	s_nop 0
	v_lshl_add_u64 v[22:23], v[30:31], 0, v[8:9]
	s_waitcnt lgkmcnt(1)
	global_store_dwordx4 v[22:23], v[18:21], off nt
	s_nop 1
	v_lshl_add_u64 v[18:19], v[30:31], 0, v[10:11]
	s_waitcnt lgkmcnt(0)
	global_store_dwordx4 v[18:19], v[26:29], off nt
	s_branch .LBB0_1283
